# GEMM K-loops: vmcnt/lgkmcnt waits merged into one s_waitcnt, redundant post-barrier lgkmcnt(0) dropped
# speedup vs baseline: 1.0018x; 1.0018x over previous
; #define PG8_STAGE(bufoff, gbase, voff) do { _Pragma("unroll") for (int _i = 0; _i < 2; ++_i) \
;         __builtin_amdgcn_global_load_lds((const unsigned*)((const char*)(gbase) + (voff)[_i]), (PG8_LAS unsigned*)(lds + (bufoff) + ldsw + _i * 8192), 16, 0, 0); } while (0)
; #define PG8_LDA(dst, b, h) do { if constexpr (DT != 1) { _Pragma("unroll") for (int m = 0; m < 4; ++m) _Pragma("unroll") for (int k = 0; k < 2; ++k) dst[m][k] = *(const PG8_LAS bf16x8*)(lds + PG8_SA(b, h) + aoff + m * 2048 + k * 1024); } \
;         else { _Pragma("unroll") for (int m = 0; m < 4; ++m) dst##8[m] = ld32(lds + PG8_SA(b, h) + aoff + m * 2048); } } while (0)
; #define PG8_LDB(dst, b, h) do { if constexpr (DT != 1) { _Pragma("unroll") for (int n = 0; n < 2; ++n) _Pragma("unroll") for (int k = 0; k < 2; ++k) dst[n][k] = *(const PG8_LAS bf16x8*)(lds + PG8_SB(b, h) + boff + n * 2048 + k * 1024); } \
;         else { _Pragma("unroll") for (int n = 0; n < 2; ++n) dst##8[n] = ld32(lds + PG8_SB(b, h) + boff + n * 2048); } } while (0)
; #define PG8_WAIT_V(n) asm volatile("s_waitcnt vmcnt(" #n ")" ::: "memory")
; #define PG8_WAIT_L(n) asm volatile("s_waitcnt lgkmcnt(" #n ")" ::: "memory")
; #define PG8_BAR __builtin_amdgcn_s_barrier()
; #define PG8_SCHED __builtin_amdgcn_sched_barrier(0)
;     ...
;             PG8_LDB(B0, 0, 0); PG8_LDB(B1, 0, 1); PG8_SCHED; PG8_LDA(At, 0, 0); PG8_STAGE(PG8_SA(1, 1), a1 + hstepA, voffA);
;             PG8_WAIT_V(8); PG8_WAIT_L(0); PG8_BAR; PG8_MMA(0, 0, At, B0); PG8_MMA(0, 1, At, B1); PG8_BAR; PG8_SCHED;
;             PG8_LDA(At, 0, 1); PG8_STAGE(PG8_SB(0, 0), b2, voffB); PG8_STAGE(PG8_SB(0, 1), b2 + hstepB, voffB); PG8_STAGE(PG8_SA(0, 0), a2, voffA);
;             PG8_WAIT_V(8); PG8_WAIT_L(0); PG8_BAR; PG8_MMA(1, 0, At, B0); PG8_MMA(1, 1, At, B1); PG8_BAR; PG8_SCHED;
.LBB0_227:
	v_add_u32_e32 v142, s35, v164
	v_add_u32_e32 v180, s36, v164
	ds_read_b128 v[130:133], v142
	ds_read_b128 v[134:137], v142 offset:1024
	ds_read_b128 v[138:141], v142 offset:2048
	ds_read_b128 v[142:145], v142 offset:3072
	ds_read_b128 v[168:171], v180
	ds_read_b128 v[172:175], v180 offset:1024
	ds_read_b128 v[176:179], v180 offset:2048
	ds_read_b128 v[180:183], v180 offset:3072
	s_add_i32 s68, s26, 2
	s_add_u32 s27, s24, 0xfffc0080
	s_addc_u32 s28, s25, -1
	s_cmp_eq_u32 s61, s26
	s_cselect_b32 s26, s65, s66
	s_cselect_b32 s29, s15, s28
	s_cselect_b32 s28, s17, s27
	s_cselect_b32 s27, s64, s67
	s_add_i32 m0, s46, 0xc000
	ds_read_b128 v[184:187], v167
	ds_read_b128 v[188:191], v167 offset:1024
	ds_read_b128 v[192:195], v167 offset:2048
	ds_read_b128 v[196:199], v167 offset:3072
	ds_read_b128 v[200:203], v167 offset:4096
	ds_read_b128 v[204:207], v167 offset:5120
	ds_read_b128 v[208:211], v167 offset:6144
	ds_read_b128 v[212:215], v167 offset:7168
	global_load_lds_dwordx4 v158, s[24:25]
	s_add_i32 m0, s46, 0xe000
	s_nop 0
	global_load_lds_dwordx4 v156, s[24:25]
	s_waitcnt vmcnt(8) lgkmcnt(0)
	s_barrier
	s_setprio 1
	v_mfma_i32_16x16x64_i8 v[126:129], v[130:133], v[184:187], v[126:129]
	v_mfma_i32_16x16x64_i8 v[118:121], v[138:141], v[184:187], v[118:121]
	v_mfma_i32_16x16x64_i8 v[110:113], v[130:133], v[192:195], v[110:113]
	v_mfma_i32_16x16x64_i8 v[102:105], v[138:141], v[192:195], v[102:105]
	v_mfma_i32_16x16x64_i8 v[94:97], v[130:133], v[200:203], v[94:97]
	v_mfma_i32_16x16x64_i8 v[86:89], v[138:141], v[200:203], v[86:89]
	v_mfma_i32_16x16x64_i8 v[78:81], v[130:133], v[208:211], v[78:81]
	v_mfma_i32_16x16x64_i8 v[70:73], v[138:141], v[208:211], v[70:73]
	v_mfma_i32_16x16x64_i8 v[126:129], v[134:137], v[188:191], v[126:129]
	v_mfma_i32_16x16x64_i8 v[118:121], v[142:145], v[188:191], v[118:121]
	v_mfma_i32_16x16x64_i8 v[110:113], v[134:137], v[196:199], v[110:113]
	v_mfma_i32_16x16x64_i8 v[102:105], v[142:145], v[196:199], v[102:105]
	v_mfma_i32_16x16x64_i8 v[94:97], v[134:137], v[204:207], v[94:97]
	v_mfma_i32_16x16x64_i8 v[86:89], v[142:145], v[204:207], v[86:89]
	v_mfma_i32_16x16x64_i8 v[78:81], v[134:137], v[212:215], v[78:81]
	v_mfma_i32_16x16x64_i8 v[70:73], v[142:145], v[212:215], v[70:73]
	s_setprio 0
	s_setprio 1
	v_mfma_i32_16x16x64_i8 v[122:125], v[168:171], v[184:187], v[122:125]
	v_mfma_i32_16x16x64_i8 v[114:117], v[176:179], v[184:187], v[114:117]
	v_mfma_i32_16x16x64_i8 v[106:109], v[168:171], v[192:195], v[106:109]
	v_mfma_i32_16x16x64_i8 v[98:101], v[176:179], v[192:195], v[98:101]
	v_mfma_i32_16x16x64_i8 v[90:93], v[168:171], v[200:203], v[90:93]
	v_mfma_i32_16x16x64_i8 v[82:85], v[176:179], v[200:203], v[82:85]
	v_mfma_i32_16x16x64_i8 v[74:77], v[168:171], v[208:211], v[74:77]
	v_mfma_i32_16x16x64_i8 v[66:69], v[176:179], v[208:211], v[66:69]
	v_mfma_i32_16x16x64_i8 v[122:125], v[172:175], v[188:191], v[122:125]
	v_mfma_i32_16x16x64_i8 v[114:117], v[180:183], v[188:191], v[114:117]
	v_mfma_i32_16x16x64_i8 v[106:109], v[172:175], v[196:199], v[106:109]
	v_mfma_i32_16x16x64_i8 v[98:101], v[180:183], v[196:199], v[98:101]
	v_mfma_i32_16x16x64_i8 v[90:93], v[172:175], v[204:207], v[90:93]
	v_mfma_i32_16x16x64_i8 v[82:85], v[180:183], v[204:207], v[82:85]
	v_mfma_i32_16x16x64_i8 v[74:77], v[172:175], v[212:215], v[74:77]
	v_mfma_i32_16x16x64_i8 v[66:69], v[180:183], v[212:215], v[66:69]
	s_setprio 0
	s_barrier
	s_mov_b32 m0, s23
	s_add_u32 s98, s26, 0x80
	s_addc_u32 s99, s27, 0
	s_add_u32 s70, s26, 0x40000
	ds_read_b128 v[184:187], v167 offset:16384
	ds_read_b128 v[188:191], v167 offset:17408
	ds_read_b128 v[192:195], v167 offset:18432
	ds_read_b128 v[196:199], v167 offset:19456
	ds_read_b128 v[200:203], v167 offset:20480
	ds_read_b128 v[204:207], v167 offset:21504
	ds_read_b128 v[208:211], v167 offset:22528
	ds_read_b128 v[212:215], v167 offset:23552
	global_load_lds_dwordx4 v148, s[26:27]
	s_mov_b32 m0, s43
	s_addc_u32 s71, s27, 0
	global_load_lds_dwordx4 v152, s[26:27]
	s_mov_b32 m0, s44
	s_nop 0
	global_load_lds_dwordx4 v148, s[70:71]
	s_mov_b32 m0, s45
	s_nop 0
	global_load_lds_dwordx4 v152, s[70:71]
	s_add_u32 s100, s28, 0x80
	s_addc_u32 s101, s29, 0
	s_mov_b32 m0, s46
	s_nop 0
	global_load_lds_dwordx4 v146, s[28:29]
	s_mov_b32 m0, s47
	s_nop 0
	global_load_lds_dwordx4 v150, s[28:29]
	s_waitcnt vmcnt(8) lgkmcnt(0)
	s_barrier
	s_setprio 1
	v_mfma_i32_16x16x64_i8 v[62:65], v[130:133], v[184:187], v[62:65]
	v_mfma_i32_16x16x64_i8 v[54:57], v[138:141], v[184:187], v[54:57]
	v_mfma_i32_16x16x64_i8 v[46:49], v[130:133], v[192:195], v[46:49]
	v_mfma_i32_16x16x64_i8 v[38:41], v[138:141], v[192:195], v[38:41]
	v_mfma_i32_16x16x64_i8 v[30:33], v[130:133], v[200:203], v[30:33]
	v_mfma_i32_16x16x64_i8 v[22:25], v[138:141], v[200:203], v[22:25]
	v_mfma_i32_16x16x64_i8 v[14:17], v[130:133], v[208:211], v[14:17]
	v_mfma_i32_16x16x64_i8 v[6:9], v[138:141], v[208:211], v[6:9]
	v_mfma_i32_16x16x64_i8 v[62:65], v[134:137], v[188:191], v[62:65]
	v_mfma_i32_16x16x64_i8 v[54:57], v[142:145], v[188:191], v[54:57]
	v_mfma_i32_16x16x64_i8 v[46:49], v[134:137], v[196:199], v[46:49]
	v_mfma_i32_16x16x64_i8 v[38:41], v[142:145], v[196:199], v[38:41]
	v_mfma_i32_16x16x64_i8 v[30:33], v[134:137], v[204:207], v[30:33]
	v_mfma_i32_16x16x64_i8 v[22:25], v[142:145], v[204:207], v[22:25]
	v_mfma_i32_16x16x64_i8 v[14:17], v[134:137], v[212:215], v[14:17]
	v_mfma_i32_16x16x64_i8 v[6:9], v[142:145], v[212:215], v[6:9]
	s_setprio 0
	s_setprio 1
	v_mfma_i32_16x16x64_i8 v[58:61], v[168:171], v[184:187], v[58:61]
	v_mfma_i32_16x16x64_i8 v[50:53], v[176:179], v[184:187], v[50:53]
	v_mfma_i32_16x16x64_i8 v[42:45], v[168:171], v[192:195], v[42:45]
	v_mfma_i32_16x16x64_i8 v[34:37], v[176:179], v[192:195], v[34:37]
	v_mfma_i32_16x16x64_i8 v[26:29], v[168:171], v[200:203], v[26:29]
	v_mfma_i32_16x16x64_i8 v[18:21], v[176:179], v[200:203], v[18:21]
	v_mfma_i32_16x16x64_i8 v[10:13], v[168:171], v[208:211], v[10:13]
	v_mfma_i32_16x16x64_i8 v[2:5], v[176:179], v[208:211], v[2:5]
	v_mfma_i32_16x16x64_i8 v[58:61], v[172:175], v[188:191], v[58:61]
	v_mfma_i32_16x16x64_i8 v[50:53], v[180:183], v[188:191], v[50:53]
	v_mfma_i32_16x16x64_i8 v[42:45], v[172:175], v[196:199], v[42:45]
	v_mfma_i32_16x16x64_i8 v[34:37], v[180:183], v[196:199], v[34:37]
	v_mfma_i32_16x16x64_i8 v[26:29], v[172:175], v[204:207], v[26:29]
	v_mfma_i32_16x16x64_i8 v[18:21], v[180:183], v[204:207], v[18:21]
	v_mfma_i32_16x16x64_i8 v[10:13], v[172:175], v[212:215], v[10:13]
	v_mfma_i32_16x16x64_i8 v[2:5], v[180:183], v[212:215], v[2:5]
	s_setprio 0
	s_barrier
; #define PG8_STAGE(bufoff, gbase, voff) do { _Pragma("unroll") for (int _i = 0; _i < 2; ++_i) \
;         __builtin_amdgcn_global_load_lds((const unsigned*)((const char*)(gbase) + (voff)[_i]), (PG8_LAS unsigned*)(lds + (bufoff) + ldsw + _i * 8192), 16, 0, 0); } while (0)
; #define PG8_LDA(dst, b, h) do { if constexpr (DT != 1) { _Pragma("unroll") for (int m = 0; m < 4; ++m) _Pragma("unroll") for (int k = 0; k < 2; ++k) dst[m][k] = *(const PG8_LAS bf16x8*)(lds + PG8_SA(b, h) + aoff + m * 2048 + k * 1024); } \
;         else { _Pragma("unroll") for (int m = 0; m < 4; ++m) dst##8[m] = ld32(lds + PG8_SA(b, h) + aoff + m * 2048); } } while (0)
; #define PG8_LDB(dst, b, h) do { if constexpr (DT != 1) { _Pragma("unroll") for (int n = 0; n < 2; ++n) _Pragma("unroll") for (int k = 0; k < 2; ++k) dst[n][k] = *(const PG8_LAS bf16x8*)(lds + PG8_SB(b, h) + boff + n * 2048 + k * 1024); } \
;         else { _Pragma("unroll") for (int n = 0; n < 2; ++n) dst##8[n] = ld32(lds + PG8_SB(b, h) + boff + n * 2048); } } while (0)
; #define PG8_WAIT_V(n) asm volatile("s_waitcnt vmcnt(" #n ")" ::: "memory")
; #define PG8_WAIT_L(n) asm volatile("s_waitcnt lgkmcnt(" #n ")" ::: "memory")
; #define PG8_BAR __builtin_amdgcn_s_barrier()
; #define PG8_SCHED __builtin_amdgcn_sched_barrier(0)
;     ...
;             PG8_LDB(B0, 1, 0); PG8_LDB(B1, 1, 1); PG8_SCHED; PG8_LDA(At, 1, 0); PG8_STAGE(PG8_SA(0, 1), a2 + hstepA, voffA);
;             PG8_WAIT_V(8); PG8_WAIT_L(0); PG8_BAR; PG8_MMA(0, 0, At, B0); PG8_MMA(0, 1, At, B1); PG8_BAR; PG8_SCHED;
;             PG8_LDA(At, 1, 1); PG8_STAGE(PG8_SB(1, 0), b3, voffB); PG8_STAGE(PG8_SB(1, 1), b3 + hstepB, voffB); PG8_STAGE(PG8_SA(1, 0), a3, voffA);
;             PG8_WAIT_V(8); PG8_WAIT_L(0); PG8_BAR; PG8_MMA(1, 0, At, B0); PG8_MMA(1, 1, At, B1); PG8_BAR; PG8_SCHED;
	v_add_u32_e32 v142, s51, v164
	v_add_u32_e32 v180, s52, v164
	ds_read_b128 v[130:133], v142
	ds_read_b128 v[134:137], v142 offset:1024
	ds_read_b128 v[138:141], v142 offset:2048
	ds_read_b128 v[142:145], v142 offset:3072
	ds_read_b128 v[168:171], v180
	ds_read_b128 v[172:175], v180 offset:1024
	ds_read_b128 v[176:179], v180 offset:2048
	ds_read_b128 v[180:183], v180 offset:3072
	s_add_u32 s28, s28, 0x40000
	s_addc_u32 s29, s29, 0
	s_mov_b32 m0, s48
	ds_read_b128 v[184:187], v167 offset:32768
	ds_read_b128 v[188:191], v167 offset:33792
	ds_read_b128 v[192:195], v167 offset:34816
	ds_read_b128 v[196:199], v167 offset:35840
	ds_read_b128 v[200:203], v167 offset:36864
	ds_read_b128 v[204:207], v167 offset:37888
	ds_read_b128 v[208:211], v167 offset:38912
	ds_read_b128 v[212:215], v167 offset:39936
	global_load_lds_dwordx4 v146, s[28:29]
	s_mov_b32 m0, s49
	s_nop 0
	global_load_lds_dwordx4 v150, s[28:29]
	s_waitcnt vmcnt(8) lgkmcnt(0)
	s_barrier
	s_setprio 1
	v_mfma_i32_16x16x64_i8 v[126:129], v[130:133], v[184:187], v[126:129]
	v_mfma_i32_16x16x64_i8 v[118:121], v[138:141], v[184:187], v[118:121]
	v_mfma_i32_16x16x64_i8 v[110:113], v[130:133], v[192:195], v[110:113]
	v_mfma_i32_16x16x64_i8 v[102:105], v[138:141], v[192:195], v[102:105]
	v_mfma_i32_16x16x64_i8 v[94:97], v[130:133], v[200:203], v[94:97]
	v_mfma_i32_16x16x64_i8 v[86:89], v[138:141], v[200:203], v[86:89]
	v_mfma_i32_16x16x64_i8 v[78:81], v[130:133], v[208:211], v[78:81]
	v_mfma_i32_16x16x64_i8 v[70:73], v[138:141], v[208:211], v[70:73]
	v_mfma_i32_16x16x64_i8 v[126:129], v[134:137], v[188:191], v[126:129]
	v_mfma_i32_16x16x64_i8 v[118:121], v[142:145], v[188:191], v[118:121]
	v_mfma_i32_16x16x64_i8 v[110:113], v[134:137], v[196:199], v[110:113]
	v_mfma_i32_16x16x64_i8 v[102:105], v[142:145], v[196:199], v[102:105]
	v_mfma_i32_16x16x64_i8 v[94:97], v[134:137], v[204:207], v[94:97]
	v_mfma_i32_16x16x64_i8 v[86:89], v[142:145], v[204:207], v[86:89]
	v_mfma_i32_16x16x64_i8 v[78:81], v[134:137], v[212:215], v[78:81]
	v_mfma_i32_16x16x64_i8 v[70:73], v[142:145], v[212:215], v[70:73]
	s_setprio 0
	s_setprio 1
	v_mfma_i32_16x16x64_i8 v[122:125], v[168:171], v[184:187], v[122:125]
	v_mfma_i32_16x16x64_i8 v[114:117], v[176:179], v[184:187], v[114:117]
	v_mfma_i32_16x16x64_i8 v[106:109], v[168:171], v[192:195], v[106:109]
	v_mfma_i32_16x16x64_i8 v[98:101], v[176:179], v[192:195], v[98:101]
	v_mfma_i32_16x16x64_i8 v[90:93], v[168:171], v[200:203], v[90:93]
	v_mfma_i32_16x16x64_i8 v[82:85], v[176:179], v[200:203], v[82:85]
	v_mfma_i32_16x16x64_i8 v[74:77], v[168:171], v[208:211], v[74:77]
	v_mfma_i32_16x16x64_i8 v[66:69], v[176:179], v[208:211], v[66:69]
	v_mfma_i32_16x16x64_i8 v[122:125], v[172:175], v[188:191], v[122:125]
	v_mfma_i32_16x16x64_i8 v[114:117], v[180:183], v[188:191], v[114:117]
	v_mfma_i32_16x16x64_i8 v[106:109], v[172:175], v[196:199], v[106:109]
	v_mfma_i32_16x16x64_i8 v[98:101], v[180:183], v[196:199], v[98:101]
	v_mfma_i32_16x16x64_i8 v[90:93], v[172:175], v[204:207], v[90:93]
	v_mfma_i32_16x16x64_i8 v[82:85], v[180:183], v[204:207], v[82:85]
	v_mfma_i32_16x16x64_i8 v[74:77], v[172:175], v[212:215], v[74:77]
	v_mfma_i32_16x16x64_i8 v[66:69], v[180:183], v[212:215], v[66:69]
	s_setprio 0
	s_barrier
	s_mov_b32 m0, s55
	s_add_u32 s26, s26, 0x40080
	ds_read_b128 v[184:187], v167 offset:49152
	ds_read_b128 v[188:191], v167 offset:50176
	ds_read_b128 v[192:195], v167 offset:51200
	ds_read_b128 v[196:199], v167 offset:52224
	ds_read_b128 v[200:203], v167 offset:53248
	ds_read_b128 v[204:207], v167 offset:54272
	ds_read_b128 v[208:211], v167 offset:55296
	ds_read_b128 v[212:215], v167 offset:56320
	global_load_lds_dwordx4 v148, s[98:99]
	s_mov_b32 m0, s56
	s_addc_u32 s27, s27, 0
	global_load_lds_dwordx4 v152, s[98:99]
	s_mov_b32 m0, s59
	s_nop 0
	global_load_lds_dwordx4 v148, s[26:27]
	s_mov_b32 m0, s60
	s_nop 0
	global_load_lds_dwordx4 v152, s[26:27]
	s_mov_b32 m0, s57
	s_nop 0
	global_load_lds_dwordx4 v146, s[100:101]
	s_mov_b32 m0, s58
	s_nop 0
	global_load_lds_dwordx4 v150, s[100:101]
	s_waitcnt vmcnt(8) lgkmcnt(0)
	s_barrier
	s_setprio 1
	v_mfma_i32_16x16x64_i8 v[62:65], v[130:133], v[184:187], v[62:65]
	v_mfma_i32_16x16x64_i8 v[54:57], v[138:141], v[184:187], v[54:57]
	v_mfma_i32_16x16x64_i8 v[46:49], v[130:133], v[192:195], v[46:49]
	v_mfma_i32_16x16x64_i8 v[38:41], v[138:141], v[192:195], v[38:41]
	v_mfma_i32_16x16x64_i8 v[30:33], v[130:133], v[200:203], v[30:33]
	v_mfma_i32_16x16x64_i8 v[22:25], v[138:141], v[200:203], v[22:25]
	v_mfma_i32_16x16x64_i8 v[14:17], v[130:133], v[208:211], v[14:17]
	v_mfma_i32_16x16x64_i8 v[6:9], v[138:141], v[208:211], v[6:9]
	v_mfma_i32_16x16x64_i8 v[62:65], v[134:137], v[188:191], v[62:65]
	v_mfma_i32_16x16x64_i8 v[54:57], v[142:145], v[188:191], v[54:57]
	v_mfma_i32_16x16x64_i8 v[46:49], v[134:137], v[196:199], v[46:49]
	v_mfma_i32_16x16x64_i8 v[38:41], v[142:145], v[196:199], v[38:41]
	v_mfma_i32_16x16x64_i8 v[30:33], v[134:137], v[204:207], v[30:33]
	v_mfma_i32_16x16x64_i8 v[22:25], v[142:145], v[204:207], v[22:25]
	v_mfma_i32_16x16x64_i8 v[14:17], v[134:137], v[212:215], v[14:17]
	v_mfma_i32_16x16x64_i8 v[6:9], v[142:145], v[212:215], v[6:9]
	s_setprio 0
	s_setprio 1
	v_mfma_i32_16x16x64_i8 v[58:61], v[168:171], v[184:187], v[58:61]
	v_mfma_i32_16x16x64_i8 v[50:53], v[176:179], v[184:187], v[50:53]
	v_mfma_i32_16x16x64_i8 v[42:45], v[168:171], v[192:195], v[42:45]
	v_mfma_i32_16x16x64_i8 v[34:37], v[176:179], v[192:195], v[34:37]
	v_mfma_i32_16x16x64_i8 v[26:29], v[168:171], v[200:203], v[26:29]
	v_mfma_i32_16x16x64_i8 v[18:21], v[176:179], v[200:203], v[18:21]
	v_mfma_i32_16x16x64_i8 v[10:13], v[168:171], v[208:211], v[10:13]
	v_mfma_i32_16x16x64_i8 v[2:5], v[176:179], v[208:211], v[2:5]
	v_mfma_i32_16x16x64_i8 v[58:61], v[172:175], v[188:191], v[58:61]
	v_mfma_i32_16x16x64_i8 v[50:53], v[180:183], v[188:191], v[50:53]
	v_mfma_i32_16x16x64_i8 v[42:45], v[172:175], v[196:199], v[42:45]
	v_mfma_i32_16x16x64_i8 v[34:37], v[180:183], v[196:199], v[34:37]
	v_mfma_i32_16x16x64_i8 v[26:29], v[172:175], v[204:207], v[26:29]
	v_mfma_i32_16x16x64_i8 v[18:21], v[180:183], v[204:207], v[18:21]
	v_mfma_i32_16x16x64_i8 v[10:13], v[172:175], v[212:215], v[10:13]
	v_mfma_i32_16x16x64_i8 v[2:5], v[180:183], v[212:215], v[2:5]
	s_setprio 0
	s_barrier
	s_add_u32 s66, s66, 0x100
	s_addc_u32 s67, s67, 0
	s_add_u32 s24, s24, 0x100
	s_addc_u32 s25, s25, 0
	s_cmp_ge_i32 s68, s54
	s_mov_b32 s26, s68
	s_cbranch_scc0 .LBB0_227

; #define PG8_STAGE(bufoff, gbase, voff) do { _Pragma("unroll") for (int _i = 0; _i < 2; ++_i) \
;         __builtin_amdgcn_global_load_lds((const unsigned*)((const char*)(gbase) + (voff)[_i]), (PG8_LAS unsigned*)(lds + (bufoff) + ldsw + _i * 8192), 16, 0, 0); } while (0)
; #define PG8_LDA(dst, b, h) do { if constexpr (DT != 1) { _Pragma("unroll") for (int m = 0; m < 4; ++m) _Pragma("unroll") for (int k = 0; k < 2; ++k) dst[m][k] = *(const PG8_LAS bf16x8*)(lds + PG8_SA(b, h) + aoff + m * 2048 + k * 1024); } \
;         else { _Pragma("unroll") for (int m = 0; m < 4; ++m) dst##8[m] = ld32(lds + PG8_SA(b, h) + aoff + m * 2048); } } while (0)
; #define PG8_LDB(dst, b, h) do { if constexpr (DT != 1) { _Pragma("unroll") for (int n = 0; n < 2; ++n) _Pragma("unroll") for (int k = 0; k < 2; ++k) dst[n][k] = *(const PG8_LAS bf16x8*)(lds + PG8_SB(b, h) + boff + n * 2048 + k * 1024); } \
;         else { _Pragma("unroll") for (int n = 0; n < 2; ++n) dst##8[n] = ld32(lds + PG8_SB(b, h) + boff + n * 2048); } } while (0)
; #define PG8_WAIT_V(n) asm volatile("s_waitcnt vmcnt(" #n ")" ::: "memory")
; #define PG8_WAIT_L(n) asm volatile("s_waitcnt lgkmcnt(" #n ")" ::: "memory")
; #define PG8_BAR __builtin_amdgcn_s_barrier()
; #define PG8_SCHED __builtin_amdgcn_sched_barrier(0)
;     ...
;             PG8_LDB(B0, 0, 0); PG8_LDB(B1, 0, 1); PG8_SCHED; PG8_LDA(At, 0, 0); PG8_STAGE(PG8_SA(1, 1), a1 + hstepA, voffA);
;             PG8_WAIT_V(8); PG8_WAIT_L(0); PG8_BAR; PG8_MMA(0, 0, At, B0); PG8_MMA(0, 1, At, B1); PG8_BAR; PG8_SCHED;
;             PG8_LDA(At, 0, 1); PG8_STAGE(PG8_SB(0, 0), b2, voffB); PG8_STAGE(PG8_SB(0, 1), b2 + hstepB, voffB); PG8_STAGE(PG8_SA(0, 0), a2, voffA);
;             PG8_WAIT_V(8); PG8_WAIT_L(0); PG8_BAR; PG8_MMA(1, 0, At, B0); PG8_MMA(1, 1, At, B1); PG8_BAR; PG8_SCHED;
.LBB0_303:
	ds_read_b128 v[146:149], v159
	ds_read_b128 v[150:153], v159 offset:1024
	ds_read_b128 v[154:157], v159 offset:2048
	ds_read_b128 v[164:167], v159 offset:3072
	ds_read_b128 v[168:171], v160
	ds_read_b128 v[172:175], v160 offset:1024
	ds_read_b128 v[176:179], v160 offset:2048
	ds_read_b128 v[180:183], v160 offset:3072
	s_add_i32 s69, s34, 2
	s_add_u32 s30, s28, 0x100
	s_addc_u32 s31, s29, 0
	s_cmp_eq_u32 s60, s34
	s_cselect_b32 s34, s26, s67
	s_cselect_b32 s37, s3, s31
	s_cselect_b32 s36, s2, s30
	s_cselect_b32 s35, s27, s68
	v_lshl_add_u64 v[216:217], s[28:29], 0, v[140:141]
	s_add_i32 m0, s48, 0xc000
	ds_read_b128 v[184:187], v161
	ds_read_b128 v[188:191], v161 offset:1024
	ds_read_b128 v[192:195], v161 offset:2048
	ds_read_b128 v[196:199], v161 offset:3072
	ds_read_b128 v[200:203], v161 offset:4096
	ds_read_b128 v[204:207], v161 offset:5120
	ds_read_b128 v[208:211], v161 offset:6144
	ds_read_b128 v[212:215], v161 offset:7168
	global_load_lds_dwordx4 v[216:217], off
	v_lshl_add_u64 v[216:217], s[28:29], 0, v[138:139]
	s_add_i32 m0, s48, 0xe000
	s_nop 0
	global_load_lds_dwordx4 v[216:217], off
	s_waitcnt vmcnt(8) lgkmcnt(0)
	s_barrier
	s_setprio 1
	v_mfma_f32_16x16x32_bf16 v[126:129], v[146:149], v[184:187], v[126:129]
	v_mfma_f32_16x16x32_bf16 v[122:125], v[154:157], v[184:187], v[122:125]
	v_mfma_f32_16x16x32_bf16 v[118:121], v[146:149], v[192:195], v[118:121]
	v_mfma_f32_16x16x32_bf16 v[114:117], v[154:157], v[192:195], v[114:117]
	v_mfma_f32_16x16x32_bf16 v[106:109], v[146:149], v[200:203], v[106:109]
	v_mfma_f32_16x16x32_bf16 v[98:101], v[154:157], v[200:203], v[98:101]
	v_mfma_f32_16x16x32_bf16 v[90:93], v[146:149], v[208:211], v[90:93]
	v_mfma_f32_16x16x32_bf16 v[82:85], v[154:157], v[208:211], v[82:85]
	v_mfma_f32_16x16x32_bf16 v[126:129], v[150:153], v[188:191], v[126:129]
	v_mfma_f32_16x16x32_bf16 v[122:125], v[164:167], v[188:191], v[122:125]
	v_mfma_f32_16x16x32_bf16 v[118:121], v[150:153], v[196:199], v[118:121]
	v_mfma_f32_16x16x32_bf16 v[114:117], v[164:167], v[196:199], v[114:117]
	v_mfma_f32_16x16x32_bf16 v[106:109], v[150:153], v[204:207], v[106:109]
	v_mfma_f32_16x16x32_bf16 v[98:101], v[164:167], v[204:207], v[98:101]
	v_mfma_f32_16x16x32_bf16 v[90:93], v[150:153], v[212:215], v[90:93]
	v_mfma_f32_16x16x32_bf16 v[82:85], v[164:167], v[212:215], v[82:85]
	s_setprio 0
	s_setprio 1
	v_mfma_f32_16x16x32_bf16 v[110:113], v[168:171], v[184:187], v[110:113]
	v_mfma_f32_16x16x32_bf16 v[102:105], v[176:179], v[184:187], v[102:105]
	v_mfma_f32_16x16x32_bf16 v[94:97], v[168:171], v[192:195], v[94:97]
	v_mfma_f32_16x16x32_bf16 v[86:89], v[176:179], v[192:195], v[86:89]
	v_mfma_f32_16x16x32_bf16 v[78:81], v[168:171], v[200:203], v[78:81]
	v_mfma_f32_16x16x32_bf16 v[74:77], v[176:179], v[200:203], v[74:77]
	v_mfma_f32_16x16x32_bf16 v[70:73], v[168:171], v[208:211], v[70:73]
	v_mfma_f32_16x16x32_bf16 v[66:69], v[176:179], v[208:211], v[66:69]
	v_mfma_f32_16x16x32_bf16 v[110:113], v[172:175], v[188:191], v[110:113]
	v_mfma_f32_16x16x32_bf16 v[102:105], v[180:183], v[188:191], v[102:105]
	v_mfma_f32_16x16x32_bf16 v[94:97], v[172:175], v[196:199], v[94:97]
	v_mfma_f32_16x16x32_bf16 v[86:89], v[180:183], v[196:199], v[86:89]
	v_mfma_f32_16x16x32_bf16 v[78:81], v[172:175], v[204:207], v[78:81]
	v_mfma_f32_16x16x32_bf16 v[74:77], v[180:183], v[204:207], v[74:77]
	v_mfma_f32_16x16x32_bf16 v[70:73], v[172:175], v[212:215], v[70:73]
	v_mfma_f32_16x16x32_bf16 v[66:69], v[180:183], v[212:215], v[66:69]
	s_setprio 0
	s_barrier
	s_mov_b32 m0, s44
	s_add_u32 s98, s34, 0x80
	s_addc_u32 s99, s35, 0
	s_add_u32 s28, s34, 0x160000
	ds_read_b128 v[184:187], v161 offset:16384
	ds_read_b128 v[188:191], v161 offset:17408
	ds_read_b128 v[192:195], v161 offset:18432
	ds_read_b128 v[196:199], v161 offset:19456
	ds_read_b128 v[200:203], v161 offset:20480
	ds_read_b128 v[204:207], v161 offset:21504
	ds_read_b128 v[208:211], v161 offset:22528
	ds_read_b128 v[212:215], v161 offset:23552
	global_load_lds_dwordx4 v132, s[34:35]
	s_mov_b32 m0, s45
	s_addc_u32 s29, s35, 0
	global_load_lds_dwordx4 v136, s[34:35]
	s_mov_b32 m0, s46
	s_nop 0
	global_load_lds_dwordx4 v132, s[28:29]
	s_mov_b32 m0, s47
	s_nop 0
	global_load_lds_dwordx4 v136, s[28:29]
	s_add_u32 s100, s36, 0x80
	s_addc_u32 s101, s37, 0
	s_mov_b32 m0, s48
	s_nop 0
	global_load_lds_dwordx4 v130, s[36:37]
	s_mov_b32 m0, s49
	s_nop 0
	global_load_lds_dwordx4 v134, s[36:37]
	s_waitcnt vmcnt(8) lgkmcnt(0)
	s_barrier
	s_setprio 1
	v_mfma_f32_16x16x32_bf16 v[62:65], v[146:149], v[184:187], v[62:65]
	v_mfma_f32_16x16x32_bf16 v[58:61], v[154:157], v[184:187], v[58:61]
	v_mfma_f32_16x16x32_bf16 v[54:57], v[146:149], v[192:195], v[54:57]
	v_mfma_f32_16x16x32_bf16 v[50:53], v[154:157], v[192:195], v[50:53]
	v_mfma_f32_16x16x32_bf16 v[42:45], v[146:149], v[200:203], v[42:45]
	v_mfma_f32_16x16x32_bf16 v[34:37], v[154:157], v[200:203], v[34:37]
	v_mfma_f32_16x16x32_bf16 v[26:29], v[146:149], v[208:211], v[26:29]
	v_mfma_f32_16x16x32_bf16 v[18:21], v[154:157], v[208:211], v[18:21]
	v_mfma_f32_16x16x32_bf16 v[62:65], v[150:153], v[188:191], v[62:65]
	v_mfma_f32_16x16x32_bf16 v[58:61], v[164:167], v[188:191], v[58:61]
	v_mfma_f32_16x16x32_bf16 v[54:57], v[150:153], v[196:199], v[54:57]
	v_mfma_f32_16x16x32_bf16 v[50:53], v[164:167], v[196:199], v[50:53]
	v_mfma_f32_16x16x32_bf16 v[42:45], v[150:153], v[204:207], v[42:45]
	v_mfma_f32_16x16x32_bf16 v[34:37], v[164:167], v[204:207], v[34:37]
	v_mfma_f32_16x16x32_bf16 v[26:29], v[150:153], v[212:215], v[26:29]
	v_mfma_f32_16x16x32_bf16 v[18:21], v[164:167], v[212:215], v[18:21]
	s_setprio 0
	s_setprio 1
	v_mfma_f32_16x16x32_bf16 v[46:49], v[168:171], v[184:187], v[46:49]
	v_mfma_f32_16x16x32_bf16 v[38:41], v[176:179], v[184:187], v[38:41]
	v_mfma_f32_16x16x32_bf16 v[30:33], v[168:171], v[192:195], v[30:33]
	v_mfma_f32_16x16x32_bf16 v[22:25], v[176:179], v[192:195], v[22:25]
	v_mfma_f32_16x16x32_bf16 v[14:17], v[168:171], v[200:203], v[14:17]
	v_mfma_f32_16x16x32_bf16 v[10:13], v[176:179], v[200:203], v[10:13]
	v_mfma_f32_16x16x32_bf16 v[6:9], v[168:171], v[208:211], v[6:9]
	v_mfma_f32_16x16x32_bf16 v[2:5], v[176:179], v[208:211], v[2:5]
	v_mfma_f32_16x16x32_bf16 v[46:49], v[172:175], v[188:191], v[46:49]
	v_mfma_f32_16x16x32_bf16 v[38:41], v[180:183], v[188:191], v[38:41]
	v_mfma_f32_16x16x32_bf16 v[30:33], v[172:175], v[196:199], v[30:33]
	v_mfma_f32_16x16x32_bf16 v[22:25], v[180:183], v[196:199], v[22:25]
	v_mfma_f32_16x16x32_bf16 v[14:17], v[172:175], v[204:207], v[14:17]
	v_mfma_f32_16x16x32_bf16 v[10:13], v[180:183], v[204:207], v[10:13]
	v_mfma_f32_16x16x32_bf16 v[6:9], v[172:175], v[212:215], v[6:9]
	v_mfma_f32_16x16x32_bf16 v[2:5], v[180:183], v[212:215], v[2:5]
	s_setprio 0
	s_barrier
; #define PG8_STAGE(bufoff, gbase, voff) do { _Pragma("unroll") for (int _i = 0; _i < 2; ++_i) \
;         __builtin_amdgcn_global_load_lds((const unsigned*)((const char*)(gbase) + (voff)[_i]), (PG8_LAS unsigned*)(lds + (bufoff) + ldsw + _i * 8192), 16, 0, 0); } while (0)
; #define PG8_LDA(dst, b, h) do { if constexpr (DT != 1) { _Pragma("unroll") for (int m = 0; m < 4; ++m) _Pragma("unroll") for (int k = 0; k < 2; ++k) dst[m][k] = *(const PG8_LAS bf16x8*)(lds + PG8_SA(b, h) + aoff + m * 2048 + k * 1024); } \
;         else { _Pragma("unroll") for (int m = 0; m < 4; ++m) dst##8[m] = ld32(lds + PG8_SA(b, h) + aoff + m * 2048); } } while (0)
; #define PG8_LDB(dst, b, h) do { if constexpr (DT != 1) { _Pragma("unroll") for (int n = 0; n < 2; ++n) _Pragma("unroll") for (int k = 0; k < 2; ++k) dst[n][k] = *(const PG8_LAS bf16x8*)(lds + PG8_SB(b, h) + boff + n * 2048 + k * 1024); } \
;         else { _Pragma("unroll") for (int n = 0; n < 2; ++n) dst##8[n] = ld32(lds + PG8_SB(b, h) + boff + n * 2048); } } while (0)
; #define PG8_WAIT_V(n) asm volatile("s_waitcnt vmcnt(" #n ")" ::: "memory")
; #define PG8_WAIT_L(n) asm volatile("s_waitcnt lgkmcnt(" #n ")" ::: "memory")
; #define PG8_BAR __builtin_amdgcn_s_barrier()
; #define PG8_SCHED __builtin_amdgcn_sched_barrier(0)
;     ...
;             PG8_LDB(B0, 1, 0); PG8_LDB(B1, 1, 1); PG8_SCHED; PG8_LDA(At, 1, 0); PG8_STAGE(PG8_SA(0, 1), a2 + hstepA, voffA);
;             PG8_WAIT_V(8); PG8_WAIT_L(0); PG8_BAR; PG8_MMA(0, 0, At, B0); PG8_MMA(0, 1, At, B1); PG8_BAR; PG8_SCHED;
;             PG8_LDA(At, 1, 1); PG8_STAGE(PG8_SB(1, 0), b3, voffB); PG8_STAGE(PG8_SB(1, 1), b3 + hstepB, voffB); PG8_STAGE(PG8_SA(1, 0), a3, voffA);
;             PG8_WAIT_V(8); PG8_WAIT_L(0); PG8_BAR; PG8_MMA(1, 0, At, B0); PG8_MMA(1, 1, At, B1); PG8_BAR; PG8_SCHED;
	ds_read_b128 v[146:149], v162
	ds_read_b128 v[150:153], v162 offset:1024
	ds_read_b128 v[154:157], v162 offset:2048
	ds_read_b128 v[164:167], v162 offset:3072
	ds_read_b128 v[168:171], v163
	ds_read_b128 v[172:175], v163 offset:1024
	ds_read_b128 v[176:179], v163 offset:2048
	ds_read_b128 v[180:183], v163 offset:3072
	s_add_u32 s28, s36, 0x160000
	s_addc_u32 s29, s37, 0
	s_mov_b32 m0, s50
	ds_read_b128 v[184:187], v161 offset:32768
	ds_read_b128 v[188:191], v161 offset:33792
	ds_read_b128 v[192:195], v161 offset:34816
	ds_read_b128 v[196:199], v161 offset:35840
	ds_read_b128 v[200:203], v161 offset:36864
	ds_read_b128 v[204:207], v161 offset:37888
	ds_read_b128 v[208:211], v161 offset:38912
	ds_read_b128 v[212:215], v161 offset:39936
	global_load_lds_dwordx4 v130, s[28:29]
	s_mov_b32 m0, s51
	s_nop 0
	global_load_lds_dwordx4 v134, s[28:29]
	s_waitcnt vmcnt(8) lgkmcnt(0)
	s_barrier
	s_setprio 1
	v_mfma_f32_16x16x32_bf16 v[126:129], v[146:149], v[184:187], v[126:129]
	v_mfma_f32_16x16x32_bf16 v[122:125], v[154:157], v[184:187], v[122:125]
	v_mfma_f32_16x16x32_bf16 v[118:121], v[146:149], v[192:195], v[118:121]
	v_mfma_f32_16x16x32_bf16 v[114:117], v[154:157], v[192:195], v[114:117]
	v_mfma_f32_16x16x32_bf16 v[106:109], v[146:149], v[200:203], v[106:109]
	v_mfma_f32_16x16x32_bf16 v[98:101], v[154:157], v[200:203], v[98:101]
	v_mfma_f32_16x16x32_bf16 v[90:93], v[146:149], v[208:211], v[90:93]
	v_mfma_f32_16x16x32_bf16 v[82:85], v[154:157], v[208:211], v[82:85]
	v_mfma_f32_16x16x32_bf16 v[126:129], v[150:153], v[188:191], v[126:129]
	v_mfma_f32_16x16x32_bf16 v[122:125], v[164:167], v[188:191], v[122:125]
	v_mfma_f32_16x16x32_bf16 v[118:121], v[150:153], v[196:199], v[118:121]
	v_mfma_f32_16x16x32_bf16 v[114:117], v[164:167], v[196:199], v[114:117]
	v_mfma_f32_16x16x32_bf16 v[106:109], v[150:153], v[204:207], v[106:109]
	v_mfma_f32_16x16x32_bf16 v[98:101], v[164:167], v[204:207], v[98:101]
	v_mfma_f32_16x16x32_bf16 v[90:93], v[150:153], v[212:215], v[90:93]
	v_mfma_f32_16x16x32_bf16 v[82:85], v[164:167], v[212:215], v[82:85]
	s_setprio 0
	s_setprio 1
	v_mfma_f32_16x16x32_bf16 v[110:113], v[168:171], v[184:187], v[110:113]
	v_mfma_f32_16x16x32_bf16 v[102:105], v[176:179], v[184:187], v[102:105]
	v_mfma_f32_16x16x32_bf16 v[94:97], v[168:171], v[192:195], v[94:97]
	v_mfma_f32_16x16x32_bf16 v[86:89], v[176:179], v[192:195], v[86:89]
	v_mfma_f32_16x16x32_bf16 v[78:81], v[168:171], v[200:203], v[78:81]
	v_mfma_f32_16x16x32_bf16 v[74:77], v[176:179], v[200:203], v[74:77]
	v_mfma_f32_16x16x32_bf16 v[70:73], v[168:171], v[208:211], v[70:73]
	v_mfma_f32_16x16x32_bf16 v[66:69], v[176:179], v[208:211], v[66:69]
	v_mfma_f32_16x16x32_bf16 v[110:113], v[172:175], v[188:191], v[110:113]
	v_mfma_f32_16x16x32_bf16 v[102:105], v[180:183], v[188:191], v[102:105]
	v_mfma_f32_16x16x32_bf16 v[94:97], v[172:175], v[196:199], v[94:97]
	v_mfma_f32_16x16x32_bf16 v[86:89], v[180:183], v[196:199], v[86:89]
	v_mfma_f32_16x16x32_bf16 v[78:81], v[172:175], v[204:207], v[78:81]
	v_mfma_f32_16x16x32_bf16 v[74:77], v[180:183], v[204:207], v[74:77]
	v_mfma_f32_16x16x32_bf16 v[70:73], v[172:175], v[212:215], v[70:73]
	v_mfma_f32_16x16x32_bf16 v[66:69], v[180:183], v[212:215], v[66:69]
	s_setprio 0
	s_barrier
	s_mov_b32 m0, s54
	s_add_u32 s28, s34, 0x160080
	ds_read_b128 v[184:187], v161 offset:49152
	ds_read_b128 v[188:191], v161 offset:50176
	ds_read_b128 v[192:195], v161 offset:51200
	ds_read_b128 v[196:199], v161 offset:52224
	ds_read_b128 v[200:203], v161 offset:53248
	ds_read_b128 v[204:207], v161 offset:54272
	ds_read_b128 v[208:211], v161 offset:55296
	ds_read_b128 v[212:215], v161 offset:56320
	global_load_lds_dwordx4 v132, s[98:99]
	s_mov_b32 m0, s55
	s_addc_u32 s29, s35, 0
	global_load_lds_dwordx4 v136, s[98:99]
	s_mov_b32 m0, s58
	s_nop 0
	global_load_lds_dwordx4 v132, s[28:29]
	s_mov_b32 m0, s59
	s_nop 0
	global_load_lds_dwordx4 v136, s[28:29]
	s_mov_b32 m0, s56
	s_nop 0
	global_load_lds_dwordx4 v130, s[100:101]
	s_mov_b32 m0, s57
	s_nop 0
	global_load_lds_dwordx4 v134, s[100:101]
	s_waitcnt vmcnt(8) lgkmcnt(0)
	s_barrier
; #define PG8_WAIT_V(n) asm volatile("s_waitcnt vmcnt(" #n ")" ::: "memory")
; #define PG8_WAIT_L(n) asm volatile("s_waitcnt lgkmcnt(" #n ")" ::: "memory")
; #define PG8_BAR __builtin_amdgcn_s_barrier()
; #define PG8_SCHED __builtin_amdgcn_sched_barrier(0)
;     __device__ __forceinline__ void operator()(const f32x4 (&acc)[2][2][4][2], const Unit& u, int wr, int wc, int fr, int fq) const {
;     ...
;                     for (int bj = 0; bj < 2; ++bj) { const h16x8_t w = wv[m][bj];
;                         const f32x4 b0 = (f32x4){(float)w[0], (float)w[1], (float)w[2], (float)w[3]}, b1 = (f32x4){(float)w[4], (float)w[5], (float)w[6], (float)w[7]};
;                         const f32x4 o0 = b0 + acc[ai][bj][m][0] * s, o1 = b1 + acc[ai][bj][m][1] * s;
;     ...
;             PG8_WAIT_V(8); PG8_WAIT_L(0); PG8_BAR; PG8_MMA(1, 0, At, B0); PG8_MMA(1, 1, At, B1); PG8_BAR; PG8_SCHED;
	s_setprio 1
	v_mfma_f32_16x16x32_bf16 v[62:65], v[146:149], v[184:187], v[62:65]
	v_mfma_f32_16x16x32_bf16 v[58:61], v[154:157], v[184:187], v[58:61]
	v_mfma_f32_16x16x32_bf16 v[54:57], v[146:149], v[192:195], v[54:57]
	v_mfma_f32_16x16x32_bf16 v[50:53], v[154:157], v[192:195], v[50:53]
	v_mfma_f32_16x16x32_bf16 v[42:45], v[146:149], v[200:203], v[42:45]
	v_mfma_f32_16x16x32_bf16 v[34:37], v[154:157], v[200:203], v[34:37]
	v_mfma_f32_16x16x32_bf16 v[26:29], v[146:149], v[208:211], v[26:29]
	v_mfma_f32_16x16x32_bf16 v[18:21], v[154:157], v[208:211], v[18:21]
	v_mfma_f32_16x16x32_bf16 v[62:65], v[150:153], v[188:191], v[62:65]
	v_mfma_f32_16x16x32_bf16 v[58:61], v[164:167], v[188:191], v[58:61]
	v_mfma_f32_16x16x32_bf16 v[54:57], v[150:153], v[196:199], v[54:57]
	v_mfma_f32_16x16x32_bf16 v[50:53], v[164:167], v[196:199], v[50:53]
	v_mfma_f32_16x16x32_bf16 v[42:45], v[150:153], v[204:207], v[42:45]
	v_mfma_f32_16x16x32_bf16 v[34:37], v[164:167], v[204:207], v[34:37]
	v_mfma_f32_16x16x32_bf16 v[26:29], v[150:153], v[212:215], v[26:29]
	v_mfma_f32_16x16x32_bf16 v[18:21], v[164:167], v[212:215], v[18:21]
	s_setprio 0
	s_setprio 1
	v_mfma_f32_16x16x32_bf16 v[46:49], v[168:171], v[184:187], v[46:49]
	v_mfma_f32_16x16x32_bf16 v[38:41], v[176:179], v[184:187], v[38:41]
	v_mfma_f32_16x16x32_bf16 v[30:33], v[168:171], v[192:195], v[30:33]
	v_mfma_f32_16x16x32_bf16 v[22:25], v[176:179], v[192:195], v[22:25]
	v_mfma_f32_16x16x32_bf16 v[14:17], v[168:171], v[200:203], v[14:17]
	v_mfma_f32_16x16x32_bf16 v[10:13], v[176:179], v[200:203], v[10:13]
	v_mfma_f32_16x16x32_bf16 v[6:9], v[168:171], v[208:211], v[6:9]
	v_mfma_f32_16x16x32_bf16 v[2:5], v[176:179], v[208:211], v[2:5]
	v_mfma_f32_16x16x32_bf16 v[46:49], v[172:175], v[188:191], v[46:49]
	v_mfma_f32_16x16x32_bf16 v[38:41], v[180:183], v[188:191], v[38:41]
	v_mfma_f32_16x16x32_bf16 v[30:33], v[172:175], v[196:199], v[30:33]
	v_mfma_f32_16x16x32_bf16 v[22:25], v[180:183], v[196:199], v[22:25]
	v_mfma_f32_16x16x32_bf16 v[14:17], v[172:175], v[204:207], v[14:17]
	v_mfma_f32_16x16x32_bf16 v[10:13], v[180:183], v[204:207], v[10:13]
	v_mfma_f32_16x16x32_bf16 v[6:9], v[172:175], v[212:215], v[6:9]
	v_mfma_f32_16x16x32_bf16 v[2:5], v[180:183], v[212:215], v[2:5]
	s_setprio 0
	s_barrier
	s_add_u32 s67, s67, 0x100
	s_addc_u32 s68, s68, 0
	s_cmp_ge_i32 s69, s53
	s_mov_b64 s[28:29], s[30:31]
	s_mov_b32 s34, s69
	s_cbranch_scc0 .LBB0_303
	v_pk_mul_f32 v[128:129], v[128:129], 0.5 op_sel_hi:[1,0]
	v_pk_mul_f32 v[126:127], v[126:127], 0.5 op_sel_hi:[1,0]
	v_pk_mul_f32 v[146:147], v[124:125], 0.5 op_sel_hi:[1,0]
	v_pk_mul_f32 v[148:149], v[122:123], 0.5 op_sel_hi:[1,0]
	v_pk_mul_f32 v[150:151], v[112:113], 0.5 op_sel_hi:[1,0]
	v_pk_mul_f32 v[152:153], v[110:111], 0.5 op_sel_hi:[1,0]
	v_pk_mul_f32 v[154:155], v[104:105], 0.5 op_sel_hi:[1,0]
	v_pk_mul_f32 v[156:157], v[102:103], 0.5 op_sel_hi:[1,0]
	v_pk_mul_f32 v[110:111], v[120:121], 0.5 op_sel_hi:[1,0]
	v_pk_mul_f32 v[112:113], v[118:119], 0.5 op_sel_hi:[1,0]
	v_pk_mul_f32 v[116:117], v[116:117], 0.5 op_sel_hi:[1,0]
	v_pk_mul_f32 v[114:115], v[114:115], 0.5 op_sel_hi:[1,0]
	v_pk_mul_f32 v[118:119], v[96:97], 0.5 op_sel_hi:[1,0]
	v_pk_mul_f32 v[120:121], v[94:95], 0.5 op_sel_hi:[1,0]
	v_pk_mul_f32 v[122:123], v[88:89], 0.5 op_sel_hi:[1,0]
	v_pk_mul_f32 v[124:125], v[86:87], 0.5 op_sel_hi:[1,0]
	v_pk_mul_f32 v[94:95], v[108:109], 0.5 op_sel_hi:[1,0]
	v_pk_mul_f32 v[96:97], v[106:107], 0.5 op_sel_hi:[1,0]
	v_pk_mul_f32 v[100:101], v[100:101], 0.5 op_sel_hi:[1,0]
	v_pk_mul_f32 v[98:99], v[98:99], 0.5 op_sel_hi:[1,0]
	v_pk_mul_f32 v[102:103], v[80:81], 0.5 op_sel_hi:[1,0]
	v_pk_mul_f32 v[104:105], v[78:79], 0.5 op_sel_hi:[1,0]
	v_pk_mul_f32 v[106:107], v[76:77], 0.5 op_sel_hi:[1,0]
	v_pk_mul_f32 v[108:109], v[74:75], 0.5 op_sel_hi:[1,0]
	v_pk_mul_f32 v[74:75], v[92:93], 0.5 op_sel_hi:[1,0]
	v_pk_mul_f32 v[76:77], v[90:91], 0.5 op_sel_hi:[1,0]
	v_pk_mul_f32 v[78:79], v[84:85], 0.5 op_sel_hi:[1,0]
	v_pk_mul_f32 v[80:81], v[82:83], 0.5 op_sel_hi:[1,0]
	v_pk_mul_f32 v[86:87], v[72:73], 0.5 op_sel_hi:[1,0]
	v_pk_mul_f32 v[88:89], v[70:71], 0.5 op_sel_hi:[1,0]
	v_pk_mul_f32 v[90:91], v[68:69], 0.5 op_sel_hi:[1,0]
	v_pk_mul_f32 v[92:93], v[66:67], 0.5 op_sel_hi:[1,0]
	v_pk_mul_f32 v[64:65], v[64:65], 0.5 op_sel_hi:[1,0]
	v_pk_mul_f32 v[62:63], v[62:63], 0.5 op_sel_hi:[1,0]
	v_pk_mul_f32 v[66:67], v[60:61], 0.5 op_sel_hi:[1,0]
	v_pk_mul_f32 v[68:69], v[58:59], 0.5 op_sel_hi:[1,0]
	v_pk_mul_f32 v[70:71], v[48:49], 0.5 op_sel_hi:[1,0]
	v_pk_mul_f32 v[72:73], v[46:47], 0.5 op_sel_hi:[1,0]
	v_pk_mul_f32 v[82:83], v[40:41], 0.5 op_sel_hi:[1,0]
	v_pk_mul_f32 v[84:85], v[38:39], 0.5 op_sel_hi:[1,0]
	v_pk_mul_f32 v[46:47], v[56:57], 0.5 op_sel_hi:[1,0]
	v_pk_mul_f32 v[48:49], v[54:55], 0.5 op_sel_hi:[1,0]
	v_pk_mul_f32 v[52:53], v[52:53], 0.5 op_sel_hi:[1,0]
	v_pk_mul_f32 v[50:51], v[50:51], 0.5 op_sel_hi:[1,0]
	v_pk_mul_f32 v[54:55], v[32:33], 0.5 op_sel_hi:[1,0]
	v_pk_mul_f32 v[56:57], v[30:31], 0.5 op_sel_hi:[1,0]
	v_pk_mul_f32 v[58:59], v[24:25], 0.5 op_sel_hi:[1,0]
	v_pk_mul_f32 v[60:61], v[22:23], 0.5 op_sel_hi:[1,0]
	v_pk_mul_f32 v[22:23], v[44:45], 0.5 op_sel_hi:[1,0]
	v_pk_mul_f32 v[24:25], v[42:43], 0.5 op_sel_hi:[1,0]
	v_pk_mul_f32 v[30:31], v[36:37], 0.5 op_sel_hi:[1,0]
	v_pk_mul_f32 v[32:33], v[34:35], 0.5 op_sel_hi:[1,0]
	v_pk_mul_f32 v[34:35], v[16:17], 0.5 op_sel_hi:[1,0]
	v_pk_mul_f32 v[36:37], v[14:15], 0.5 op_sel_hi:[1,0]
	v_pk_mul_f32 v[38:39], v[12:13], 0.5 op_sel_hi:[1,0]
	v_pk_mul_f32 v[40:41], v[10:11], 0.5 op_sel_hi:[1,0]
	v_pk_mul_f32 v[10:11], v[28:29], 0.5 op_sel_hi:[1,0]
	v_pk_mul_f32 v[12:13], v[26:27], 0.5 op_sel_hi:[1,0]
	v_pk_mul_f32 v[14:15], v[20:21], 0.5 op_sel_hi:[1,0]
	v_pk_mul_f32 v[16:17], v[18:19], 0.5 op_sel_hi:[1,0]
	v_pk_mul_f32 v[8:9], v[8:9], 0.5 op_sel_hi:[1,0]
	v_pk_mul_f32 v[6:7], v[6:7], 0.5 op_sel_hi:[1,0]
	v_pk_mul_f32 v[4:5], v[4:5], 0.5 op_sel_hi:[1,0]
	v_pk_mul_f32 v[2:3], v[2:3], 0.5 op_sel_hi:[1,0]

; #define PG8_STAGE(bufoff, gbase, voff) do { _Pragma("unroll") for (int _i = 0; _i < 2; ++_i) \
;         __builtin_amdgcn_global_load_lds((const unsigned*)((const char*)(gbase) + (voff)[_i]), (PG8_LAS unsigned*)(lds + (bufoff) + ldsw + _i * 8192), 16, 0, 0); } while (0)
; #define PG8_LDA(dst, b, h) do { if constexpr (DT != 1) { _Pragma("unroll") for (int m = 0; m < 4; ++m) _Pragma("unroll") for (int k = 0; k < 2; ++k) dst[m][k] = *(const PG8_LAS bf16x8*)(lds + PG8_SA(b, h) + aoff + m * 2048 + k * 1024); } \
;         else { _Pragma("unroll") for (int m = 0; m < 4; ++m) dst##8[m] = ld32(lds + PG8_SA(b, h) + aoff + m * 2048); } } while (0)
; #define PG8_LDB(dst, b, h) do { if constexpr (DT != 1) { _Pragma("unroll") for (int n = 0; n < 2; ++n) _Pragma("unroll") for (int k = 0; k < 2; ++k) dst[n][k] = *(const PG8_LAS bf16x8*)(lds + PG8_SB(b, h) + boff + n * 2048 + k * 1024); } \
;         else { _Pragma("unroll") for (int n = 0; n < 2; ++n) dst##8[n] = ld32(lds + PG8_SB(b, h) + boff + n * 2048); } } while (0)
; #define PG8_WAIT_V(n) asm volatile("s_waitcnt vmcnt(" #n ")" ::: "memory")
; #define PG8_WAIT_L(n) asm volatile("s_waitcnt lgkmcnt(" #n ")" ::: "memory")
; #define PG8_BAR __builtin_amdgcn_s_barrier()
; #define PG8_SCHED __builtin_amdgcn_sched_barrier(0)
;     ...
;             PG8_LDB(B0, 0, 0); PG8_LDB(B1, 0, 1); PG8_SCHED; PG8_LDA(At, 0, 0); PG8_STAGE(PG8_SA(1, 1), a1 + hstepA, voffA);
;             PG8_WAIT_V(8); PG8_WAIT_L(0); PG8_BAR; PG8_MMA(0, 0, At, B0); PG8_MMA(0, 1, At, B1); PG8_BAR; PG8_SCHED;
;             PG8_LDA(At, 0, 1); PG8_STAGE(PG8_SB(0, 0), b2, voffB); PG8_STAGE(PG8_SB(0, 1), b2 + hstepB, voffB); PG8_STAGE(PG8_SA(0, 0), a2, voffA);
;             PG8_WAIT_V(8); PG8_WAIT_L(0); PG8_BAR; PG8_MMA(1, 0, At, B0); PG8_MMA(1, 1, At, B1); PG8_BAR; PG8_SCHED;
.LBB0_418:
	ds_read_b128 v[156:159], v150
	ds_read_b128 v[160:163], v150 offset:1024
	ds_read_b128 v[164:167], v150 offset:2048
	ds_read_b128 v[168:171], v150 offset:3072
	ds_read_b128 v[172:175], v151
	ds_read_b128 v[176:179], v151 offset:1024
	ds_read_b128 v[180:183], v151 offset:2048
	ds_read_b128 v[184:187], v151 offset:3072
	s_add_i32 s65, s28, 2
	s_add_u32 s29, s26, 0xfff80080
	s_addc_u32 s30, s27, -1
	s_cmp_eq_u32 s59, s28
	s_cselect_b32 s28, s62, s63
	s_cselect_b32 s31, s19, s30
	s_cselect_b32 s30, s21, s29
	s_cselect_b32 s29, s61, s64
	s_add_i32 m0, s45, 0xc000
	ds_read_b128 v[188:191], v152
	ds_read_b128 v[192:195], v152 offset:1024
	ds_read_b128 v[196:199], v152 offset:2048
	ds_read_b128 v[200:203], v152 offset:3072
	ds_read_b128 v[204:207], v152 offset:4096
	ds_read_b128 v[208:211], v152 offset:5120
	ds_read_b128 v[212:215], v152 offset:6144
	ds_read_b128 v[216:219], v152 offset:7168
	global_load_lds_dwordx4 v144, s[26:27]
	s_add_i32 m0, s45, 0xe000
	s_nop 0
	global_load_lds_dwordx4 v142, s[26:27]
	s_waitcnt vmcnt(8) lgkmcnt(0)
	s_barrier
	s_setprio 1
	v_mfma_f32_16x16x32_bf16 v[122:125], v[156:159], v[188:191], v[122:125]
	v_mfma_f32_16x16x32_bf16 v[126:129], v[164:167], v[188:191], v[126:129]
	v_mfma_f32_16x16x32_bf16 v[110:113], v[156:159], v[196:199], v[110:113]
	v_mfma_f32_16x16x32_bf16 v[106:109], v[164:167], v[196:199], v[106:109]
	v_mfma_f32_16x16x32_bf16 v[94:97], v[156:159], v[204:207], v[94:97]
	v_mfma_f32_16x16x32_bf16 v[90:93], v[164:167], v[204:207], v[90:93]
	v_mfma_f32_16x16x32_bf16 v[78:81], v[156:159], v[212:215], v[78:81]
	v_mfma_f32_16x16x32_bf16 v[74:77], v[164:167], v[212:215], v[74:77]
	v_mfma_f32_16x16x32_bf16 v[122:125], v[160:163], v[192:195], v[122:125]
	v_mfma_f32_16x16x32_bf16 v[126:129], v[168:171], v[192:195], v[126:129]
	v_mfma_f32_16x16x32_bf16 v[110:113], v[160:163], v[200:203], v[110:113]
	v_mfma_f32_16x16x32_bf16 v[106:109], v[168:171], v[200:203], v[106:109]
	v_mfma_f32_16x16x32_bf16 v[94:97], v[160:163], v[208:211], v[94:97]
	v_mfma_f32_16x16x32_bf16 v[90:93], v[168:171], v[208:211], v[90:93]
	v_mfma_f32_16x16x32_bf16 v[78:81], v[160:163], v[216:219], v[78:81]
	v_mfma_f32_16x16x32_bf16 v[74:77], v[168:171], v[216:219], v[74:77]
	s_setprio 0
	s_setprio 1
	v_mfma_f32_16x16x32_bf16 v[118:121], v[172:175], v[188:191], v[118:121]
	v_mfma_f32_16x16x32_bf16 v[114:117], v[180:183], v[188:191], v[114:117]
	v_mfma_f32_16x16x32_bf16 v[102:105], v[172:175], v[196:199], v[102:105]
	v_mfma_f32_16x16x32_bf16 v[98:101], v[180:183], v[196:199], v[98:101]
	v_mfma_f32_16x16x32_bf16 v[86:89], v[172:175], v[204:207], v[86:89]
	v_mfma_f32_16x16x32_bf16 v[82:85], v[180:183], v[204:207], v[82:85]
	v_mfma_f32_16x16x32_bf16 v[70:73], v[172:175], v[212:215], v[70:73]
	v_mfma_f32_16x16x32_bf16 v[66:69], v[180:183], v[212:215], v[66:69]
	v_mfma_f32_16x16x32_bf16 v[118:121], v[176:179], v[192:195], v[118:121]
	v_mfma_f32_16x16x32_bf16 v[114:117], v[184:187], v[192:195], v[114:117]
	v_mfma_f32_16x16x32_bf16 v[102:105], v[176:179], v[200:203], v[102:105]
	v_mfma_f32_16x16x32_bf16 v[98:101], v[184:187], v[200:203], v[98:101]
	v_mfma_f32_16x16x32_bf16 v[86:89], v[176:179], v[208:211], v[86:89]
	v_mfma_f32_16x16x32_bf16 v[82:85], v[184:187], v[208:211], v[82:85]
	v_mfma_f32_16x16x32_bf16 v[70:73], v[176:179], v[216:219], v[70:73]
	v_mfma_f32_16x16x32_bf16 v[66:69], v[184:187], v[216:219], v[66:69]
	s_setprio 0
	s_barrier
	s_mov_b32 m0, s41
	s_add_u32 s98, s28, 0x80
	s_addc_u32 s99, s29, 0
	s_add_u32 s66, s28, 0x80000
	ds_read_b128 v[188:191], v152 offset:16384
	ds_read_b128 v[192:195], v152 offset:17408
	ds_read_b128 v[196:199], v152 offset:18432
	ds_read_b128 v[200:203], v152 offset:19456
	ds_read_b128 v[204:207], v152 offset:20480
	ds_read_b128 v[208:211], v152 offset:21504
	ds_read_b128 v[212:215], v152 offset:22528
	ds_read_b128 v[216:219], v152 offset:23552
	global_load_lds_dwordx4 v132, s[28:29]
	s_mov_b32 m0, s42
	s_addc_u32 s67, s29, 0
	global_load_lds_dwordx4 v136, s[28:29]
	s_mov_b32 m0, s43
	s_nop 0
	global_load_lds_dwordx4 v132, s[66:67]
	s_mov_b32 m0, s44
	s_nop 0
	global_load_lds_dwordx4 v136, s[66:67]
	s_add_u32 s100, s30, 0x80
	s_addc_u32 s101, s31, 0
	s_mov_b32 m0, s45
	s_nop 0
	global_load_lds_dwordx4 v130, s[30:31]
	s_mov_b32 m0, s46
	s_nop 0
	global_load_lds_dwordx4 v134, s[30:31]
	s_waitcnt vmcnt(8) lgkmcnt(0)
	s_barrier
	s_setprio 1
	v_mfma_f32_16x16x32_bf16 v[62:65], v[156:159], v[188:191], v[62:65]
	v_mfma_f32_16x16x32_bf16 v[58:61], v[164:167], v[188:191], v[58:61]
	v_mfma_f32_16x16x32_bf16 v[46:49], v[156:159], v[196:199], v[46:49]
	v_mfma_f32_16x16x32_bf16 v[42:45], v[164:167], v[196:199], v[42:45]
	v_mfma_f32_16x16x32_bf16 v[30:33], v[156:159], v[204:207], v[30:33]
	v_mfma_f32_16x16x32_bf16 v[26:29], v[164:167], v[204:207], v[26:29]
	v_mfma_f32_16x16x32_bf16 v[14:17], v[156:159], v[212:215], v[14:17]
	v_mfma_f32_16x16x32_bf16 v[10:13], v[164:167], v[212:215], v[10:13]
	v_mfma_f32_16x16x32_bf16 v[62:65], v[160:163], v[192:195], v[62:65]
	v_mfma_f32_16x16x32_bf16 v[58:61], v[168:171], v[192:195], v[58:61]
	v_mfma_f32_16x16x32_bf16 v[46:49], v[160:163], v[200:203], v[46:49]
	v_mfma_f32_16x16x32_bf16 v[42:45], v[168:171], v[200:203], v[42:45]
	v_mfma_f32_16x16x32_bf16 v[30:33], v[160:163], v[208:211], v[30:33]
	v_mfma_f32_16x16x32_bf16 v[26:29], v[168:171], v[208:211], v[26:29]
	v_mfma_f32_16x16x32_bf16 v[14:17], v[160:163], v[216:219], v[14:17]
	v_mfma_f32_16x16x32_bf16 v[10:13], v[168:171], v[216:219], v[10:13]
	s_setprio 0
	s_setprio 1
	v_mfma_f32_16x16x32_bf16 v[54:57], v[172:175], v[188:191], v[54:57]
	v_mfma_f32_16x16x32_bf16 v[50:53], v[180:183], v[188:191], v[50:53]
	v_mfma_f32_16x16x32_bf16 v[38:41], v[172:175], v[196:199], v[38:41]
	v_mfma_f32_16x16x32_bf16 v[34:37], v[180:183], v[196:199], v[34:37]
	v_mfma_f32_16x16x32_bf16 v[22:25], v[172:175], v[204:207], v[22:25]
	v_mfma_f32_16x16x32_bf16 v[18:21], v[180:183], v[204:207], v[18:21]
	v_mfma_f32_16x16x32_bf16 v[6:9], v[172:175], v[212:215], v[6:9]
	v_mfma_f32_16x16x32_bf16 v[2:5], v[180:183], v[212:215], v[2:5]
	v_mfma_f32_16x16x32_bf16 v[54:57], v[176:179], v[192:195], v[54:57]
	v_mfma_f32_16x16x32_bf16 v[50:53], v[184:187], v[192:195], v[50:53]
	v_mfma_f32_16x16x32_bf16 v[38:41], v[176:179], v[200:203], v[38:41]
	v_mfma_f32_16x16x32_bf16 v[34:37], v[184:187], v[200:203], v[34:37]
	v_mfma_f32_16x16x32_bf16 v[22:25], v[176:179], v[208:211], v[22:25]
	v_mfma_f32_16x16x32_bf16 v[18:21], v[184:187], v[208:211], v[18:21]
	v_mfma_f32_16x16x32_bf16 v[6:9], v[176:179], v[216:219], v[6:9]
	v_mfma_f32_16x16x32_bf16 v[2:5], v[184:187], v[216:219], v[2:5]
	s_setprio 0
	s_barrier
; #define PG8_STAGE(bufoff, gbase, voff) do { _Pragma("unroll") for (int _i = 0; _i < 2; ++_i) \
;         __builtin_amdgcn_global_load_lds((const unsigned*)((const char*)(gbase) + (voff)[_i]), (PG8_LAS unsigned*)(lds + (bufoff) + ldsw + _i * 8192), 16, 0, 0); } while (0)
; #define PG8_LDA(dst, b, h) do { if constexpr (DT != 1) { _Pragma("unroll") for (int m = 0; m < 4; ++m) _Pragma("unroll") for (int k = 0; k < 2; ++k) dst[m][k] = *(const PG8_LAS bf16x8*)(lds + PG8_SA(b, h) + aoff + m * 2048 + k * 1024); } \
;         else { _Pragma("unroll") for (int m = 0; m < 4; ++m) dst##8[m] = ld32(lds + PG8_SA(b, h) + aoff + m * 2048); } } while (0)
; #define PG8_LDB(dst, b, h) do { if constexpr (DT != 1) { _Pragma("unroll") for (int n = 0; n < 2; ++n) _Pragma("unroll") for (int k = 0; k < 2; ++k) dst[n][k] = *(const PG8_LAS bf16x8*)(lds + PG8_SB(b, h) + boff + n * 2048 + k * 1024); } \
;         else { _Pragma("unroll") for (int n = 0; n < 2; ++n) dst##8[n] = ld32(lds + PG8_SB(b, h) + boff + n * 2048); } } while (0)
; #define PG8_WAIT_V(n) asm volatile("s_waitcnt vmcnt(" #n ")" ::: "memory")
; #define PG8_WAIT_L(n) asm volatile("s_waitcnt lgkmcnt(" #n ")" ::: "memory")
; #define PG8_BAR __builtin_amdgcn_s_barrier()
; #define PG8_SCHED __builtin_amdgcn_sched_barrier(0)
;     ...
;             PG8_LDB(B0, 1, 0); PG8_LDB(B1, 1, 1); PG8_SCHED; PG8_LDA(At, 1, 0); PG8_STAGE(PG8_SA(0, 1), a2 + hstepA, voffA);
;             PG8_WAIT_V(8); PG8_WAIT_L(0); PG8_BAR; PG8_MMA(0, 0, At, B0); PG8_MMA(0, 1, At, B1); PG8_BAR; PG8_SCHED;
;             PG8_LDA(At, 1, 1); PG8_STAGE(PG8_SB(1, 0), b3, voffB); PG8_STAGE(PG8_SB(1, 1), b3 + hstepB, voffB); PG8_STAGE(PG8_SA(1, 0), a3, voffA);
;             PG8_WAIT_V(8); PG8_WAIT_L(0); PG8_BAR; PG8_MMA(1, 0, At, B0); PG8_MMA(1, 1, At, B1); PG8_BAR; PG8_SCHED;
	ds_read_b128 v[156:159], v153
	ds_read_b128 v[160:163], v153 offset:1024
	ds_read_b128 v[164:167], v153 offset:2048
	ds_read_b128 v[168:171], v153 offset:3072
	ds_read_b128 v[172:175], v154
	ds_read_b128 v[176:179], v154 offset:1024
	ds_read_b128 v[180:183], v154 offset:2048
	ds_read_b128 v[184:187], v154 offset:3072
	s_add_u32 s30, s30, 0x80000
	s_addc_u32 s31, s31, 0
	s_mov_b32 m0, s47
	ds_read_b128 v[188:191], v152 offset:32768
	ds_read_b128 v[192:195], v152 offset:33792
	ds_read_b128 v[196:199], v152 offset:34816
	ds_read_b128 v[200:203], v152 offset:35840
	ds_read_b128 v[204:207], v152 offset:36864
	ds_read_b128 v[208:211], v152 offset:37888
	ds_read_b128 v[212:215], v152 offset:38912
	ds_read_b128 v[216:219], v152 offset:39936
	global_load_lds_dwordx4 v130, s[30:31]
	s_mov_b32 m0, s48
	s_nop 0
	global_load_lds_dwordx4 v134, s[30:31]
	s_waitcnt vmcnt(8) lgkmcnt(0)
	s_barrier
	s_setprio 1
	v_mfma_f32_16x16x32_bf16 v[122:125], v[156:159], v[188:191], v[122:125]
	v_mfma_f32_16x16x32_bf16 v[126:129], v[164:167], v[188:191], v[126:129]
	v_mfma_f32_16x16x32_bf16 v[110:113], v[156:159], v[196:199], v[110:113]
	v_mfma_f32_16x16x32_bf16 v[106:109], v[164:167], v[196:199], v[106:109]
	v_mfma_f32_16x16x32_bf16 v[94:97], v[156:159], v[204:207], v[94:97]
	v_mfma_f32_16x16x32_bf16 v[90:93], v[164:167], v[204:207], v[90:93]
	v_mfma_f32_16x16x32_bf16 v[78:81], v[156:159], v[212:215], v[78:81]
	v_mfma_f32_16x16x32_bf16 v[74:77], v[164:167], v[212:215], v[74:77]
	v_mfma_f32_16x16x32_bf16 v[122:125], v[160:163], v[192:195], v[122:125]
	v_mfma_f32_16x16x32_bf16 v[126:129], v[168:171], v[192:195], v[126:129]
	v_mfma_f32_16x16x32_bf16 v[110:113], v[160:163], v[200:203], v[110:113]
	v_mfma_f32_16x16x32_bf16 v[106:109], v[168:171], v[200:203], v[106:109]
	v_mfma_f32_16x16x32_bf16 v[94:97], v[160:163], v[208:211], v[94:97]
	v_mfma_f32_16x16x32_bf16 v[90:93], v[168:171], v[208:211], v[90:93]
	v_mfma_f32_16x16x32_bf16 v[78:81], v[160:163], v[216:219], v[78:81]
	v_mfma_f32_16x16x32_bf16 v[74:77], v[168:171], v[216:219], v[74:77]
	s_setprio 0
	s_setprio 1
	v_mfma_f32_16x16x32_bf16 v[118:121], v[172:175], v[188:191], v[118:121]
	v_mfma_f32_16x16x32_bf16 v[114:117], v[180:183], v[188:191], v[114:117]
	v_mfma_f32_16x16x32_bf16 v[102:105], v[172:175], v[196:199], v[102:105]
	v_mfma_f32_16x16x32_bf16 v[98:101], v[180:183], v[196:199], v[98:101]
	v_mfma_f32_16x16x32_bf16 v[86:89], v[172:175], v[204:207], v[86:89]
	v_mfma_f32_16x16x32_bf16 v[82:85], v[180:183], v[204:207], v[82:85]
	v_mfma_f32_16x16x32_bf16 v[70:73], v[172:175], v[212:215], v[70:73]
	v_mfma_f32_16x16x32_bf16 v[66:69], v[180:183], v[212:215], v[66:69]
	v_mfma_f32_16x16x32_bf16 v[118:121], v[176:179], v[192:195], v[118:121]
	v_mfma_f32_16x16x32_bf16 v[114:117], v[184:187], v[192:195], v[114:117]
	v_mfma_f32_16x16x32_bf16 v[102:105], v[176:179], v[200:203], v[102:105]
	v_mfma_f32_16x16x32_bf16 v[98:101], v[184:187], v[200:203], v[98:101]
	v_mfma_f32_16x16x32_bf16 v[86:89], v[176:179], v[208:211], v[86:89]
	v_mfma_f32_16x16x32_bf16 v[82:85], v[184:187], v[208:211], v[82:85]
	v_mfma_f32_16x16x32_bf16 v[70:73], v[176:179], v[216:219], v[70:73]
	v_mfma_f32_16x16x32_bf16 v[66:69], v[184:187], v[216:219], v[66:69]
	s_setprio 0
	s_barrier
	s_mov_b32 m0, s50
	s_add_u32 s28, s28, 0x80080
	ds_read_b128 v[188:191], v152 offset:49152
	ds_read_b128 v[192:195], v152 offset:50176
	ds_read_b128 v[196:199], v152 offset:51200
	ds_read_b128 v[200:203], v152 offset:52224
	ds_read_b128 v[204:207], v152 offset:53248
	ds_read_b128 v[208:211], v152 offset:54272
	ds_read_b128 v[212:215], v152 offset:55296
	ds_read_b128 v[216:219], v152 offset:56320
	global_load_lds_dwordx4 v132, s[98:99]
	s_mov_b32 m0, s51
	s_addc_u32 s29, s29, 0
	global_load_lds_dwordx4 v136, s[98:99]
	s_mov_b32 m0, s54
	s_nop 0
	global_load_lds_dwordx4 v132, s[28:29]
	s_mov_b32 m0, s55
	s_nop 0
	global_load_lds_dwordx4 v136, s[28:29]
	s_mov_b32 m0, s52
	s_nop 0
	global_load_lds_dwordx4 v130, s[100:101]
	s_mov_b32 m0, s53
	s_nop 0
	global_load_lds_dwordx4 v134, s[100:101]
	s_waitcnt vmcnt(8) lgkmcnt(0)
	s_barrier
	s_setprio 1
	v_mfma_f32_16x16x32_bf16 v[62:65], v[156:159], v[188:191], v[62:65]
	v_mfma_f32_16x16x32_bf16 v[58:61], v[164:167], v[188:191], v[58:61]
	v_mfma_f32_16x16x32_bf16 v[46:49], v[156:159], v[196:199], v[46:49]
	v_mfma_f32_16x16x32_bf16 v[42:45], v[164:167], v[196:199], v[42:45]
	v_mfma_f32_16x16x32_bf16 v[30:33], v[156:159], v[204:207], v[30:33]
	v_mfma_f32_16x16x32_bf16 v[26:29], v[164:167], v[204:207], v[26:29]
	v_mfma_f32_16x16x32_bf16 v[14:17], v[156:159], v[212:215], v[14:17]
	v_mfma_f32_16x16x32_bf16 v[10:13], v[164:167], v[212:215], v[10:13]
	v_mfma_f32_16x16x32_bf16 v[62:65], v[160:163], v[192:195], v[62:65]
	v_mfma_f32_16x16x32_bf16 v[58:61], v[168:171], v[192:195], v[58:61]
	v_mfma_f32_16x16x32_bf16 v[46:49], v[160:163], v[200:203], v[46:49]
	v_mfma_f32_16x16x32_bf16 v[42:45], v[168:171], v[200:203], v[42:45]
	v_mfma_f32_16x16x32_bf16 v[30:33], v[160:163], v[208:211], v[30:33]
	v_mfma_f32_16x16x32_bf16 v[26:29], v[168:171], v[208:211], v[26:29]
	v_mfma_f32_16x16x32_bf16 v[14:17], v[160:163], v[216:219], v[14:17]
	v_mfma_f32_16x16x32_bf16 v[10:13], v[168:171], v[216:219], v[10:13]
	s_setprio 0
	s_setprio 1
	v_mfma_f32_16x16x32_bf16 v[54:57], v[172:175], v[188:191], v[54:57]
	v_mfma_f32_16x16x32_bf16 v[50:53], v[180:183], v[188:191], v[50:53]
	v_mfma_f32_16x16x32_bf16 v[38:41], v[172:175], v[196:199], v[38:41]
	v_mfma_f32_16x16x32_bf16 v[34:37], v[180:183], v[196:199], v[34:37]
	v_mfma_f32_16x16x32_bf16 v[22:25], v[172:175], v[204:207], v[22:25]
	v_mfma_f32_16x16x32_bf16 v[18:21], v[180:183], v[204:207], v[18:21]
	v_mfma_f32_16x16x32_bf16 v[6:9], v[172:175], v[212:215], v[6:9]
	v_mfma_f32_16x16x32_bf16 v[2:5], v[180:183], v[212:215], v[2:5]
	v_mfma_f32_16x16x32_bf16 v[54:57], v[176:179], v[192:195], v[54:57]
	v_mfma_f32_16x16x32_bf16 v[50:53], v[184:187], v[192:195], v[50:53]
	v_mfma_f32_16x16x32_bf16 v[38:41], v[176:179], v[200:203], v[38:41]
	v_mfma_f32_16x16x32_bf16 v[34:37], v[184:187], v[200:203], v[34:37]
	v_mfma_f32_16x16x32_bf16 v[22:25], v[176:179], v[208:211], v[22:25]
	v_mfma_f32_16x16x32_bf16 v[18:21], v[184:187], v[208:211], v[18:21]
	v_mfma_f32_16x16x32_bf16 v[6:9], v[176:179], v[216:219], v[6:9]
	v_mfma_f32_16x16x32_bf16 v[2:5], v[184:187], v[216:219], v[2:5]
	s_setprio 0
	s_barrier
	s_add_u32 s63, s63, 0x100
	s_addc_u32 s64, s64, 0
	s_add_u32 s26, s26, 0x100
	s_addc_u32 s27, s27, 0
	s_cmp_ge_i32 s65, s49
	s_mov_b32 s28, s65
	s_cbranch_scc0 .LBB0_418

; #define PG8_STAGE(bufoff, gbase, voff) do { _Pragma("unroll") for (int _i = 0; _i < 2; ++_i) \
;         __builtin_amdgcn_global_load_lds((const unsigned*)((const char*)(gbase) + (voff)[_i]), (PG8_LAS unsigned*)(lds + (bufoff) + ldsw + _i * 8192), 16, 0, 0); } while (0)
; #define PG8_LDA(dst, b, h) do { if constexpr (DT != 1) { _Pragma("unroll") for (int m = 0; m < 4; ++m) _Pragma("unroll") for (int k = 0; k < 2; ++k) dst[m][k] = *(const PG8_LAS bf16x8*)(lds + PG8_SA(b, h) + aoff + m * 2048 + k * 1024); } \
;         else { _Pragma("unroll") for (int m = 0; m < 4; ++m) dst##8[m] = ld32(lds + PG8_SA(b, h) + aoff + m * 2048); } } while (0)
; #define PG8_LDB(dst, b, h) do { if constexpr (DT != 1) { _Pragma("unroll") for (int n = 0; n < 2; ++n) _Pragma("unroll") for (int k = 0; k < 2; ++k) dst[n][k] = *(const PG8_LAS bf16x8*)(lds + PG8_SB(b, h) + boff + n * 2048 + k * 1024); } \
;         else { _Pragma("unroll") for (int n = 0; n < 2; ++n) dst##8[n] = ld32(lds + PG8_SB(b, h) + boff + n * 2048); } } while (0)
; #define PG8_WAIT_V(n) asm volatile("s_waitcnt vmcnt(" #n ")" ::: "memory")
; #define PG8_WAIT_L(n) asm volatile("s_waitcnt lgkmcnt(" #n ")" ::: "memory")
; #define PG8_BAR __builtin_amdgcn_s_barrier()
; #define PG8_SCHED __builtin_amdgcn_sched_barrier(0)
;     ...
;             PG8_LDB(B0, 0, 0); PG8_LDB(B1, 0, 1); PG8_SCHED; PG8_LDA(At, 0, 0); PG8_STAGE(PG8_SA(1, 1), a1 + hstepA, voffA);
;             PG8_WAIT_V(8); PG8_WAIT_L(0); PG8_BAR; PG8_MMA(0, 0, At, B0); PG8_MMA(0, 1, At, B1); PG8_BAR; PG8_SCHED;
;             PG8_LDA(At, 0, 1); PG8_STAGE(PG8_SB(0, 0), b2, voffB); PG8_STAGE(PG8_SB(0, 1), b2 + hstepB, voffB); PG8_STAGE(PG8_SA(0, 0), a2, voffA);
;             PG8_WAIT_V(8); PG8_WAIT_L(0); PG8_BAR; PG8_MMA(1, 0, At, B0); PG8_MMA(1, 1, At, B1); PG8_BAR; PG8_SCHED;
.LBB0_713:
	ds_read_b128 v[130:133], v173
	ds_read_b128 v[134:137], v173 offset:1024
	ds_read_b128 v[138:141], v173 offset:2048
	ds_read_b128 v[142:145], v173 offset:3072
	ds_read_b128 v[162:165], v174
	ds_read_b128 v[166:169], v174 offset:1024
	ds_read_b128 v[178:181], v174 offset:2048
	ds_read_b128 v[182:185], v174 offset:3072
	s_add_i32 s69, s36, 2
	s_add_u32 s37, s34, 0xfff80080
	s_addc_u32 s38, s35, -1
	s_cmp_eq_u32 s61, s36
	s_cselect_b32 s36, s66, s67
	s_cselect_b32 s39, s23, s38
	s_cselect_b32 s38, s25, s37
	s_cselect_b32 s37, s65, s68
	s_add_i32 m0, s49, 0xc000
	ds_read_b128 v[186:189], v175
	ds_read_b128 v[190:193], v175 offset:1024
	ds_read_b128 v[194:197], v175 offset:2048
	ds_read_b128 v[198:201], v175 offset:3072
	ds_read_b128 v[202:205], v175 offset:4096
	ds_read_b128 v[206:209], v175 offset:5120
	ds_read_b128 v[210:213], v175 offset:6144
	ds_read_b128 v[214:217], v175 offset:7168
	global_load_lds_dwordx4 v156, s[34:35]
	s_add_i32 m0, s49, 0xe000
	s_nop 0
	global_load_lds_dwordx4 v154, s[34:35]
	s_waitcnt vmcnt(8) lgkmcnt(0)
	s_barrier
	s_setprio 1
	v_mfma_f32_16x16x32_bf16 v[122:125], v[130:133], v[186:189], v[122:125]
	v_mfma_f32_16x16x32_bf16 v[126:129], v[138:141], v[186:189], v[126:129]
	v_mfma_f32_16x16x32_bf16 v[110:113], v[130:133], v[194:197], v[110:113]
	v_mfma_f32_16x16x32_bf16 v[106:109], v[138:141], v[194:197], v[106:109]
	v_mfma_f32_16x16x32_bf16 v[94:97], v[130:133], v[202:205], v[94:97]
	v_mfma_f32_16x16x32_bf16 v[90:93], v[138:141], v[202:205], v[90:93]
	v_mfma_f32_16x16x32_bf16 v[78:81], v[130:133], v[210:213], v[78:81]
	v_mfma_f32_16x16x32_bf16 v[74:77], v[138:141], v[210:213], v[74:77]
	v_mfma_f32_16x16x32_bf16 v[122:125], v[134:137], v[190:193], v[122:125]
	v_mfma_f32_16x16x32_bf16 v[126:129], v[142:145], v[190:193], v[126:129]
	v_mfma_f32_16x16x32_bf16 v[110:113], v[134:137], v[198:201], v[110:113]
	v_mfma_f32_16x16x32_bf16 v[106:109], v[142:145], v[198:201], v[106:109]
	v_mfma_f32_16x16x32_bf16 v[94:97], v[134:137], v[206:209], v[94:97]
	v_mfma_f32_16x16x32_bf16 v[90:93], v[142:145], v[206:209], v[90:93]
	v_mfma_f32_16x16x32_bf16 v[78:81], v[134:137], v[214:217], v[78:81]
	v_mfma_f32_16x16x32_bf16 v[74:77], v[142:145], v[214:217], v[74:77]
	s_setprio 0
	s_setprio 1
	v_mfma_f32_16x16x32_bf16 v[118:121], v[162:165], v[186:189], v[118:121]
	v_mfma_f32_16x16x32_bf16 v[114:117], v[178:181], v[186:189], v[114:117]
	v_mfma_f32_16x16x32_bf16 v[102:105], v[162:165], v[194:197], v[102:105]
	v_mfma_f32_16x16x32_bf16 v[98:101], v[178:181], v[194:197], v[98:101]
	v_mfma_f32_16x16x32_bf16 v[86:89], v[162:165], v[202:205], v[86:89]
	v_mfma_f32_16x16x32_bf16 v[82:85], v[178:181], v[202:205], v[82:85]
	v_mfma_f32_16x16x32_bf16 v[70:73], v[162:165], v[210:213], v[70:73]
	v_mfma_f32_16x16x32_bf16 v[66:69], v[178:181], v[210:213], v[66:69]
	v_mfma_f32_16x16x32_bf16 v[118:121], v[166:169], v[190:193], v[118:121]
	v_mfma_f32_16x16x32_bf16 v[114:117], v[182:185], v[190:193], v[114:117]
	v_mfma_f32_16x16x32_bf16 v[102:105], v[166:169], v[198:201], v[102:105]
	v_mfma_f32_16x16x32_bf16 v[98:101], v[182:185], v[198:201], v[98:101]
	v_mfma_f32_16x16x32_bf16 v[86:89], v[166:169], v[206:209], v[86:89]
	v_mfma_f32_16x16x32_bf16 v[82:85], v[182:185], v[206:209], v[82:85]
	v_mfma_f32_16x16x32_bf16 v[70:73], v[166:169], v[214:217], v[70:73]
	v_mfma_f32_16x16x32_bf16 v[66:69], v[182:185], v[214:217], v[66:69]
	s_setprio 0
	s_barrier
	s_mov_b32 m0, s31
	s_add_u32 s98, s36, 0x80
	s_addc_u32 s99, s37, 0
	s_add_u32 s70, s36, 0x80000
	ds_read_b128 v[186:189], v175 offset:16384
	ds_read_b128 v[190:193], v175 offset:17408
	ds_read_b128 v[194:197], v175 offset:18432
	ds_read_b128 v[198:201], v175 offset:19456
	ds_read_b128 v[202:205], v175 offset:20480
	ds_read_b128 v[206:209], v175 offset:21504
	ds_read_b128 v[210:213], v175 offset:22528
	ds_read_b128 v[214:217], v175 offset:23552
	global_load_lds_dwordx4 v148, s[36:37]
	s_mov_b32 m0, s46
	s_addc_u32 s71, s37, 0
	global_load_lds_dwordx4 v152, s[36:37]
	s_mov_b32 m0, s47
	s_nop 0
	global_load_lds_dwordx4 v148, s[70:71]
	s_mov_b32 m0, s48
	s_nop 0
	global_load_lds_dwordx4 v152, s[70:71]
	s_add_u32 s100, s38, 0x80
	s_addc_u32 s101, s39, 0
	s_mov_b32 m0, s49
	s_nop 0
	global_load_lds_dwordx4 v146, s[38:39]
	s_mov_b32 m0, s50
	s_nop 0
	global_load_lds_dwordx4 v150, s[38:39]
	s_waitcnt vmcnt(8) lgkmcnt(0)
	s_barrier
	s_setprio 1
	v_mfma_f32_16x16x32_bf16 v[62:65], v[130:133], v[186:189], v[62:65]
	v_mfma_f32_16x16x32_bf16 v[58:61], v[138:141], v[186:189], v[58:61]
	v_mfma_f32_16x16x32_bf16 v[46:49], v[130:133], v[194:197], v[46:49]
	v_mfma_f32_16x16x32_bf16 v[42:45], v[138:141], v[194:197], v[42:45]
	v_mfma_f32_16x16x32_bf16 v[30:33], v[130:133], v[202:205], v[30:33]
	v_mfma_f32_16x16x32_bf16 v[26:29], v[138:141], v[202:205], v[26:29]
	v_mfma_f32_16x16x32_bf16 v[14:17], v[130:133], v[210:213], v[14:17]
	v_mfma_f32_16x16x32_bf16 v[10:13], v[138:141], v[210:213], v[10:13]
	v_mfma_f32_16x16x32_bf16 v[62:65], v[134:137], v[190:193], v[62:65]
	v_mfma_f32_16x16x32_bf16 v[58:61], v[142:145], v[190:193], v[58:61]
	v_mfma_f32_16x16x32_bf16 v[46:49], v[134:137], v[198:201], v[46:49]
	v_mfma_f32_16x16x32_bf16 v[42:45], v[142:145], v[198:201], v[42:45]
	v_mfma_f32_16x16x32_bf16 v[30:33], v[134:137], v[206:209], v[30:33]
	v_mfma_f32_16x16x32_bf16 v[26:29], v[142:145], v[206:209], v[26:29]
	v_mfma_f32_16x16x32_bf16 v[14:17], v[134:137], v[214:217], v[14:17]
	v_mfma_f32_16x16x32_bf16 v[10:13], v[142:145], v[214:217], v[10:13]
	s_setprio 0
	s_setprio 1
	v_mfma_f32_16x16x32_bf16 v[54:57], v[162:165], v[186:189], v[54:57]
	v_mfma_f32_16x16x32_bf16 v[50:53], v[178:181], v[186:189], v[50:53]
	v_mfma_f32_16x16x32_bf16 v[38:41], v[162:165], v[194:197], v[38:41]
	v_mfma_f32_16x16x32_bf16 v[34:37], v[178:181], v[194:197], v[34:37]
	v_mfma_f32_16x16x32_bf16 v[22:25], v[162:165], v[202:205], v[22:25]
	v_mfma_f32_16x16x32_bf16 v[18:21], v[178:181], v[202:205], v[18:21]
	v_mfma_f32_16x16x32_bf16 v[6:9], v[162:165], v[210:213], v[6:9]
	v_mfma_f32_16x16x32_bf16 v[2:5], v[178:181], v[210:213], v[2:5]
	v_mfma_f32_16x16x32_bf16 v[54:57], v[166:169], v[190:193], v[54:57]
	v_mfma_f32_16x16x32_bf16 v[50:53], v[182:185], v[190:193], v[50:53]
	v_mfma_f32_16x16x32_bf16 v[38:41], v[166:169], v[198:201], v[38:41]
	v_mfma_f32_16x16x32_bf16 v[34:37], v[182:185], v[198:201], v[34:37]
	v_mfma_f32_16x16x32_bf16 v[22:25], v[166:169], v[206:209], v[22:25]
	v_mfma_f32_16x16x32_bf16 v[18:21], v[182:185], v[206:209], v[18:21]
	v_mfma_f32_16x16x32_bf16 v[6:9], v[166:169], v[214:217], v[6:9]
	v_mfma_f32_16x16x32_bf16 v[2:5], v[182:185], v[214:217], v[2:5]
	s_setprio 0
	s_barrier
; #define PG8_STAGE(bufoff, gbase, voff) do { _Pragma("unroll") for (int _i = 0; _i < 2; ++_i) \
;         __builtin_amdgcn_global_load_lds((const unsigned*)((const char*)(gbase) + (voff)[_i]), (PG8_LAS unsigned*)(lds + (bufoff) + ldsw + _i * 8192), 16, 0, 0); } while (0)
; #define PG8_LDA(dst, b, h) do { if constexpr (DT != 1) { _Pragma("unroll") for (int m = 0; m < 4; ++m) _Pragma("unroll") for (int k = 0; k < 2; ++k) dst[m][k] = *(const PG8_LAS bf16x8*)(lds + PG8_SA(b, h) + aoff + m * 2048 + k * 1024); } \
;         else { _Pragma("unroll") for (int m = 0; m < 4; ++m) dst##8[m] = ld32(lds + PG8_SA(b, h) + aoff + m * 2048); } } while (0)
; #define PG8_LDB(dst, b, h) do { if constexpr (DT != 1) { _Pragma("unroll") for (int n = 0; n < 2; ++n) _Pragma("unroll") for (int k = 0; k < 2; ++k) dst[n][k] = *(const PG8_LAS bf16x8*)(lds + PG8_SB(b, h) + boff + n * 2048 + k * 1024); } \
;         else { _Pragma("unroll") for (int n = 0; n < 2; ++n) dst##8[n] = ld32(lds + PG8_SB(b, h) + boff + n * 2048); } } while (0)
; #define PG8_WAIT_V(n) asm volatile("s_waitcnt vmcnt(" #n ")" ::: "memory")
; #define PG8_WAIT_L(n) asm volatile("s_waitcnt lgkmcnt(" #n ")" ::: "memory")
; #define PG8_BAR __builtin_amdgcn_s_barrier()
; #define PG8_SCHED __builtin_amdgcn_sched_barrier(0)
;     ...
;             PG8_LDB(B0, 1, 0); PG8_LDB(B1, 1, 1); PG8_SCHED; PG8_LDA(At, 1, 0); PG8_STAGE(PG8_SA(0, 1), a2 + hstepA, voffA);
;             PG8_WAIT_V(8); PG8_WAIT_L(0); PG8_BAR; PG8_MMA(0, 0, At, B0); PG8_MMA(0, 1, At, B1); PG8_BAR; PG8_SCHED;
;             PG8_LDA(At, 1, 1); PG8_STAGE(PG8_SB(1, 0), b3, voffB); PG8_STAGE(PG8_SB(1, 1), b3 + hstepB, voffB); PG8_STAGE(PG8_SA(1, 0), a3, voffA);
;             PG8_WAIT_V(8); PG8_WAIT_L(0); PG8_BAR; PG8_MMA(1, 0, At, B0); PG8_MMA(1, 1, At, B1); PG8_BAR; PG8_SCHED;
	ds_read_b128 v[130:133], v176
	ds_read_b128 v[134:137], v176 offset:1024
	ds_read_b128 v[138:141], v176 offset:2048
	ds_read_b128 v[142:145], v176 offset:3072
	ds_read_b128 v[162:165], v177
	ds_read_b128 v[166:169], v177 offset:1024
	ds_read_b128 v[178:181], v177 offset:2048
	ds_read_b128 v[182:185], v177 offset:3072
	s_add_u32 s38, s38, 0x80000
	s_addc_u32 s39, s39, 0
	s_mov_b32 m0, s51
	ds_read_b128 v[186:189], v175 offset:32768
	ds_read_b128 v[190:193], v175 offset:33792
	ds_read_b128 v[194:197], v175 offset:34816
	ds_read_b128 v[198:201], v175 offset:35840
	ds_read_b128 v[202:205], v175 offset:36864
	ds_read_b128 v[206:209], v175 offset:37888
	ds_read_b128 v[210:213], v175 offset:38912
	ds_read_b128 v[214:217], v175 offset:39936
	global_load_lds_dwordx4 v146, s[38:39]
	s_mov_b32 m0, s52
	s_nop 0
	global_load_lds_dwordx4 v150, s[38:39]
	s_waitcnt vmcnt(8) lgkmcnt(0)
	s_barrier
	s_setprio 1
	v_mfma_f32_16x16x32_bf16 v[122:125], v[130:133], v[186:189], v[122:125]
	v_mfma_f32_16x16x32_bf16 v[126:129], v[138:141], v[186:189], v[126:129]
	v_mfma_f32_16x16x32_bf16 v[110:113], v[130:133], v[194:197], v[110:113]
	v_mfma_f32_16x16x32_bf16 v[106:109], v[138:141], v[194:197], v[106:109]
	v_mfma_f32_16x16x32_bf16 v[94:97], v[130:133], v[202:205], v[94:97]
	v_mfma_f32_16x16x32_bf16 v[90:93], v[138:141], v[202:205], v[90:93]
	v_mfma_f32_16x16x32_bf16 v[78:81], v[130:133], v[210:213], v[78:81]
	v_mfma_f32_16x16x32_bf16 v[74:77], v[138:141], v[210:213], v[74:77]
	v_mfma_f32_16x16x32_bf16 v[122:125], v[134:137], v[190:193], v[122:125]
	v_mfma_f32_16x16x32_bf16 v[126:129], v[142:145], v[190:193], v[126:129]
	v_mfma_f32_16x16x32_bf16 v[110:113], v[134:137], v[198:201], v[110:113]
	v_mfma_f32_16x16x32_bf16 v[106:109], v[142:145], v[198:201], v[106:109]
	v_mfma_f32_16x16x32_bf16 v[94:97], v[134:137], v[206:209], v[94:97]
	v_mfma_f32_16x16x32_bf16 v[90:93], v[142:145], v[206:209], v[90:93]
	v_mfma_f32_16x16x32_bf16 v[78:81], v[134:137], v[214:217], v[78:81]
	v_mfma_f32_16x16x32_bf16 v[74:77], v[142:145], v[214:217], v[74:77]
	s_setprio 0
	s_setprio 1
	v_mfma_f32_16x16x32_bf16 v[118:121], v[162:165], v[186:189], v[118:121]
	v_mfma_f32_16x16x32_bf16 v[114:117], v[178:181], v[186:189], v[114:117]
	v_mfma_f32_16x16x32_bf16 v[102:105], v[162:165], v[194:197], v[102:105]
	v_mfma_f32_16x16x32_bf16 v[98:101], v[178:181], v[194:197], v[98:101]
	v_mfma_f32_16x16x32_bf16 v[86:89], v[162:165], v[202:205], v[86:89]
	v_mfma_f32_16x16x32_bf16 v[82:85], v[178:181], v[202:205], v[82:85]
	v_mfma_f32_16x16x32_bf16 v[70:73], v[162:165], v[210:213], v[70:73]
	v_mfma_f32_16x16x32_bf16 v[66:69], v[178:181], v[210:213], v[66:69]
	v_mfma_f32_16x16x32_bf16 v[118:121], v[166:169], v[190:193], v[118:121]
	v_mfma_f32_16x16x32_bf16 v[114:117], v[182:185], v[190:193], v[114:117]
	v_mfma_f32_16x16x32_bf16 v[102:105], v[166:169], v[198:201], v[102:105]
	v_mfma_f32_16x16x32_bf16 v[98:101], v[182:185], v[198:201], v[98:101]
	v_mfma_f32_16x16x32_bf16 v[86:89], v[166:169], v[206:209], v[86:89]
	v_mfma_f32_16x16x32_bf16 v[82:85], v[182:185], v[206:209], v[82:85]
	v_mfma_f32_16x16x32_bf16 v[70:73], v[166:169], v[214:217], v[70:73]
	v_mfma_f32_16x16x32_bf16 v[66:69], v[182:185], v[214:217], v[66:69]
	s_setprio 0
	s_barrier
	s_mov_b32 m0, s55
	s_add_u32 s36, s36, 0x80080
	ds_read_b128 v[186:189], v175 offset:49152
	ds_read_b128 v[190:193], v175 offset:50176
	ds_read_b128 v[194:197], v175 offset:51200
	ds_read_b128 v[198:201], v175 offset:52224
	ds_read_b128 v[202:205], v175 offset:53248
	ds_read_b128 v[206:209], v175 offset:54272
	ds_read_b128 v[210:213], v175 offset:55296
	ds_read_b128 v[214:217], v175 offset:56320
	global_load_lds_dwordx4 v148, s[98:99]
	s_mov_b32 m0, s56
	s_addc_u32 s37, s37, 0
	global_load_lds_dwordx4 v152, s[98:99]
	s_mov_b32 m0, s59
	s_nop 0
	global_load_lds_dwordx4 v148, s[36:37]
	s_mov_b32 m0, s60
	s_nop 0
	global_load_lds_dwordx4 v152, s[36:37]
	s_mov_b32 m0, s57
	s_nop 0
	global_load_lds_dwordx4 v146, s[100:101]
	s_mov_b32 m0, s58
	s_nop 0
	global_load_lds_dwordx4 v150, s[100:101]
	s_waitcnt vmcnt(8) lgkmcnt(0)
	s_barrier
	s_setprio 1
	v_mfma_f32_16x16x32_bf16 v[62:65], v[130:133], v[186:189], v[62:65]
	v_mfma_f32_16x16x32_bf16 v[58:61], v[138:141], v[186:189], v[58:61]
	v_mfma_f32_16x16x32_bf16 v[46:49], v[130:133], v[194:197], v[46:49]
	v_mfma_f32_16x16x32_bf16 v[42:45], v[138:141], v[194:197], v[42:45]
	v_mfma_f32_16x16x32_bf16 v[30:33], v[130:133], v[202:205], v[30:33]
	v_mfma_f32_16x16x32_bf16 v[26:29], v[138:141], v[202:205], v[26:29]
	v_mfma_f32_16x16x32_bf16 v[14:17], v[130:133], v[210:213], v[14:17]
	v_mfma_f32_16x16x32_bf16 v[10:13], v[138:141], v[210:213], v[10:13]
	v_mfma_f32_16x16x32_bf16 v[62:65], v[134:137], v[190:193], v[62:65]
	v_mfma_f32_16x16x32_bf16 v[58:61], v[142:145], v[190:193], v[58:61]
	v_mfma_f32_16x16x32_bf16 v[46:49], v[134:137], v[198:201], v[46:49]
	v_mfma_f32_16x16x32_bf16 v[42:45], v[142:145], v[198:201], v[42:45]
	v_mfma_f32_16x16x32_bf16 v[30:33], v[134:137], v[206:209], v[30:33]
	v_mfma_f32_16x16x32_bf16 v[26:29], v[142:145], v[206:209], v[26:29]
	v_mfma_f32_16x16x32_bf16 v[14:17], v[134:137], v[214:217], v[14:17]
	v_mfma_f32_16x16x32_bf16 v[10:13], v[142:145], v[214:217], v[10:13]
	s_setprio 0
	s_setprio 1
	v_mfma_f32_16x16x32_bf16 v[54:57], v[162:165], v[186:189], v[54:57]
	v_mfma_f32_16x16x32_bf16 v[50:53], v[178:181], v[186:189], v[50:53]
	v_mfma_f32_16x16x32_bf16 v[38:41], v[162:165], v[194:197], v[38:41]
	v_mfma_f32_16x16x32_bf16 v[34:37], v[178:181], v[194:197], v[34:37]
	v_mfma_f32_16x16x32_bf16 v[22:25], v[162:165], v[202:205], v[22:25]
	v_mfma_f32_16x16x32_bf16 v[18:21], v[178:181], v[202:205], v[18:21]
	v_mfma_f32_16x16x32_bf16 v[6:9], v[162:165], v[210:213], v[6:9]
	v_mfma_f32_16x16x32_bf16 v[2:5], v[178:181], v[210:213], v[2:5]
	v_mfma_f32_16x16x32_bf16 v[54:57], v[166:169], v[190:193], v[54:57]
	v_mfma_f32_16x16x32_bf16 v[50:53], v[182:185], v[190:193], v[50:53]
	v_mfma_f32_16x16x32_bf16 v[38:41], v[166:169], v[198:201], v[38:41]
	v_mfma_f32_16x16x32_bf16 v[34:37], v[182:185], v[198:201], v[34:37]
	v_mfma_f32_16x16x32_bf16 v[22:25], v[166:169], v[206:209], v[22:25]
	v_mfma_f32_16x16x32_bf16 v[18:21], v[182:185], v[206:209], v[18:21]
	v_mfma_f32_16x16x32_bf16 v[6:9], v[166:169], v[214:217], v[6:9]
	v_mfma_f32_16x16x32_bf16 v[2:5], v[182:185], v[214:217], v[2:5]
	s_setprio 0
	s_barrier
	s_add_u32 s67, s67, 0x100
	s_addc_u32 s68, s68, 0
	s_add_u32 s34, s34, 0x100
	s_addc_u32 s35, s35, 0
	s_cmp_ge_i32 s69, s54
	s_mov_b32 s36, s69
	s_cbranch_scc0 .LBB0_713

; #define PG8_STAGE(bufoff, gbase, voff) do { _Pragma("unroll") for (int _i = 0; _i < 2; ++_i) \
;         __builtin_amdgcn_global_load_lds((const unsigned*)((const char*)(gbase) + (voff)[_i]), (PG8_LAS unsigned*)(lds + (bufoff) + ldsw + _i * 8192), 16, 0, 0); } while (0)
; #define PG8_LDA(dst, b, h) do { if constexpr (DT != 1) { _Pragma("unroll") for (int m = 0; m < 4; ++m) _Pragma("unroll") for (int k = 0; k < 2; ++k) dst[m][k] = *(const PG8_LAS bf16x8*)(lds + PG8_SA(b, h) + aoff + m * 2048 + k * 1024); } \
;         else { _Pragma("unroll") for (int m = 0; m < 4; ++m) dst##8[m] = ld32(lds + PG8_SA(b, h) + aoff + m * 2048); } } while (0)
; #define PG8_LDB(dst, b, h) do { if constexpr (DT != 1) { _Pragma("unroll") for (int n = 0; n < 2; ++n) _Pragma("unroll") for (int k = 0; k < 2; ++k) dst[n][k] = *(const PG8_LAS bf16x8*)(lds + PG8_SB(b, h) + boff + n * 2048 + k * 1024); } \
;         else { _Pragma("unroll") for (int n = 0; n < 2; ++n) dst##8[n] = ld32(lds + PG8_SB(b, h) + boff + n * 2048); } } while (0)
; #define PG8_WAIT_V(n) asm volatile("s_waitcnt vmcnt(" #n ")" ::: "memory")
; #define PG8_WAIT_L(n) asm volatile("s_waitcnt lgkmcnt(" #n ")" ::: "memory")
; #define PG8_BAR __builtin_amdgcn_s_barrier()
; #define PG8_SCHED __builtin_amdgcn_sched_barrier(0)
;     ...
;             PG8_LDB(B0, 0, 0); PG8_LDB(B1, 0, 1); PG8_SCHED; PG8_LDA(At, 0, 0); PG8_STAGE(PG8_SA(1, 1), a1 + hstepA, voffA);
;             PG8_WAIT_V(8); PG8_WAIT_L(0); PG8_BAR; PG8_MMA(0, 0, At, B0); PG8_MMA(0, 1, At, B1); PG8_BAR; PG8_SCHED;
;             PG8_LDA(At, 0, 1); PG8_STAGE(PG8_SB(0, 0), b2, voffB); PG8_STAGE(PG8_SB(0, 1), b2 + hstepB, voffB); PG8_STAGE(PG8_SA(0, 0), a2, voffA);
;             PG8_WAIT_V(8); PG8_WAIT_L(0); PG8_BAR; PG8_MMA(1, 0, At, B0); PG8_MMA(1, 1, At, B1); PG8_BAR; PG8_SCHED;
.LBB0_922:
	ds_read_b128 v[146:149], v173
	ds_read_b128 v[150:153], v173 offset:1024
	ds_read_b128 v[154:157], v173 offset:2048
	ds_read_b128 v[158:161], v173 offset:3072
	ds_read_b128 v[162:165], v174
	ds_read_b128 v[166:169], v174 offset:1024
	ds_read_b128 v[178:181], v174 offset:2048
	ds_read_b128 v[182:185], v174 offset:3072
	s_add_i32 s67, s30, 2
	s_add_u32 s28, s26, 0x100
	s_addc_u32 s29, s27, 0
	s_cmp_eq_u32 s58, s30
	s_cselect_b32 s30, s24, s65
	s_cselect_b32 s35, s3, s29
	s_cselect_b32 s34, s2, s28
	s_cselect_b32 s31, s25, s66
	v_lshl_add_u64 v[170:171], s[26:27], 0, v[140:141]
	s_add_i32 m0, s46, 0xc000
	ds_read_b128 v[186:189], v175
	ds_read_b128 v[190:193], v175 offset:1024
	ds_read_b128 v[194:197], v175 offset:2048
	ds_read_b128 v[198:201], v175 offset:3072
	ds_read_b128 v[202:205], v175 offset:4096
	ds_read_b128 v[206:209], v175 offset:5120
	ds_read_b128 v[210:213], v175 offset:6144
	ds_read_b128 v[214:217], v175 offset:7168
	global_load_lds_dwordx4 v[170:171], off
	v_lshl_add_u64 v[170:171], s[26:27], 0, v[138:139]
	s_add_i32 m0, s46, 0xe000
	s_nop 0
	global_load_lds_dwordx4 v[170:171], off
	s_waitcnt vmcnt(8) lgkmcnt(0)
	s_barrier
	s_setprio 1
	v_mfma_f32_16x16x32_bf16 v[126:129], v[146:149], v[186:189], v[126:129]
	v_mfma_f32_16x16x32_bf16 v[122:125], v[154:157], v[186:189], v[122:125]
	v_mfma_f32_16x16x32_bf16 v[118:121], v[146:149], v[194:197], v[118:121]
	v_mfma_f32_16x16x32_bf16 v[114:117], v[154:157], v[194:197], v[114:117]
	v_mfma_f32_16x16x32_bf16 v[106:109], v[146:149], v[202:205], v[106:109]
	v_mfma_f32_16x16x32_bf16 v[98:101], v[154:157], v[202:205], v[98:101]
	v_mfma_f32_16x16x32_bf16 v[90:93], v[146:149], v[210:213], v[90:93]
	v_mfma_f32_16x16x32_bf16 v[82:85], v[154:157], v[210:213], v[82:85]
	v_mfma_f32_16x16x32_bf16 v[126:129], v[150:153], v[190:193], v[126:129]
	v_mfma_f32_16x16x32_bf16 v[122:125], v[158:161], v[190:193], v[122:125]
	v_mfma_f32_16x16x32_bf16 v[118:121], v[150:153], v[198:201], v[118:121]
	v_mfma_f32_16x16x32_bf16 v[114:117], v[158:161], v[198:201], v[114:117]
	v_mfma_f32_16x16x32_bf16 v[106:109], v[150:153], v[206:209], v[106:109]
	v_mfma_f32_16x16x32_bf16 v[98:101], v[158:161], v[206:209], v[98:101]
	v_mfma_f32_16x16x32_bf16 v[90:93], v[150:153], v[214:217], v[90:93]
	v_mfma_f32_16x16x32_bf16 v[82:85], v[158:161], v[214:217], v[82:85]
	s_setprio 0
	s_setprio 1
	v_mfma_f32_16x16x32_bf16 v[110:113], v[162:165], v[186:189], v[110:113]
	v_mfma_f32_16x16x32_bf16 v[102:105], v[178:181], v[186:189], v[102:105]
	v_mfma_f32_16x16x32_bf16 v[94:97], v[162:165], v[194:197], v[94:97]
	v_mfma_f32_16x16x32_bf16 v[86:89], v[178:181], v[194:197], v[86:89]
	v_mfma_f32_16x16x32_bf16 v[78:81], v[162:165], v[202:205], v[78:81]
	v_mfma_f32_16x16x32_bf16 v[74:77], v[178:181], v[202:205], v[74:77]
	v_mfma_f32_16x16x32_bf16 v[70:73], v[162:165], v[210:213], v[70:73]
	v_mfma_f32_16x16x32_bf16 v[66:69], v[178:181], v[210:213], v[66:69]
	v_mfma_f32_16x16x32_bf16 v[110:113], v[166:169], v[190:193], v[110:113]
	v_mfma_f32_16x16x32_bf16 v[102:105], v[182:185], v[190:193], v[102:105]
	v_mfma_f32_16x16x32_bf16 v[94:97], v[166:169], v[198:201], v[94:97]
	v_mfma_f32_16x16x32_bf16 v[86:89], v[182:185], v[198:201], v[86:89]
	v_mfma_f32_16x16x32_bf16 v[78:81], v[166:169], v[206:209], v[78:81]
	v_mfma_f32_16x16x32_bf16 v[74:77], v[182:185], v[206:209], v[74:77]
	v_mfma_f32_16x16x32_bf16 v[70:73], v[166:169], v[214:217], v[70:73]
	v_mfma_f32_16x16x32_bf16 v[66:69], v[182:185], v[214:217], v[66:69]
	s_setprio 0
	s_barrier
	s_mov_b32 m0, s42
	s_add_u32 s98, s30, 0x80
	s_addc_u32 s99, s31, 0
	s_add_u32 s26, s30, 0x160000
	ds_read_b128 v[186:189], v175 offset:16384
	ds_read_b128 v[190:193], v175 offset:17408
	ds_read_b128 v[194:197], v175 offset:18432
	ds_read_b128 v[198:201], v175 offset:19456
	ds_read_b128 v[202:205], v175 offset:20480
	ds_read_b128 v[206:209], v175 offset:21504
	ds_read_b128 v[210:213], v175 offset:22528
	ds_read_b128 v[214:217], v175 offset:23552
	global_load_lds_dwordx4 v132, s[30:31]
	s_mov_b32 m0, s43
	s_addc_u32 s27, s31, 0
	global_load_lds_dwordx4 v136, s[30:31]
	s_mov_b32 m0, s44
	s_nop 0
	global_load_lds_dwordx4 v132, s[26:27]
	s_mov_b32 m0, s45
	s_nop 0
	global_load_lds_dwordx4 v136, s[26:27]
	s_add_u32 s100, s34, 0x80
	s_addc_u32 s101, s35, 0
	s_mov_b32 m0, s46
	s_nop 0
	global_load_lds_dwordx4 v130, s[34:35]
	s_mov_b32 m0, s47
	s_nop 0
	global_load_lds_dwordx4 v134, s[34:35]
	s_waitcnt vmcnt(8) lgkmcnt(0)
	s_barrier
	s_setprio 1
	v_mfma_f32_16x16x32_bf16 v[62:65], v[146:149], v[186:189], v[62:65]
	v_mfma_f32_16x16x32_bf16 v[58:61], v[154:157], v[186:189], v[58:61]
	v_mfma_f32_16x16x32_bf16 v[54:57], v[146:149], v[194:197], v[54:57]
	v_mfma_f32_16x16x32_bf16 v[50:53], v[154:157], v[194:197], v[50:53]
	v_mfma_f32_16x16x32_bf16 v[42:45], v[146:149], v[202:205], v[42:45]
	v_mfma_f32_16x16x32_bf16 v[34:37], v[154:157], v[202:205], v[34:37]
	v_mfma_f32_16x16x32_bf16 v[26:29], v[146:149], v[210:213], v[26:29]
	v_mfma_f32_16x16x32_bf16 v[18:21], v[154:157], v[210:213], v[18:21]
	v_mfma_f32_16x16x32_bf16 v[62:65], v[150:153], v[190:193], v[62:65]
	v_mfma_f32_16x16x32_bf16 v[58:61], v[158:161], v[190:193], v[58:61]
	v_mfma_f32_16x16x32_bf16 v[54:57], v[150:153], v[198:201], v[54:57]
	v_mfma_f32_16x16x32_bf16 v[50:53], v[158:161], v[198:201], v[50:53]
	v_mfma_f32_16x16x32_bf16 v[42:45], v[150:153], v[206:209], v[42:45]
	v_mfma_f32_16x16x32_bf16 v[34:37], v[158:161], v[206:209], v[34:37]
	v_mfma_f32_16x16x32_bf16 v[26:29], v[150:153], v[214:217], v[26:29]
	v_mfma_f32_16x16x32_bf16 v[18:21], v[158:161], v[214:217], v[18:21]
	s_setprio 0
	s_setprio 1
	v_mfma_f32_16x16x32_bf16 v[46:49], v[162:165], v[186:189], v[46:49]
	v_mfma_f32_16x16x32_bf16 v[38:41], v[178:181], v[186:189], v[38:41]
	v_mfma_f32_16x16x32_bf16 v[30:33], v[162:165], v[194:197], v[30:33]
	v_mfma_f32_16x16x32_bf16 v[22:25], v[178:181], v[194:197], v[22:25]
	v_mfma_f32_16x16x32_bf16 v[14:17], v[162:165], v[202:205], v[14:17]
	v_mfma_f32_16x16x32_bf16 v[10:13], v[178:181], v[202:205], v[10:13]
	v_mfma_f32_16x16x32_bf16 v[6:9], v[162:165], v[210:213], v[6:9]
	v_mfma_f32_16x16x32_bf16 v[2:5], v[178:181], v[210:213], v[2:5]
	v_mfma_f32_16x16x32_bf16 v[46:49], v[166:169], v[190:193], v[46:49]
	v_mfma_f32_16x16x32_bf16 v[38:41], v[182:185], v[190:193], v[38:41]
	v_mfma_f32_16x16x32_bf16 v[30:33], v[166:169], v[198:201], v[30:33]
	v_mfma_f32_16x16x32_bf16 v[22:25], v[182:185], v[198:201], v[22:25]
	v_mfma_f32_16x16x32_bf16 v[14:17], v[166:169], v[206:209], v[14:17]
	v_mfma_f32_16x16x32_bf16 v[10:13], v[182:185], v[206:209], v[10:13]
	v_mfma_f32_16x16x32_bf16 v[6:9], v[166:169], v[214:217], v[6:9]
	v_mfma_f32_16x16x32_bf16 v[2:5], v[182:185], v[214:217], v[2:5]
	s_setprio 0
	s_barrier
; #define PG8_STAGE(bufoff, gbase, voff) do { _Pragma("unroll") for (int _i = 0; _i < 2; ++_i) \
;         __builtin_amdgcn_global_load_lds((const unsigned*)((const char*)(gbase) + (voff)[_i]), (PG8_LAS unsigned*)(lds + (bufoff) + ldsw + _i * 8192), 16, 0, 0); } while (0)
; #define PG8_LDA(dst, b, h) do { if constexpr (DT != 1) { _Pragma("unroll") for (int m = 0; m < 4; ++m) _Pragma("unroll") for (int k = 0; k < 2; ++k) dst[m][k] = *(const PG8_LAS bf16x8*)(lds + PG8_SA(b, h) + aoff + m * 2048 + k * 1024); } \
;         else { _Pragma("unroll") for (int m = 0; m < 4; ++m) dst##8[m] = ld32(lds + PG8_SA(b, h) + aoff + m * 2048); } } while (0)
; #define PG8_LDB(dst, b, h) do { if constexpr (DT != 1) { _Pragma("unroll") for (int n = 0; n < 2; ++n) _Pragma("unroll") for (int k = 0; k < 2; ++k) dst[n][k] = *(const PG8_LAS bf16x8*)(lds + PG8_SB(b, h) + boff + n * 2048 + k * 1024); } \
;         else { _Pragma("unroll") for (int n = 0; n < 2; ++n) dst##8[n] = ld32(lds + PG8_SB(b, h) + boff + n * 2048); } } while (0)
; #define PG8_WAIT_V(n) asm volatile("s_waitcnt vmcnt(" #n ")" ::: "memory")
; #define PG8_WAIT_L(n) asm volatile("s_waitcnt lgkmcnt(" #n ")" ::: "memory")
; #define PG8_BAR __builtin_amdgcn_s_barrier()
; #define PG8_SCHED __builtin_amdgcn_sched_barrier(0)
;     ...
;             PG8_LDB(B0, 1, 0); PG8_LDB(B1, 1, 1); PG8_SCHED; PG8_LDA(At, 1, 0); PG8_STAGE(PG8_SA(0, 1), a2 + hstepA, voffA);
;             PG8_WAIT_V(8); PG8_WAIT_L(0); PG8_BAR; PG8_MMA(0, 0, At, B0); PG8_MMA(0, 1, At, B1); PG8_BAR; PG8_SCHED;
;             PG8_LDA(At, 1, 1); PG8_STAGE(PG8_SB(1, 0), b3, voffB); PG8_STAGE(PG8_SB(1, 1), b3 + hstepB, voffB); PG8_STAGE(PG8_SA(1, 0), a3, voffA);
;             PG8_WAIT_V(8); PG8_WAIT_L(0); PG8_BAR; PG8_MMA(1, 0, At, B0); PG8_MMA(1, 1, At, B1); PG8_BAR; PG8_SCHED;
	ds_read_b128 v[146:149], v176
	ds_read_b128 v[150:153], v176 offset:1024
	ds_read_b128 v[154:157], v176 offset:2048
	ds_read_b128 v[158:161], v176 offset:3072
	ds_read_b128 v[162:165], v177
	ds_read_b128 v[166:169], v177 offset:1024
	ds_read_b128 v[178:181], v177 offset:2048
	ds_read_b128 v[182:185], v177 offset:3072
	s_add_u32 s26, s34, 0x160000
	s_addc_u32 s27, s35, 0
	s_mov_b32 m0, s48
	ds_read_b128 v[186:189], v175 offset:32768
	ds_read_b128 v[190:193], v175 offset:33792
	ds_read_b128 v[194:197], v175 offset:34816
	ds_read_b128 v[198:201], v175 offset:35840
	ds_read_b128 v[202:205], v175 offset:36864
	ds_read_b128 v[206:209], v175 offset:37888
	ds_read_b128 v[210:213], v175 offset:38912
	ds_read_b128 v[214:217], v175 offset:39936
	global_load_lds_dwordx4 v130, s[26:27]
	s_mov_b32 m0, s49
	s_nop 0
	global_load_lds_dwordx4 v134, s[26:27]
	s_waitcnt vmcnt(8) lgkmcnt(0)
	s_barrier
	s_setprio 1
	v_mfma_f32_16x16x32_bf16 v[126:129], v[146:149], v[186:189], v[126:129]
	v_mfma_f32_16x16x32_bf16 v[122:125], v[154:157], v[186:189], v[122:125]
	v_mfma_f32_16x16x32_bf16 v[118:121], v[146:149], v[194:197], v[118:121]
	v_mfma_f32_16x16x32_bf16 v[114:117], v[154:157], v[194:197], v[114:117]
	v_mfma_f32_16x16x32_bf16 v[106:109], v[146:149], v[202:205], v[106:109]
	v_mfma_f32_16x16x32_bf16 v[98:101], v[154:157], v[202:205], v[98:101]
	v_mfma_f32_16x16x32_bf16 v[90:93], v[146:149], v[210:213], v[90:93]
	v_mfma_f32_16x16x32_bf16 v[82:85], v[154:157], v[210:213], v[82:85]
	v_mfma_f32_16x16x32_bf16 v[126:129], v[150:153], v[190:193], v[126:129]
	v_mfma_f32_16x16x32_bf16 v[122:125], v[158:161], v[190:193], v[122:125]
	v_mfma_f32_16x16x32_bf16 v[118:121], v[150:153], v[198:201], v[118:121]
	v_mfma_f32_16x16x32_bf16 v[114:117], v[158:161], v[198:201], v[114:117]
	v_mfma_f32_16x16x32_bf16 v[106:109], v[150:153], v[206:209], v[106:109]
	v_mfma_f32_16x16x32_bf16 v[98:101], v[158:161], v[206:209], v[98:101]
	v_mfma_f32_16x16x32_bf16 v[90:93], v[150:153], v[214:217], v[90:93]
	v_mfma_f32_16x16x32_bf16 v[82:85], v[158:161], v[214:217], v[82:85]
	s_setprio 0
	s_setprio 1
	v_mfma_f32_16x16x32_bf16 v[110:113], v[162:165], v[186:189], v[110:113]
	v_mfma_f32_16x16x32_bf16 v[102:105], v[178:181], v[186:189], v[102:105]
	v_mfma_f32_16x16x32_bf16 v[94:97], v[162:165], v[194:197], v[94:97]
	v_mfma_f32_16x16x32_bf16 v[86:89], v[178:181], v[194:197], v[86:89]
	v_mfma_f32_16x16x32_bf16 v[78:81], v[162:165], v[202:205], v[78:81]
	v_mfma_f32_16x16x32_bf16 v[74:77], v[178:181], v[202:205], v[74:77]
	v_mfma_f32_16x16x32_bf16 v[70:73], v[162:165], v[210:213], v[70:73]
	v_mfma_f32_16x16x32_bf16 v[66:69], v[178:181], v[210:213], v[66:69]
	v_mfma_f32_16x16x32_bf16 v[110:113], v[166:169], v[190:193], v[110:113]
	v_mfma_f32_16x16x32_bf16 v[102:105], v[182:185], v[190:193], v[102:105]
	v_mfma_f32_16x16x32_bf16 v[94:97], v[166:169], v[198:201], v[94:97]
	v_mfma_f32_16x16x32_bf16 v[86:89], v[182:185], v[198:201], v[86:89]
	v_mfma_f32_16x16x32_bf16 v[78:81], v[166:169], v[206:209], v[78:81]
	v_mfma_f32_16x16x32_bf16 v[74:77], v[182:185], v[206:209], v[74:77]
	v_mfma_f32_16x16x32_bf16 v[70:73], v[166:169], v[214:217], v[70:73]
	v_mfma_f32_16x16x32_bf16 v[66:69], v[182:185], v[214:217], v[66:69]
	s_setprio 0
	s_barrier
	s_mov_b32 m0, s52
	s_add_u32 s26, s30, 0x160080
	ds_read_b128 v[186:189], v175 offset:49152
	ds_read_b128 v[190:193], v175 offset:50176
	ds_read_b128 v[194:197], v175 offset:51200
	ds_read_b128 v[198:201], v175 offset:52224
	ds_read_b128 v[202:205], v175 offset:53248
	ds_read_b128 v[206:209], v175 offset:54272
	ds_read_b128 v[210:213], v175 offset:55296
	ds_read_b128 v[214:217], v175 offset:56320
	global_load_lds_dwordx4 v132, s[98:99]
	s_mov_b32 m0, s53
	s_addc_u32 s27, s31, 0
	global_load_lds_dwordx4 v136, s[98:99]
	s_mov_b32 m0, s56
	s_nop 0
	global_load_lds_dwordx4 v132, s[26:27]
	s_mov_b32 m0, s57
	s_nop 0
	global_load_lds_dwordx4 v136, s[26:27]
	s_mov_b32 m0, s54
	s_nop 0
	global_load_lds_dwordx4 v130, s[100:101]
	s_mov_b32 m0, s55
	s_nop 0
	global_load_lds_dwordx4 v134, s[100:101]
	s_waitcnt vmcnt(8) lgkmcnt(0)
	s_barrier
; #define PG8_WAIT_V(n) asm volatile("s_waitcnt vmcnt(" #n ")" ::: "memory")
; #define PG8_WAIT_L(n) asm volatile("s_waitcnt lgkmcnt(" #n ")" ::: "memory")
; #define PG8_BAR __builtin_amdgcn_s_barrier()
; #define PG8_SCHED __builtin_amdgcn_sched_barrier(0)
;     __device__ __forceinline__ void operator()(const f32x4 (&acc)[2][2][4][2], const Unit& u, int wr, int wc, int fr, int fq) const {
;     ...
;                     for (int bj = 0; bj < 2; ++bj) { const h16x8_t w = wv[m][bj];
;                         const f32x4 b0 = (f32x4){(float)w[0], (float)w[1], (float)w[2], (float)w[3]}, b1 = (f32x4){(float)w[4], (float)w[5], (float)w[6], (float)w[7]};
;                         const f32x4 o0 = b0 + acc[ai][bj][m][0] * s, o1 = b1 + acc[ai][bj][m][1] * s;
;     ...
;             PG8_WAIT_V(8); PG8_WAIT_L(0); PG8_BAR; PG8_MMA(1, 0, At, B0); PG8_MMA(1, 1, At, B1); PG8_BAR; PG8_SCHED;
	s_setprio 1
	v_mfma_f32_16x16x32_bf16 v[62:65], v[146:149], v[186:189], v[62:65]
	v_mfma_f32_16x16x32_bf16 v[58:61], v[154:157], v[186:189], v[58:61]
	v_mfma_f32_16x16x32_bf16 v[54:57], v[146:149], v[194:197], v[54:57]
	v_mfma_f32_16x16x32_bf16 v[50:53], v[154:157], v[194:197], v[50:53]
	v_mfma_f32_16x16x32_bf16 v[42:45], v[146:149], v[202:205], v[42:45]
	v_mfma_f32_16x16x32_bf16 v[34:37], v[154:157], v[202:205], v[34:37]
	v_mfma_f32_16x16x32_bf16 v[26:29], v[146:149], v[210:213], v[26:29]
	v_mfma_f32_16x16x32_bf16 v[18:21], v[154:157], v[210:213], v[18:21]
	v_mfma_f32_16x16x32_bf16 v[62:65], v[150:153], v[190:193], v[62:65]
	v_mfma_f32_16x16x32_bf16 v[58:61], v[158:161], v[190:193], v[58:61]
	v_mfma_f32_16x16x32_bf16 v[54:57], v[150:153], v[198:201], v[54:57]
	v_mfma_f32_16x16x32_bf16 v[50:53], v[158:161], v[198:201], v[50:53]
	v_mfma_f32_16x16x32_bf16 v[42:45], v[150:153], v[206:209], v[42:45]
	v_mfma_f32_16x16x32_bf16 v[34:37], v[158:161], v[206:209], v[34:37]
	v_mfma_f32_16x16x32_bf16 v[26:29], v[150:153], v[214:217], v[26:29]
	v_mfma_f32_16x16x32_bf16 v[18:21], v[158:161], v[214:217], v[18:21]
	s_setprio 0
	s_setprio 1
	v_mfma_f32_16x16x32_bf16 v[46:49], v[162:165], v[186:189], v[46:49]
	v_mfma_f32_16x16x32_bf16 v[38:41], v[178:181], v[186:189], v[38:41]
	v_mfma_f32_16x16x32_bf16 v[30:33], v[162:165], v[194:197], v[30:33]
	v_mfma_f32_16x16x32_bf16 v[22:25], v[178:181], v[194:197], v[22:25]
	v_mfma_f32_16x16x32_bf16 v[14:17], v[162:165], v[202:205], v[14:17]
	v_mfma_f32_16x16x32_bf16 v[10:13], v[178:181], v[202:205], v[10:13]
	v_mfma_f32_16x16x32_bf16 v[6:9], v[162:165], v[210:213], v[6:9]
	v_mfma_f32_16x16x32_bf16 v[2:5], v[178:181], v[210:213], v[2:5]
	v_mfma_f32_16x16x32_bf16 v[46:49], v[166:169], v[190:193], v[46:49]
	v_mfma_f32_16x16x32_bf16 v[38:41], v[182:185], v[190:193], v[38:41]
	v_mfma_f32_16x16x32_bf16 v[30:33], v[166:169], v[198:201], v[30:33]
	v_mfma_f32_16x16x32_bf16 v[22:25], v[182:185], v[198:201], v[22:25]
	v_mfma_f32_16x16x32_bf16 v[14:17], v[166:169], v[206:209], v[14:17]
	v_mfma_f32_16x16x32_bf16 v[10:13], v[182:185], v[206:209], v[10:13]
	v_mfma_f32_16x16x32_bf16 v[6:9], v[166:169], v[214:217], v[6:9]
	v_mfma_f32_16x16x32_bf16 v[2:5], v[182:185], v[214:217], v[2:5]
	s_setprio 0
	s_barrier
	s_add_u32 s65, s65, 0x100
	s_addc_u32 s66, s66, 0
	s_cmp_ge_i32 s67, s51
	s_mov_b64 s[26:27], s[28:29]
	s_mov_b32 s30, s67
	s_cbranch_scc0 .LBB0_922
	v_pk_mul_f32 v[128:129], v[128:129], 0.5 op_sel_hi:[1,0]
	v_pk_mul_f32 v[126:127], v[126:127], 0.5 op_sel_hi:[1,0]
	v_pk_mul_f32 v[124:125], v[124:125], 0.5 op_sel_hi:[1,0]
	v_pk_mul_f32 v[122:123], v[122:123], 0.5 op_sel_hi:[1,0]
	v_pk_mul_f32 v[152:153], v[112:113], 0.5 op_sel_hi:[1,0]
	v_pk_mul_f32 v[154:155], v[110:111], 0.5 op_sel_hi:[1,0]
	v_pk_mul_f32 v[156:157], v[104:105], 0.5 op_sel_hi:[1,0]
	v_pk_mul_f32 v[158:159], v[102:103], 0.5 op_sel_hi:[1,0]
	v_pk_mul_f32 v[120:121], v[120:121], 0.5 op_sel_hi:[1,0]
	v_pk_mul_f32 v[118:119], v[118:119], 0.5 op_sel_hi:[1,0]
	v_pk_mul_f32 v[116:117], v[116:117], 0.5 op_sel_hi:[1,0]
	v_pk_mul_f32 v[114:115], v[114:115], 0.5 op_sel_hi:[1,0]
	v_pk_mul_f32 v[160:161], v[96:97], 0.5 op_sel_hi:[1,0]
	v_pk_mul_f32 v[146:147], v[94:95], 0.5 op_sel_hi:[1,0]
	v_pk_mul_f32 v[150:151], v[88:89], 0.5 op_sel_hi:[1,0]
	v_pk_mul_f32 v[148:149], v[86:87], 0.5 op_sel_hi:[1,0]
	v_pk_mul_f32 v[94:95], v[108:109], 0.5 op_sel_hi:[1,0]
	v_pk_mul_f32 v[96:97], v[106:107], 0.5 op_sel_hi:[1,0]
	v_pk_mul_f32 v[100:101], v[100:101], 0.5 op_sel_hi:[1,0]
	v_pk_mul_f32 v[98:99], v[98:99], 0.5 op_sel_hi:[1,0]
	v_pk_mul_f32 v[106:107], v[80:81], 0.5 op_sel_hi:[1,0]
	v_pk_mul_f32 v[108:109], v[78:79], 0.5 op_sel_hi:[1,0]
	v_pk_mul_f32 v[110:111], v[76:77], 0.5 op_sel_hi:[1,0]
	v_pk_mul_f32 v[112:113], v[74:75], 0.5 op_sel_hi:[1,0]
	v_pk_mul_f32 v[74:75], v[92:93], 0.5 op_sel_hi:[1,0]
	v_pk_mul_f32 v[86:87], v[90:91], 0.5 op_sel_hi:[1,0]
	v_pk_mul_f32 v[84:85], v[84:85], 0.5 op_sel_hi:[1,0]
	v_pk_mul_f32 v[88:89], v[82:83], 0.5 op_sel_hi:[1,0]
	v_pk_mul_f32 v[90:91], v[72:73], 0.5 op_sel_hi:[1,0]
	v_pk_mul_f32 v[92:93], v[70:71], 0.5 op_sel_hi:[1,0]
	v_pk_mul_f32 v[102:103], v[68:69], 0.5 op_sel_hi:[1,0]
	v_pk_mul_f32 v[104:105], v[66:67], 0.5 op_sel_hi:[1,0]
	v_pk_mul_f32 v[72:73], v[64:65], 0.5 op_sel_hi:[1,0]
	v_pk_mul_f32 v[70:71], v[62:63], 0.5 op_sel_hi:[1,0]
	v_pk_mul_f32 v[82:83], v[60:61], 0.5 op_sel_hi:[1,0]
	v_pk_mul_f32 v[80:81], v[58:59], 0.5 op_sel_hi:[1,0]
	v_pk_mul_f32 v[68:69], v[48:49], 0.5 op_sel_hi:[1,0]
	v_pk_mul_f32 v[66:67], v[46:47], 0.5 op_sel_hi:[1,0]
	v_pk_mul_f32 v[78:79], v[40:41], 0.5 op_sel_hi:[1,0]
	v_pk_mul_f32 v[76:77], v[38:39], 0.5 op_sel_hi:[1,0]
	v_pk_mul_f32 v[56:57], v[56:57], 0.5 op_sel_hi:[1,0]
	v_pk_mul_f32 v[54:55], v[54:55], 0.5 op_sel_hi:[1,0]
	v_pk_mul_f32 v[64:65], v[52:53], 0.5 op_sel_hi:[1,0]
	v_pk_mul_f32 v[62:63], v[50:51], 0.5 op_sel_hi:[1,0]
	v_pk_mul_f32 v[52:53], v[32:33], 0.5 op_sel_hi:[1,0]
	v_pk_mul_f32 v[50:51], v[30:31], 0.5 op_sel_hi:[1,0]
	v_pk_mul_f32 v[60:61], v[24:25], 0.5 op_sel_hi:[1,0]
	v_pk_mul_f32 v[58:59], v[22:23], 0.5 op_sel_hi:[1,0]
	v_pk_mul_f32 v[40:41], v[44:45], 0.5 op_sel_hi:[1,0]
	v_pk_mul_f32 v[38:39], v[42:43], 0.5 op_sel_hi:[1,0]
	v_pk_mul_f32 v[48:49], v[36:37], 0.5 op_sel_hi:[1,0]
	v_pk_mul_f32 v[46:47], v[34:35], 0.5 op_sel_hi:[1,0]
	v_pk_mul_f32 v[36:37], v[16:17], 0.5 op_sel_hi:[1,0]
	v_pk_mul_f32 v[34:35], v[14:15], 0.5 op_sel_hi:[1,0]
	v_pk_mul_f32 v[44:45], v[12:13], 0.5 op_sel_hi:[1,0]
	v_pk_mul_f32 v[42:43], v[10:11], 0.5 op_sel_hi:[1,0]
	v_pk_mul_f32 v[24:25], v[28:29], 0.5 op_sel_hi:[1,0]
	v_pk_mul_f32 v[22:23], v[26:27], 0.5 op_sel_hi:[1,0]
	v_pk_mul_f32 v[32:33], v[20:21], 0.5 op_sel_hi:[1,0]
	v_pk_mul_f32 v[30:31], v[18:19], 0.5 op_sel_hi:[1,0]
	v_pk_mul_f32 v[20:21], v[8:9], 0.5 op_sel_hi:[1,0]
	v_pk_mul_f32 v[18:19], v[6:7], 0.5 op_sel_hi:[1,0]
	v_pk_mul_f32 v[28:29], v[4:5], 0.5 op_sel_hi:[1,0]
	v_pk_mul_f32 v[26:27], v[2:3], 0.5 op_sel_hi:[1,0]

; #define PG8_STAGE(bufoff, gbase, voff) do { _Pragma("unroll") for (int _i = 0; _i < 2; ++_i) \
;         __builtin_amdgcn_global_load_lds((const unsigned*)((const char*)(gbase) + (voff)[_i]), (PG8_LAS unsigned*)(lds + (bufoff) + ldsw + _i * 8192), 16, 0, 0); } while (0)
; #define PG8_LDA(dst, b, h) do { if constexpr (DT != 1) { _Pragma("unroll") for (int m = 0; m < 4; ++m) _Pragma("unroll") for (int k = 0; k < 2; ++k) dst[m][k] = *(const PG8_LAS bf16x8*)(lds + PG8_SA(b, h) + aoff + m * 2048 + k * 1024); } \
;         else { _Pragma("unroll") for (int m = 0; m < 4; ++m) dst##8[m] = ld32(lds + PG8_SA(b, h) + aoff + m * 2048); } } while (0)
; #define PG8_LDB(dst, b, h) do { if constexpr (DT != 1) { _Pragma("unroll") for (int n = 0; n < 2; ++n) _Pragma("unroll") for (int k = 0; k < 2; ++k) dst[n][k] = *(const PG8_LAS bf16x8*)(lds + PG8_SB(b, h) + boff + n * 2048 + k * 1024); } \
;         else { _Pragma("unroll") for (int n = 0; n < 2; ++n) dst##8[n] = ld32(lds + PG8_SB(b, h) + boff + n * 2048); } } while (0)
; #define PG8_WAIT_V(n) asm volatile("s_waitcnt vmcnt(" #n ")" ::: "memory")
; #define PG8_WAIT_L(n) asm volatile("s_waitcnt lgkmcnt(" #n ")" ::: "memory")
; #define PG8_BAR __builtin_amdgcn_s_barrier()
; #define PG8_SCHED __builtin_amdgcn_sched_barrier(0)
;     ...
;             PG8_LDB(B0, 0, 0); PG8_LDB(B1, 0, 1); PG8_SCHED; PG8_LDA(At, 0, 0); PG8_STAGE(PG8_SA(1, 1), a1 + hstepA, voffA);
;             PG8_WAIT_V(8); PG8_WAIT_L(0); PG8_BAR; PG8_MMA(0, 0, At, B0); PG8_MMA(0, 1, At, B1); PG8_BAR; PG8_SCHED;
;             PG8_LDA(At, 0, 1); PG8_STAGE(PG8_SB(0, 0), b2, voffB); PG8_STAGE(PG8_SB(0, 1), b2 + hstepB, voffB); PG8_STAGE(PG8_SA(0, 0), a2, voffA);
;             PG8_WAIT_V(8); PG8_WAIT_L(0); PG8_BAR; PG8_MMA(1, 0, At, B0); PG8_MMA(1, 1, At, B1); PG8_BAR; PG8_SCHED;
.LBB0_1412:
	v_add_u32_e32 v162, s35, v168
	v_add_u32_e32 v166, s36, v168
	ds_read_b128 v[150:153], v162
	ds_read_b128 v[154:157], v162 offset:1024
	ds_read_b128 v[158:161], v162 offset:2048
	ds_read_b128 v[162:165], v162 offset:3072
	ds_read_b128 v[178:181], v166
	ds_read_b128 v[182:185], v166 offset:1024
	ds_read_b128 v[186:189], v166 offset:2048
	ds_read_b128 v[190:193], v166 offset:3072
	s_add_i32 s68, s26, 2
	s_add_u32 s27, s24, 0xfffc0080
	s_addc_u32 s28, s25, -1
	s_cmp_eq_u32 s61, s26
	s_cselect_b32 s26, s65, s66
	s_cselect_b32 s29, s15, s28
	s_cselect_b32 s28, s17, s27
	s_cselect_b32 s27, s64, s67
	s_add_i32 m0, s46, 0xc000
	ds_read_b128 v[194:197], v177
	ds_read_b128 v[198:201], v177 offset:1024
	ds_read_b128 v[202:205], v177 offset:2048
	ds_read_b128 v[206:209], v177 offset:3072
	ds_read_b128 v[210:213], v177 offset:4096
	ds_read_b128 v[214:217], v177 offset:5120
	ds_read_b128 v[218:221], v177 offset:6144
	ds_read_b128 v[222:225], v177 offset:7168
	global_load_lds_dwordx4 v144, s[24:25]
	s_add_i32 m0, s46, 0xe000
	s_nop 0
	global_load_lds_dwordx4 v142, s[24:25]
	s_waitcnt vmcnt(8) lgkmcnt(0)
	s_barrier
	s_setprio 1
	v_mfma_i32_16x16x64_i8 v[126:129], v[150:153], v[194:197], v[126:129]
	v_mfma_i32_16x16x64_i8 v[122:125], v[158:161], v[194:197], v[122:125]
	v_mfma_i32_16x16x64_i8 v[118:121], v[150:153], v[202:205], v[118:121]
	v_mfma_i32_16x16x64_i8 v[114:117], v[158:161], v[202:205], v[114:117]
	v_mfma_i32_16x16x64_i8 v[106:109], v[150:153], v[210:213], v[106:109]
	v_mfma_i32_16x16x64_i8 v[98:101], v[158:161], v[210:213], v[98:101]
	v_mfma_i32_16x16x64_i8 v[90:93], v[150:153], v[218:221], v[90:93]
	v_mfma_i32_16x16x64_i8 v[82:85], v[158:161], v[218:221], v[82:85]
	v_mfma_i32_16x16x64_i8 v[126:129], v[154:157], v[198:201], v[126:129]
	v_mfma_i32_16x16x64_i8 v[122:125], v[162:165], v[198:201], v[122:125]
	v_mfma_i32_16x16x64_i8 v[118:121], v[154:157], v[206:209], v[118:121]
	v_mfma_i32_16x16x64_i8 v[114:117], v[162:165], v[206:209], v[114:117]
	v_mfma_i32_16x16x64_i8 v[106:109], v[154:157], v[214:217], v[106:109]
	v_mfma_i32_16x16x64_i8 v[98:101], v[162:165], v[214:217], v[98:101]
	v_mfma_i32_16x16x64_i8 v[90:93], v[154:157], v[222:225], v[90:93]
	v_mfma_i32_16x16x64_i8 v[82:85], v[162:165], v[222:225], v[82:85]
	s_setprio 0
	s_setprio 1
	v_mfma_i32_16x16x64_i8 v[110:113], v[178:181], v[194:197], v[110:113]
	v_mfma_i32_16x16x64_i8 v[102:105], v[186:189], v[194:197], v[102:105]
	v_mfma_i32_16x16x64_i8 v[94:97], v[178:181], v[202:205], v[94:97]
	v_mfma_i32_16x16x64_i8 v[86:89], v[186:189], v[202:205], v[86:89]
	v_mfma_i32_16x16x64_i8 v[78:81], v[178:181], v[210:213], v[78:81]
	v_mfma_i32_16x16x64_i8 v[74:77], v[186:189], v[210:213], v[74:77]
	v_mfma_i32_16x16x64_i8 v[70:73], v[178:181], v[218:221], v[70:73]
	v_mfma_i32_16x16x64_i8 v[66:69], v[186:189], v[218:221], v[66:69]
	v_mfma_i32_16x16x64_i8 v[110:113], v[182:185], v[198:201], v[110:113]
	v_mfma_i32_16x16x64_i8 v[102:105], v[190:193], v[198:201], v[102:105]
	v_mfma_i32_16x16x64_i8 v[94:97], v[182:185], v[206:209], v[94:97]
	v_mfma_i32_16x16x64_i8 v[86:89], v[190:193], v[206:209], v[86:89]
	v_mfma_i32_16x16x64_i8 v[78:81], v[182:185], v[214:217], v[78:81]
	v_mfma_i32_16x16x64_i8 v[74:77], v[190:193], v[214:217], v[74:77]
	v_mfma_i32_16x16x64_i8 v[70:73], v[182:185], v[222:225], v[70:73]
	v_mfma_i32_16x16x64_i8 v[66:69], v[190:193], v[222:225], v[66:69]
	s_setprio 0
	s_barrier
	s_mov_b32 m0, s23
	s_add_u32 s98, s26, 0x80
	s_addc_u32 s99, s27, 0
	s_add_u32 s70, s26, 0x40000
	ds_read_b128 v[194:197], v177 offset:16384
	ds_read_b128 v[198:201], v177 offset:17408
	ds_read_b128 v[202:205], v177 offset:18432
	ds_read_b128 v[206:209], v177 offset:19456
	ds_read_b128 v[210:213], v177 offset:20480
	ds_read_b128 v[214:217], v177 offset:21504
	ds_read_b128 v[218:221], v177 offset:22528
	ds_read_b128 v[222:225], v177 offset:23552
	global_load_lds_dwordx4 v132, s[26:27]
	s_mov_b32 m0, s43
	s_addc_u32 s71, s27, 0
	global_load_lds_dwordx4 v136, s[26:27]
	s_mov_b32 m0, s44
	s_nop 0
	global_load_lds_dwordx4 v132, s[70:71]
	s_mov_b32 m0, s45
	s_nop 0
	global_load_lds_dwordx4 v136, s[70:71]
	s_add_u32 s100, s28, 0x80
	s_addc_u32 s101, s29, 0
	s_mov_b32 m0, s46
	s_nop 0
	global_load_lds_dwordx4 v130, s[28:29]
	s_mov_b32 m0, s47
	s_nop 0
	global_load_lds_dwordx4 v134, s[28:29]
	s_waitcnt vmcnt(8) lgkmcnt(0)
	s_barrier
	s_setprio 1
	v_mfma_i32_16x16x64_i8 v[62:65], v[150:153], v[194:197], v[62:65]
	v_mfma_i32_16x16x64_i8 v[58:61], v[158:161], v[194:197], v[58:61]
	v_mfma_i32_16x16x64_i8 v[54:57], v[150:153], v[202:205], v[54:57]
	v_mfma_i32_16x16x64_i8 v[50:53], v[158:161], v[202:205], v[50:53]
	v_mfma_i32_16x16x64_i8 v[42:45], v[150:153], v[210:213], v[42:45]
	v_mfma_i32_16x16x64_i8 v[34:37], v[158:161], v[210:213], v[34:37]
	v_mfma_i32_16x16x64_i8 v[26:29], v[150:153], v[218:221], v[26:29]
	v_mfma_i32_16x16x64_i8 v[18:21], v[158:161], v[218:221], v[18:21]
	v_mfma_i32_16x16x64_i8 v[62:65], v[154:157], v[198:201], v[62:65]
	v_mfma_i32_16x16x64_i8 v[58:61], v[162:165], v[198:201], v[58:61]
	v_mfma_i32_16x16x64_i8 v[54:57], v[154:157], v[206:209], v[54:57]
	v_mfma_i32_16x16x64_i8 v[50:53], v[162:165], v[206:209], v[50:53]
	v_mfma_i32_16x16x64_i8 v[42:45], v[154:157], v[214:217], v[42:45]
	v_mfma_i32_16x16x64_i8 v[34:37], v[162:165], v[214:217], v[34:37]
	v_mfma_i32_16x16x64_i8 v[26:29], v[154:157], v[222:225], v[26:29]
	v_mfma_i32_16x16x64_i8 v[18:21], v[162:165], v[222:225], v[18:21]
	s_setprio 0
	s_setprio 1
	v_mfma_i32_16x16x64_i8 v[46:49], v[178:181], v[194:197], v[46:49]
	v_mfma_i32_16x16x64_i8 v[38:41], v[186:189], v[194:197], v[38:41]
	v_mfma_i32_16x16x64_i8 v[30:33], v[178:181], v[202:205], v[30:33]
	v_mfma_i32_16x16x64_i8 v[22:25], v[186:189], v[202:205], v[22:25]
	v_mfma_i32_16x16x64_i8 v[14:17], v[178:181], v[210:213], v[14:17]
	v_mfma_i32_16x16x64_i8 v[10:13], v[186:189], v[210:213], v[10:13]
	v_mfma_i32_16x16x64_i8 v[6:9], v[178:181], v[218:221], v[6:9]
	v_mfma_i32_16x16x64_i8 v[2:5], v[186:189], v[218:221], v[2:5]
	v_mfma_i32_16x16x64_i8 v[46:49], v[182:185], v[198:201], v[46:49]
	v_mfma_i32_16x16x64_i8 v[38:41], v[190:193], v[198:201], v[38:41]
	v_mfma_i32_16x16x64_i8 v[30:33], v[182:185], v[206:209], v[30:33]
	v_mfma_i32_16x16x64_i8 v[22:25], v[190:193], v[206:209], v[22:25]
	v_mfma_i32_16x16x64_i8 v[14:17], v[182:185], v[214:217], v[14:17]
	v_mfma_i32_16x16x64_i8 v[10:13], v[190:193], v[214:217], v[10:13]
	v_mfma_i32_16x16x64_i8 v[6:9], v[182:185], v[222:225], v[6:9]
	v_mfma_i32_16x16x64_i8 v[2:5], v[190:193], v[222:225], v[2:5]
	s_setprio 0
	s_barrier
; #define PG8_STAGE(bufoff, gbase, voff) do { _Pragma("unroll") for (int _i = 0; _i < 2; ++_i) \
;         __builtin_amdgcn_global_load_lds((const unsigned*)((const char*)(gbase) + (voff)[_i]), (PG8_LAS unsigned*)(lds + (bufoff) + ldsw + _i * 8192), 16, 0, 0); } while (0)
; #define PG8_LDA(dst, b, h) do { if constexpr (DT != 1) { _Pragma("unroll") for (int m = 0; m < 4; ++m) _Pragma("unroll") for (int k = 0; k < 2; ++k) dst[m][k] = *(const PG8_LAS bf16x8*)(lds + PG8_SA(b, h) + aoff + m * 2048 + k * 1024); } \
;         else { _Pragma("unroll") for (int m = 0; m < 4; ++m) dst##8[m] = ld32(lds + PG8_SA(b, h) + aoff + m * 2048); } } while (0)
; #define PG8_LDB(dst, b, h) do { if constexpr (DT != 1) { _Pragma("unroll") for (int n = 0; n < 2; ++n) _Pragma("unroll") for (int k = 0; k < 2; ++k) dst[n][k] = *(const PG8_LAS bf16x8*)(lds + PG8_SB(b, h) + boff + n * 2048 + k * 1024); } \
;         else { _Pragma("unroll") for (int n = 0; n < 2; ++n) dst##8[n] = ld32(lds + PG8_SB(b, h) + boff + n * 2048); } } while (0)
; #define PG8_WAIT_V(n) asm volatile("s_waitcnt vmcnt(" #n ")" ::: "memory")
; #define PG8_WAIT_L(n) asm volatile("s_waitcnt lgkmcnt(" #n ")" ::: "memory")
; #define PG8_BAR __builtin_amdgcn_s_barrier()
; #define PG8_SCHED __builtin_amdgcn_sched_barrier(0)
;     ...
;             PG8_LDB(B0, 1, 0); PG8_LDB(B1, 1, 1); PG8_SCHED; PG8_LDA(At, 1, 0); PG8_STAGE(PG8_SA(0, 1), a2 + hstepA, voffA);
;             PG8_WAIT_V(8); PG8_WAIT_L(0); PG8_BAR; PG8_MMA(0, 0, At, B0); PG8_MMA(0, 1, At, B1); PG8_BAR; PG8_SCHED;
;             PG8_LDA(At, 1, 1); PG8_STAGE(PG8_SB(1, 0), b3, voffB); PG8_STAGE(PG8_SB(1, 1), b3 + hstepB, voffB); PG8_STAGE(PG8_SA(1, 0), a3, voffA);
;             PG8_WAIT_V(8); PG8_WAIT_L(0); PG8_BAR; PG8_MMA(1, 0, At, B0); PG8_MMA(1, 1, At, B1); PG8_BAR; PG8_SCHED;
	v_add_u32_e32 v162, s51, v168
	v_add_u32_e32 v190, s52, v168
	ds_read_b128 v[150:153], v162
	ds_read_b128 v[154:157], v162 offset:1024
	ds_read_b128 v[158:161], v162 offset:2048
	ds_read_b128 v[162:165], v162 offset:3072
	ds_read_b128 v[178:181], v190
	ds_read_b128 v[182:185], v190 offset:1024
	ds_read_b128 v[186:189], v190 offset:2048
	ds_read_b128 v[190:193], v190 offset:3072
	s_add_u32 s28, s28, 0x40000
	s_addc_u32 s29, s29, 0
	s_mov_b32 m0, s48
	ds_read_b128 v[194:197], v177 offset:32768
	ds_read_b128 v[198:201], v177 offset:33792
	ds_read_b128 v[202:205], v177 offset:34816
	ds_read_b128 v[206:209], v177 offset:35840
	ds_read_b128 v[210:213], v177 offset:36864
	ds_read_b128 v[214:217], v177 offset:37888
	ds_read_b128 v[218:221], v177 offset:38912
	ds_read_b128 v[222:225], v177 offset:39936
	global_load_lds_dwordx4 v130, s[28:29]
	s_mov_b32 m0, s49
	s_nop 0
	global_load_lds_dwordx4 v134, s[28:29]
	s_waitcnt vmcnt(8) lgkmcnt(0)
	s_barrier
	s_setprio 1
	v_mfma_i32_16x16x64_i8 v[126:129], v[150:153], v[194:197], v[126:129]
	v_mfma_i32_16x16x64_i8 v[122:125], v[158:161], v[194:197], v[122:125]
	v_mfma_i32_16x16x64_i8 v[118:121], v[150:153], v[202:205], v[118:121]
	v_mfma_i32_16x16x64_i8 v[114:117], v[158:161], v[202:205], v[114:117]
	v_mfma_i32_16x16x64_i8 v[106:109], v[150:153], v[210:213], v[106:109]
	v_mfma_i32_16x16x64_i8 v[98:101], v[158:161], v[210:213], v[98:101]
	v_mfma_i32_16x16x64_i8 v[90:93], v[150:153], v[218:221], v[90:93]
	v_mfma_i32_16x16x64_i8 v[82:85], v[158:161], v[218:221], v[82:85]
	v_mfma_i32_16x16x64_i8 v[126:129], v[154:157], v[198:201], v[126:129]
	v_mfma_i32_16x16x64_i8 v[122:125], v[162:165], v[198:201], v[122:125]
	v_mfma_i32_16x16x64_i8 v[118:121], v[154:157], v[206:209], v[118:121]
	v_mfma_i32_16x16x64_i8 v[114:117], v[162:165], v[206:209], v[114:117]
	v_mfma_i32_16x16x64_i8 v[106:109], v[154:157], v[214:217], v[106:109]
	v_mfma_i32_16x16x64_i8 v[98:101], v[162:165], v[214:217], v[98:101]
	v_mfma_i32_16x16x64_i8 v[90:93], v[154:157], v[222:225], v[90:93]
	v_mfma_i32_16x16x64_i8 v[82:85], v[162:165], v[222:225], v[82:85]
	s_setprio 0
	s_setprio 1
	v_mfma_i32_16x16x64_i8 v[110:113], v[178:181], v[194:197], v[110:113]
	v_mfma_i32_16x16x64_i8 v[102:105], v[186:189], v[194:197], v[102:105]
	v_mfma_i32_16x16x64_i8 v[94:97], v[178:181], v[202:205], v[94:97]
	v_mfma_i32_16x16x64_i8 v[86:89], v[186:189], v[202:205], v[86:89]
	v_mfma_i32_16x16x64_i8 v[78:81], v[178:181], v[210:213], v[78:81]
	v_mfma_i32_16x16x64_i8 v[74:77], v[186:189], v[210:213], v[74:77]
	v_mfma_i32_16x16x64_i8 v[70:73], v[178:181], v[218:221], v[70:73]
	v_mfma_i32_16x16x64_i8 v[66:69], v[186:189], v[218:221], v[66:69]
	v_mfma_i32_16x16x64_i8 v[110:113], v[182:185], v[198:201], v[110:113]
	v_mfma_i32_16x16x64_i8 v[102:105], v[190:193], v[198:201], v[102:105]
	v_mfma_i32_16x16x64_i8 v[94:97], v[182:185], v[206:209], v[94:97]
	v_mfma_i32_16x16x64_i8 v[86:89], v[190:193], v[206:209], v[86:89]
	v_mfma_i32_16x16x64_i8 v[78:81], v[182:185], v[214:217], v[78:81]
	v_mfma_i32_16x16x64_i8 v[74:77], v[190:193], v[214:217], v[74:77]
	v_mfma_i32_16x16x64_i8 v[70:73], v[182:185], v[222:225], v[70:73]
	v_mfma_i32_16x16x64_i8 v[66:69], v[190:193], v[222:225], v[66:69]
	s_setprio 0
	s_barrier
	s_mov_b32 m0, s55
	s_add_u32 s26, s26, 0x40080
	ds_read_b128 v[194:197], v177 offset:49152
	ds_read_b128 v[198:201], v177 offset:50176
	ds_read_b128 v[202:205], v177 offset:51200
	ds_read_b128 v[206:209], v177 offset:52224
	ds_read_b128 v[210:213], v177 offset:53248
	ds_read_b128 v[214:217], v177 offset:54272
	ds_read_b128 v[218:221], v177 offset:55296
	ds_read_b128 v[222:225], v177 offset:56320
	global_load_lds_dwordx4 v132, s[98:99]
	s_mov_b32 m0, s56
	s_addc_u32 s27, s27, 0
	global_load_lds_dwordx4 v136, s[98:99]
	s_mov_b32 m0, s59
	s_nop 0
	global_load_lds_dwordx4 v132, s[26:27]
	s_mov_b32 m0, s60
	s_nop 0
	global_load_lds_dwordx4 v136, s[26:27]
	s_mov_b32 m0, s57
	s_nop 0
	global_load_lds_dwordx4 v130, s[100:101]
	s_mov_b32 m0, s58
	s_nop 0
	global_load_lds_dwordx4 v134, s[100:101]
	s_waitcnt vmcnt(8) lgkmcnt(0)
	s_barrier
; #define PG8_WAIT_V(n) asm volatile("s_waitcnt vmcnt(" #n ")" ::: "memory")
; #define PG8_WAIT_L(n) asm volatile("s_waitcnt lgkmcnt(" #n ")" ::: "memory")
; #define PG8_BAR __builtin_amdgcn_s_barrier()
; #define PG8_SCHED __builtin_amdgcn_sched_barrier(0)
; __device__ __forceinline__ f32x4 i32bits_to_f32(f32x4 v) { return (f32x4){(float)__float_as_int(v.x), (float)__float_as_int(v.y), (float)__float_as_int(v.z), (float)__float_as_int(v.w)}; }
;     ...
;             PG8_WAIT_V(8); PG8_WAIT_L(0); PG8_BAR; PG8_MMA(1, 0, At, B0); PG8_MMA(1, 1, At, B1); PG8_BAR; PG8_SCHED;
	s_setprio 1
	v_mfma_i32_16x16x64_i8 v[62:65], v[150:153], v[194:197], v[62:65]
	v_mfma_i32_16x16x64_i8 v[58:61], v[158:161], v[194:197], v[58:61]
	v_mfma_i32_16x16x64_i8 v[54:57], v[150:153], v[202:205], v[54:57]
	v_mfma_i32_16x16x64_i8 v[50:53], v[158:161], v[202:205], v[50:53]
	v_mfma_i32_16x16x64_i8 v[42:45], v[150:153], v[210:213], v[42:45]
	v_mfma_i32_16x16x64_i8 v[34:37], v[158:161], v[210:213], v[34:37]
	v_mfma_i32_16x16x64_i8 v[26:29], v[150:153], v[218:221], v[26:29]
	v_mfma_i32_16x16x64_i8 v[18:21], v[158:161], v[218:221], v[18:21]
	v_mfma_i32_16x16x64_i8 v[62:65], v[154:157], v[198:201], v[62:65]
	v_mfma_i32_16x16x64_i8 v[58:61], v[162:165], v[198:201], v[58:61]
	v_mfma_i32_16x16x64_i8 v[54:57], v[154:157], v[206:209], v[54:57]
	v_mfma_i32_16x16x64_i8 v[50:53], v[162:165], v[206:209], v[50:53]
	v_mfma_i32_16x16x64_i8 v[42:45], v[154:157], v[214:217], v[42:45]
	v_mfma_i32_16x16x64_i8 v[34:37], v[162:165], v[214:217], v[34:37]
	v_mfma_i32_16x16x64_i8 v[26:29], v[154:157], v[222:225], v[26:29]
	v_mfma_i32_16x16x64_i8 v[18:21], v[162:165], v[222:225], v[18:21]
	s_setprio 0
	s_setprio 1
	v_mfma_i32_16x16x64_i8 v[46:49], v[178:181], v[194:197], v[46:49]
	v_mfma_i32_16x16x64_i8 v[38:41], v[186:189], v[194:197], v[38:41]
	v_mfma_i32_16x16x64_i8 v[30:33], v[178:181], v[202:205], v[30:33]
	v_mfma_i32_16x16x64_i8 v[22:25], v[186:189], v[202:205], v[22:25]
	v_mfma_i32_16x16x64_i8 v[14:17], v[178:181], v[210:213], v[14:17]
	v_mfma_i32_16x16x64_i8 v[10:13], v[186:189], v[210:213], v[10:13]
	v_mfma_i32_16x16x64_i8 v[6:9], v[178:181], v[218:221], v[6:9]
	v_mfma_i32_16x16x64_i8 v[2:5], v[186:189], v[218:221], v[2:5]
	v_mfma_i32_16x16x64_i8 v[46:49], v[182:185], v[198:201], v[46:49]
	v_mfma_i32_16x16x64_i8 v[38:41], v[190:193], v[198:201], v[38:41]
	v_mfma_i32_16x16x64_i8 v[30:33], v[182:185], v[206:209], v[30:33]
	v_mfma_i32_16x16x64_i8 v[22:25], v[190:193], v[206:209], v[22:25]
	v_mfma_i32_16x16x64_i8 v[14:17], v[182:185], v[214:217], v[14:17]
	v_mfma_i32_16x16x64_i8 v[10:13], v[190:193], v[214:217], v[10:13]
	v_mfma_i32_16x16x64_i8 v[6:9], v[182:185], v[222:225], v[6:9]
	v_mfma_i32_16x16x64_i8 v[2:5], v[190:193], v[222:225], v[2:5]
	s_setprio 0
	s_barrier
	s_add_u32 s66, s66, 0x100
	s_addc_u32 s67, s67, 0
	s_add_u32 s24, s24, 0x100
	s_addc_u32 s25, s25, 0
	s_cmp_ge_i32 s68, s54
	s_mov_b32 s26, s68
	s_cbranch_scc0 .LBB0_1412
	v_cvt_f32_i32_e32 v150, v126
	v_cvt_f32_i32_e32 v151, v127
	v_cvt_f32_i32_e32 v126, v128
	v_cvt_f32_i32_e32 v127, v129
	v_cvt_f32_i32_e32 v122, v122
	v_cvt_f32_i32_e32 v123, v123
	v_cvt_f32_i32_e32 v124, v124
	v_cvt_f32_i32_e32 v125, v125
	v_cvt_f32_i32_e32 v158, v110
	v_cvt_f32_i32_e32 v159, v111
	v_cvt_f32_i32_e32 v160, v112
	v_cvt_f32_i32_e32 v161, v113
	v_cvt_f32_i32_e32 v162, v102
	v_cvt_f32_i32_e32 v163, v103
	v_cvt_f32_i32_e32 v164, v104
	v_cvt_f32_i32_e32 v165, v105
	v_cvt_f32_i32_e32 v152, v118
	v_cvt_f32_i32_e32 v153, v119
	v_cvt_f32_i32_e32 v154, v120
	v_cvt_f32_i32_e32 v155, v121
	v_cvt_f32_i32_e32 v128, v114
	v_cvt_f32_i32_e32 v129, v115
	v_cvt_f32_i32_e32 v156, v116
	v_cvt_f32_i32_e32 v157, v117
	v_cvt_f32_i32_e32 v116, v94
	v_cvt_f32_i32_e32 v117, v95
	v_cvt_f32_i32_e32 v120, v96
	v_cvt_f32_i32_e32 v121, v97
	v_cvt_f32_i32_e32 v114, v86
	v_cvt_f32_i32_e32 v115, v87
	v_cvt_f32_i32_e32 v118, v88
	v_cvt_f32_i32_e32 v119, v89
	v_cvt_f32_i32_e32 v102, v106
	v_cvt_f32_i32_e32 v103, v107
	v_cvt_f32_i32_e32 v104, v108
	v_cvt_f32_i32_e32 v105, v109
	v_cvt_f32_i32_e32 v98, v98
	v_cvt_f32_i32_e32 v99, v99
	v_cvt_f32_i32_e32 v100, v100
	v_cvt_f32_i32_e32 v101, v101
	v_cvt_f32_i32_e32 v108, v78
	v_cvt_f32_i32_e32 v109, v79
	v_cvt_f32_i32_e32 v112, v80
	v_cvt_f32_i32_e32 v113, v81
	v_cvt_f32_i32_e32 v106, v74
	v_cvt_f32_i32_e32 v107, v75
	v_cvt_f32_i32_e32 v110, v76
	v_cvt_f32_i32_e32 v111, v77
	v_cvt_f32_i32_e32 v76, v90
	v_cvt_f32_i32_e32 v77, v91
	v_cvt_f32_i32_e32 v80, v92
	v_cvt_f32_i32_e32 v81, v93
	v_cvt_f32_i32_e32 v74, v82
	v_cvt_f32_i32_e32 v75, v83
	v_cvt_f32_i32_e32 v78, v84
	v_cvt_f32_i32_e32 v79, v85
	v_cvt_f32_i32_e32 v92, v70
	v_cvt_f32_i32_e32 v93, v71
	v_cvt_f32_i32_e32 v96, v72
	v_cvt_f32_i32_e32 v97, v73
	v_cvt_f32_i32_e32 v90, v66
	v_cvt_f32_i32_e32 v91, v67
	v_cvt_f32_i32_e32 v94, v68
	v_cvt_f32_i32_e32 v95, v69
	v_cvt_f32_i32_e32 v68, v62
	v_cvt_f32_i32_e32 v69, v63
	v_cvt_f32_i32_e32 v72, v64
	v_cvt_f32_i32_e32 v73, v65
	v_cvt_f32_i32_e32 v66, v58
	v_cvt_f32_i32_e32 v67, v59
	v_cvt_f32_i32_e32 v70, v60
	v_cvt_f32_i32_e32 v71, v61
	v_cvt_f32_i32_e32 v84, v46
	v_cvt_f32_i32_e32 v85, v47
	v_cvt_f32_i32_e32 v88, v48
	v_cvt_f32_i32_e32 v89, v49
	v_cvt_f32_i32_e32 v82, v38
	v_cvt_f32_i32_e32 v83, v39
	v_cvt_f32_i32_e32 v86, v40
	v_cvt_f32_i32_e32 v87, v41
	v_cvt_f32_i32_e32 v54, v54
	v_cvt_f32_i32_e32 v55, v55
	v_cvt_f32_i32_e32 v56, v56
	v_cvt_f32_i32_e32 v57, v57
	v_cvt_f32_i32_e32 v50, v50
	v_cvt_f32_i32_e32 v51, v51
	v_cvt_f32_i32_e32 v52, v52
	v_cvt_f32_i32_e32 v53, v53
	v_cvt_f32_i32_e32 v60, v30
	v_cvt_f32_i32_e32 v61, v31
	v_cvt_f32_i32_e32 v64, v32
	v_cvt_f32_i32_e32 v65, v33
	v_cvt_f32_i32_e32 v58, v22
	v_cvt_f32_i32_e32 v59, v23
	v_cvt_f32_i32_e32 v62, v24
	v_cvt_f32_i32_e32 v63, v25
	v_cvt_f32_i32_e32 v38, v42
	v_cvt_f32_i32_e32 v39, v43
	v_cvt_f32_i32_e32 v40, v44
	v_cvt_f32_i32_e32 v41, v45
	v_cvt_f32_i32_e32 v34, v34
	v_cvt_f32_i32_e32 v35, v35
	v_cvt_f32_i32_e32 v36, v36
	v_cvt_f32_i32_e32 v37, v37
	v_cvt_f32_i32_e32 v44, v14
	v_cvt_f32_i32_e32 v45, v15
	v_cvt_f32_i32_e32 v48, v16
	v_cvt_f32_i32_e32 v49, v17
	v_cvt_f32_i32_e32 v42, v10
	v_cvt_f32_i32_e32 v43, v11
	v_cvt_f32_i32_e32 v46, v12
	v_cvt_f32_i32_e32 v47, v13
	v_cvt_f32_i32_e32 v22, v26
	v_cvt_f32_i32_e32 v23, v27
	v_cvt_f32_i32_e32 v24, v28
	v_cvt_f32_i32_e32 v25, v29
	v_cvt_f32_i32_e32 v18, v18
	v_cvt_f32_i32_e32 v19, v19
	v_cvt_f32_i32_e32 v20, v20
	v_cvt_f32_i32_e32 v21, v21
	v_cvt_f32_i32_e32 v28, v6
	v_cvt_f32_i32_e32 v29, v7
	v_cvt_f32_i32_e32 v32, v8
	v_cvt_f32_i32_e32 v33, v9
	v_cvt_f32_i32_e32 v26, v2
	v_cvt_f32_i32_e32 v27, v3
	v_cvt_f32_i32_e32 v30, v4
	v_cvt_f32_i32_e32 v31, v5

; #define PG8_STAGE(bufoff, gbase, voff) do { _Pragma("unroll") for (int _i = 0; _i < 2; ++_i) \
;         __builtin_amdgcn_global_load_lds((const unsigned*)((const char*)(gbase) + (voff)[_i]), (PG8_LAS unsigned*)(lds + (bufoff) + ldsw + _i * 8192), 16, 0, 0); } while (0)
; #define PG8_LDA(dst, b, h) do { if constexpr (DT != 1) { _Pragma("unroll") for (int m = 0; m < 4; ++m) _Pragma("unroll") for (int k = 0; k < 2; ++k) dst[m][k] = *(const PG8_LAS bf16x8*)(lds + PG8_SA(b, h) + aoff + m * 2048 + k * 1024); } \
;         else { _Pragma("unroll") for (int m = 0; m < 4; ++m) dst##8[m] = ld32(lds + PG8_SA(b, h) + aoff + m * 2048); } } while (0)
; #define PG8_WAIT_V(n) asm volatile("s_waitcnt vmcnt(" #n ")" ::: "memory")
; #define PG8_WAIT_L(n) asm volatile("s_waitcnt lgkmcnt(" #n ")" ::: "memory")
; #define PG8_BAR __builtin_amdgcn_s_barrier()
; #define PG8_SCHED __builtin_amdgcn_sched_barrier(0)
;     ...
;         for (int t = 0; t < nt; t += 2) {
;             const bool last = (t == nt - 2);
;             const char* a1 = cA + (size_t)(t + 1) * kstep;
;             const char* a2 = last ? nA : cA + (size_t)(t + 2) * kstep; const char* b2 = last ? nB : cB + (size_t)(t + 2) * kstep;
;             const char* a3 = a2 + kstep; const char* b3 = b2 + kstep;
;             if (last && has_next) S.a_ready(nxt);
;             if constexpr (SP2) {
;             PG8_LDB(B0, 0, 0); PG8_LDB(B1, 0, 1); PG8_SCHED; PG8_LDA(At, 0, 0); PG8_STAGE(PG8_SA(1, 1), a1 + hstepA, voffA);
;             PG8_WAIT_V(8); PG8_WAIT_L(0); PG8_BAR; PG8_MMA(0, 0, At, B0); PG8_MMA(0, 1, At, B1); PG8_BAR; PG8_SCHED;
;             PG8_LDA(At, 0, 1); PG8_STAGE(PG8_SB(0, 0), b2, voffB); PG8_STAGE(PG8_SB(0, 1), b2 + hstepB, voffB); PG8_STAGE(PG8_SA(0, 0), a2, voffA);
;             PG8_WAIT_V(8); PG8_WAIT_L(0); PG8_BAR; PG8_MMA(1, 0, At, B0); PG8_MMA(1, 1, At, B1); PG8_BAR; PG8_SCHED;
;             PG8_LDB(B0, 1, 0); PG8_LDB(B1, 1, 1); PG8_SCHED; PG8_LDA(At, 1, 0); PG8_STAGE(PG8_SA(0, 1), a2 + hstepA, voffA);
;             PG8_WAIT_V(8); PG8_WAIT_L(0); PG8_BAR; PG8_MMA(0, 0, At, B0); PG8_MMA(0, 1, At, B1); PG8_BAR; PG8_SCHED;
;             PG8_LDA(At, 1, 1); PG8_STAGE(PG8_SB(1, 0), b3, voffB); PG8_STAGE(PG8_SB(1, 1), b3 + hstepB, voffB); PG8_STAGE(PG8_SA(1, 0), a3, voffA);
;             PG8_WAIT_V(8); PG8_WAIT_L(0); PG8_BAR; PG8_MMA(1, 0, At, B0); PG8_MMA(1, 1, At, B1); PG8_BAR; PG8_SCHED;
.LBB0_2262:
	ds_read_b128 v[154:157], v148
	ds_read_b128 v[158:161], v148 offset:1024
	ds_read_b128 v[162:165], v148 offset:2048
	ds_read_b128 v[166:169], v148 offset:3072
	ds_read_b128 v[170:173], v149
	ds_read_b128 v[174:177], v149 offset:1024
	ds_read_b128 v[178:181], v149 offset:2048
	ds_read_b128 v[182:185], v149 offset:3072
	s_add_i32 s65, s28, 2
	s_add_u32 s29, s26, 0xfff80080
	s_addc_u32 s30, s27, -1
	s_cmp_eq_u32 s61, s28
	s_cselect_b32 s28, s23, s25
	s_cselect_b32 s31, s2, s30
	s_cselect_b32 s30, s15, s29
	s_cselect_b32 s29, s17, s64
	s_add_i32 m0, s44, 0xc000
	ds_read_b128 v[186:189], v150
	ds_read_b128 v[190:193], v150 offset:1024
	ds_read_b128 v[194:197], v150 offset:2048
	ds_read_b128 v[198:201], v150 offset:3072
	ds_read_b128 v[202:205], v150 offset:4096
	ds_read_b128 v[206:209], v150 offset:5120
	ds_read_b128 v[210:213], v150 offset:6144
	ds_read_b128 v[214:217], v150 offset:7168
	global_load_lds_dwordx4 v142, s[26:27]
	s_add_i32 m0, s44, 0xe000
	s_nop 0
	global_load_lds_dwordx4 v140, s[26:27]
	s_waitcnt vmcnt(8) lgkmcnt(0)
	s_barrier
	s_setprio 1
	v_mfma_f32_16x16x32_bf16 v[126:129], v[154:157], v[186:189], v[126:129]
	v_mfma_f32_16x16x32_bf16 v[122:125], v[162:165], v[186:189], v[122:125]
	v_mfma_f32_16x16x32_bf16 v[110:113], v[154:157], v[194:197], v[110:113]
	v_mfma_f32_16x16x32_bf16 v[106:109], v[162:165], v[194:197], v[106:109]
	v_mfma_f32_16x16x32_bf16 v[94:97], v[154:157], v[202:205], v[94:97]
	v_mfma_f32_16x16x32_bf16 v[90:93], v[162:165], v[202:205], v[90:93]
	v_mfma_f32_16x16x32_bf16 v[78:81], v[154:157], v[210:213], v[78:81]
	v_mfma_f32_16x16x32_bf16 v[74:77], v[162:165], v[210:213], v[74:77]
	v_mfma_f32_16x16x32_bf16 v[126:129], v[158:161], v[190:193], v[126:129]
	v_mfma_f32_16x16x32_bf16 v[122:125], v[166:169], v[190:193], v[122:125]
	v_mfma_f32_16x16x32_bf16 v[110:113], v[158:161], v[198:201], v[110:113]
	v_mfma_f32_16x16x32_bf16 v[106:109], v[166:169], v[198:201], v[106:109]
	v_mfma_f32_16x16x32_bf16 v[94:97], v[158:161], v[206:209], v[94:97]
	v_mfma_f32_16x16x32_bf16 v[90:93], v[166:169], v[206:209], v[90:93]
	v_mfma_f32_16x16x32_bf16 v[78:81], v[158:161], v[214:217], v[78:81]
	v_mfma_f32_16x16x32_bf16 v[74:77], v[166:169], v[214:217], v[74:77]
	s_setprio 0
	s_setprio 1
	v_mfma_f32_16x16x32_bf16 v[118:121], v[170:173], v[186:189], v[118:121]
	v_mfma_f32_16x16x32_bf16 v[114:117], v[178:181], v[186:189], v[114:117]
	v_mfma_f32_16x16x32_bf16 v[102:105], v[170:173], v[194:197], v[102:105]
	v_mfma_f32_16x16x32_bf16 v[98:101], v[178:181], v[194:197], v[98:101]
	v_mfma_f32_16x16x32_bf16 v[86:89], v[170:173], v[202:205], v[86:89]
	v_mfma_f32_16x16x32_bf16 v[82:85], v[178:181], v[202:205], v[82:85]
	v_mfma_f32_16x16x32_bf16 v[70:73], v[170:173], v[210:213], v[70:73]
	v_mfma_f32_16x16x32_bf16 v[66:69], v[178:181], v[210:213], v[66:69]
	v_mfma_f32_16x16x32_bf16 v[118:121], v[174:177], v[190:193], v[118:121]
	v_mfma_f32_16x16x32_bf16 v[114:117], v[182:185], v[190:193], v[114:117]
	v_mfma_f32_16x16x32_bf16 v[102:105], v[174:177], v[198:201], v[102:105]
	v_mfma_f32_16x16x32_bf16 v[98:101], v[182:185], v[198:201], v[98:101]
	v_mfma_f32_16x16x32_bf16 v[86:89], v[174:177], v[206:209], v[86:89]
	v_mfma_f32_16x16x32_bf16 v[82:85], v[182:185], v[206:209], v[82:85]
	v_mfma_f32_16x16x32_bf16 v[70:73], v[174:177], v[214:217], v[70:73]
	v_mfma_f32_16x16x32_bf16 v[66:69], v[182:185], v[214:217], v[66:69]
	s_setprio 0
	s_barrier
	s_mov_b32 m0, s40
	s_add_u32 s98, s28, 0x80
	s_addc_u32 s99, s29, 0
	s_add_u32 s66, s28, 0x80000
	ds_read_b128 v[186:189], v150 offset:16384
	ds_read_b128 v[190:193], v150 offset:17408
	ds_read_b128 v[194:197], v150 offset:18432
	ds_read_b128 v[198:201], v150 offset:19456
	ds_read_b128 v[202:205], v150 offset:20480
	ds_read_b128 v[206:209], v150 offset:21504
	ds_read_b128 v[210:213], v150 offset:22528
	ds_read_b128 v[214:217], v150 offset:23552
	global_load_lds_dwordx4 v132, s[28:29]
	s_mov_b32 m0, s41
	s_addc_u32 s67, s29, 0
	global_load_lds_dwordx4 v136, s[28:29]
	s_mov_b32 m0, s42
	s_nop 0
	global_load_lds_dwordx4 v132, s[66:67]
	s_mov_b32 m0, s43
	s_nop 0
	global_load_lds_dwordx4 v136, s[66:67]
	s_add_u32 s100, s30, 0x80
	s_addc_u32 s101, s31, 0
	s_mov_b32 m0, s44
	s_nop 0
	global_load_lds_dwordx4 v130, s[30:31]
	s_mov_b32 m0, s45
	s_nop 0
	global_load_lds_dwordx4 v134, s[30:31]
	s_waitcnt vmcnt(8) lgkmcnt(0)
	s_barrier
	s_setprio 1
	v_mfma_f32_16x16x32_bf16 v[62:65], v[154:157], v[186:189], v[62:65]
	v_mfma_f32_16x16x32_bf16 v[58:61], v[162:165], v[186:189], v[58:61]
	v_mfma_f32_16x16x32_bf16 v[46:49], v[154:157], v[194:197], v[46:49]
	v_mfma_f32_16x16x32_bf16 v[42:45], v[162:165], v[194:197], v[42:45]
	v_mfma_f32_16x16x32_bf16 v[30:33], v[154:157], v[202:205], v[30:33]
	v_mfma_f32_16x16x32_bf16 v[26:29], v[162:165], v[202:205], v[26:29]
	v_mfma_f32_16x16x32_bf16 v[14:17], v[154:157], v[210:213], v[14:17]
	v_mfma_f32_16x16x32_bf16 v[10:13], v[162:165], v[210:213], v[10:13]
	v_mfma_f32_16x16x32_bf16 v[62:65], v[158:161], v[190:193], v[62:65]
	v_mfma_f32_16x16x32_bf16 v[58:61], v[166:169], v[190:193], v[58:61]
	v_mfma_f32_16x16x32_bf16 v[46:49], v[158:161], v[198:201], v[46:49]
	v_mfma_f32_16x16x32_bf16 v[42:45], v[166:169], v[198:201], v[42:45]
	v_mfma_f32_16x16x32_bf16 v[30:33], v[158:161], v[206:209], v[30:33]
	v_mfma_f32_16x16x32_bf16 v[26:29], v[166:169], v[206:209], v[26:29]
	v_mfma_f32_16x16x32_bf16 v[14:17], v[158:161], v[214:217], v[14:17]
	v_mfma_f32_16x16x32_bf16 v[10:13], v[166:169], v[214:217], v[10:13]
	s_setprio 0
	s_setprio 1
	v_mfma_f32_16x16x32_bf16 v[54:57], v[170:173], v[186:189], v[54:57]
	v_mfma_f32_16x16x32_bf16 v[50:53], v[178:181], v[186:189], v[50:53]
	v_mfma_f32_16x16x32_bf16 v[38:41], v[170:173], v[194:197], v[38:41]
	v_mfma_f32_16x16x32_bf16 v[34:37], v[178:181], v[194:197], v[34:37]
	v_mfma_f32_16x16x32_bf16 v[22:25], v[170:173], v[202:205], v[22:25]
	v_mfma_f32_16x16x32_bf16 v[18:21], v[178:181], v[202:205], v[18:21]
	v_mfma_f32_16x16x32_bf16 v[6:9], v[170:173], v[210:213], v[6:9]
	v_mfma_f32_16x16x32_bf16 v[2:5], v[178:181], v[210:213], v[2:5]
	v_mfma_f32_16x16x32_bf16 v[54:57], v[174:177], v[190:193], v[54:57]
	v_mfma_f32_16x16x32_bf16 v[50:53], v[182:185], v[190:193], v[50:53]
	v_mfma_f32_16x16x32_bf16 v[38:41], v[174:177], v[198:201], v[38:41]
	v_mfma_f32_16x16x32_bf16 v[34:37], v[182:185], v[198:201], v[34:37]
	v_mfma_f32_16x16x32_bf16 v[22:25], v[174:177], v[206:209], v[22:25]
	v_mfma_f32_16x16x32_bf16 v[18:21], v[182:185], v[206:209], v[18:21]
	v_mfma_f32_16x16x32_bf16 v[6:9], v[174:177], v[214:217], v[6:9]
	v_mfma_f32_16x16x32_bf16 v[2:5], v[182:185], v[214:217], v[2:5]
	s_setprio 0
	s_barrier
; #define PG8_STAGE(bufoff, gbase, voff) do { _Pragma("unroll") for (int _i = 0; _i < 2; ++_i) \
;         __builtin_amdgcn_global_load_lds((const unsigned*)((const char*)(gbase) + (voff)[_i]), (PG8_LAS unsigned*)(lds + (bufoff) + ldsw + _i * 8192), 16, 0, 0); } while (0)
; #define PG8_LDA(dst, b, h) do { if constexpr (DT != 1) { _Pragma("unroll") for (int m = 0; m < 4; ++m) _Pragma("unroll") for (int k = 0; k < 2; ++k) dst[m][k] = *(const PG8_LAS bf16x8*)(lds + PG8_SA(b, h) + aoff + m * 2048 + k * 1024); } \
;         else { _Pragma("unroll") for (int m = 0; m < 4; ++m) dst##8[m] = ld32(lds + PG8_SA(b, h) + aoff + m * 2048); } } while (0)
; #define PG8_WAIT_V(n) asm volatile("s_waitcnt vmcnt(" #n ")" ::: "memory")
; #define PG8_WAIT_L(n) asm volatile("s_waitcnt lgkmcnt(" #n ")" ::: "memory")
; #define PG8_BAR __builtin_amdgcn_s_barrier()
; #define PG8_SCHED __builtin_amdgcn_sched_barrier(0)
;     ...
;         for (int t = 0; t < nt; t += 2) {
;             const bool last = (t == nt - 2);
;             const char* a1 = cA + (size_t)(t + 1) * kstep;
;             const char* a2 = last ? nA : cA + (size_t)(t + 2) * kstep; const char* b2 = last ? nB : cB + (size_t)(t + 2) * kstep;
;             const char* a3 = a2 + kstep; const char* b3 = b2 + kstep;
;             if (last && has_next) S.a_ready(nxt);
;             if constexpr (SP2) {
;             PG8_LDB(B0, 0, 0); PG8_LDB(B1, 0, 1); PG8_SCHED; PG8_LDA(At, 0, 0); PG8_STAGE(PG8_SA(1, 1), a1 + hstepA, voffA);
;             PG8_WAIT_V(8); PG8_WAIT_L(0); PG8_BAR; PG8_MMA(0, 0, At, B0); PG8_MMA(0, 1, At, B1); PG8_BAR; PG8_SCHED;
;             PG8_LDA(At, 0, 1); PG8_STAGE(PG8_SB(0, 0), b2, voffB); PG8_STAGE(PG8_SB(0, 1), b2 + hstepB, voffB); PG8_STAGE(PG8_SA(0, 0), a2, voffA);
;             PG8_WAIT_V(8); PG8_WAIT_L(0); PG8_BAR; PG8_MMA(1, 0, At, B0); PG8_MMA(1, 1, At, B1); PG8_BAR; PG8_SCHED;
;             PG8_LDB(B0, 1, 0); PG8_LDB(B1, 1, 1); PG8_SCHED; PG8_LDA(At, 1, 0); PG8_STAGE(PG8_SA(0, 1), a2 + hstepA, voffA);
;             PG8_WAIT_V(8); PG8_WAIT_L(0); PG8_BAR; PG8_MMA(0, 0, At, B0); PG8_MMA(0, 1, At, B1); PG8_BAR; PG8_SCHED;
;             PG8_LDA(At, 1, 1); PG8_STAGE(PG8_SB(1, 0), b3, voffB); PG8_STAGE(PG8_SB(1, 1), b3 + hstepB, voffB); PG8_STAGE(PG8_SA(1, 0), a3, voffA);
;             PG8_WAIT_V(8); PG8_WAIT_L(0); PG8_BAR; PG8_MMA(1, 0, At, B0); PG8_MMA(1, 1, At, B1); PG8_BAR; PG8_SCHED;
	ds_read_b128 v[154:157], v151
	ds_read_b128 v[158:161], v151 offset:1024
	ds_read_b128 v[162:165], v151 offset:2048
	ds_read_b128 v[166:169], v151 offset:3072
	ds_read_b128 v[170:173], v152
	ds_read_b128 v[174:177], v152 offset:1024
	ds_read_b128 v[178:181], v152 offset:2048
	ds_read_b128 v[182:185], v152 offset:3072
	s_add_u32 s30, s30, 0x80000
	s_addc_u32 s31, s31, 0
	s_mov_b32 m0, s46
	ds_read_b128 v[186:189], v150 offset:32768
	ds_read_b128 v[190:193], v150 offset:33792
	ds_read_b128 v[194:197], v150 offset:34816
	ds_read_b128 v[198:201], v150 offset:35840
	ds_read_b128 v[202:205], v150 offset:36864
	ds_read_b128 v[206:209], v150 offset:37888
	ds_read_b128 v[210:213], v150 offset:38912
	ds_read_b128 v[214:217], v150 offset:39936
	global_load_lds_dwordx4 v130, s[30:31]
	s_mov_b32 m0, s47
	s_nop 0
	global_load_lds_dwordx4 v134, s[30:31]
	s_waitcnt vmcnt(8) lgkmcnt(0)
	s_barrier
	s_setprio 1
	v_mfma_f32_16x16x32_bf16 v[126:129], v[154:157], v[186:189], v[126:129]
	v_mfma_f32_16x16x32_bf16 v[122:125], v[162:165], v[186:189], v[122:125]
	v_mfma_f32_16x16x32_bf16 v[110:113], v[154:157], v[194:197], v[110:113]
	v_mfma_f32_16x16x32_bf16 v[106:109], v[162:165], v[194:197], v[106:109]
	v_mfma_f32_16x16x32_bf16 v[94:97], v[154:157], v[202:205], v[94:97]
	v_mfma_f32_16x16x32_bf16 v[90:93], v[162:165], v[202:205], v[90:93]
	v_mfma_f32_16x16x32_bf16 v[78:81], v[154:157], v[210:213], v[78:81]
	v_mfma_f32_16x16x32_bf16 v[74:77], v[162:165], v[210:213], v[74:77]
	v_mfma_f32_16x16x32_bf16 v[126:129], v[158:161], v[190:193], v[126:129]
	v_mfma_f32_16x16x32_bf16 v[122:125], v[166:169], v[190:193], v[122:125]
	v_mfma_f32_16x16x32_bf16 v[110:113], v[158:161], v[198:201], v[110:113]
	v_mfma_f32_16x16x32_bf16 v[106:109], v[166:169], v[198:201], v[106:109]
	v_mfma_f32_16x16x32_bf16 v[94:97], v[158:161], v[206:209], v[94:97]
	v_mfma_f32_16x16x32_bf16 v[90:93], v[166:169], v[206:209], v[90:93]
	v_mfma_f32_16x16x32_bf16 v[78:81], v[158:161], v[214:217], v[78:81]
	v_mfma_f32_16x16x32_bf16 v[74:77], v[166:169], v[214:217], v[74:77]
	s_setprio 0
	s_setprio 1
	v_mfma_f32_16x16x32_bf16 v[118:121], v[170:173], v[186:189], v[118:121]
	v_mfma_f32_16x16x32_bf16 v[114:117], v[178:181], v[186:189], v[114:117]
	v_mfma_f32_16x16x32_bf16 v[102:105], v[170:173], v[194:197], v[102:105]
	v_mfma_f32_16x16x32_bf16 v[98:101], v[178:181], v[194:197], v[98:101]
	v_mfma_f32_16x16x32_bf16 v[86:89], v[170:173], v[202:205], v[86:89]
	v_mfma_f32_16x16x32_bf16 v[82:85], v[178:181], v[202:205], v[82:85]
	v_mfma_f32_16x16x32_bf16 v[70:73], v[170:173], v[210:213], v[70:73]
	v_mfma_f32_16x16x32_bf16 v[66:69], v[178:181], v[210:213], v[66:69]
	v_mfma_f32_16x16x32_bf16 v[118:121], v[174:177], v[190:193], v[118:121]
	v_mfma_f32_16x16x32_bf16 v[114:117], v[182:185], v[190:193], v[114:117]
	v_mfma_f32_16x16x32_bf16 v[102:105], v[174:177], v[198:201], v[102:105]
	v_mfma_f32_16x16x32_bf16 v[98:101], v[182:185], v[198:201], v[98:101]
	v_mfma_f32_16x16x32_bf16 v[86:89], v[174:177], v[206:209], v[86:89]
	v_mfma_f32_16x16x32_bf16 v[82:85], v[182:185], v[206:209], v[82:85]
	v_mfma_f32_16x16x32_bf16 v[70:73], v[174:177], v[214:217], v[70:73]
	v_mfma_f32_16x16x32_bf16 v[66:69], v[182:185], v[214:217], v[66:69]
	s_setprio 0
	s_barrier
	s_mov_b32 m0, s53
	s_add_u32 s28, s28, 0x80080
	ds_read_b128 v[186:189], v150 offset:49152
	ds_read_b128 v[190:193], v150 offset:50176
	ds_read_b128 v[194:197], v150 offset:51200
	ds_read_b128 v[198:201], v150 offset:52224
	ds_read_b128 v[202:205], v150 offset:53248
	ds_read_b128 v[206:209], v150 offset:54272
	ds_read_b128 v[210:213], v150 offset:55296
	ds_read_b128 v[214:217], v150 offset:56320
	global_load_lds_dwordx4 v132, s[98:99]
	s_mov_b32 m0, s54
	s_addc_u32 s29, s29, 0
	global_load_lds_dwordx4 v136, s[98:99]
	s_mov_b32 m0, s57
	s_nop 0
	global_load_lds_dwordx4 v132, s[28:29]
	s_mov_b32 m0, s58
	s_nop 0
	global_load_lds_dwordx4 v136, s[28:29]
	s_mov_b32 m0, s55
	s_nop 0
	global_load_lds_dwordx4 v130, s[100:101]
	s_mov_b32 m0, s56
	s_nop 0
	global_load_lds_dwordx4 v134, s[100:101]
	s_waitcnt vmcnt(8) lgkmcnt(0)
	s_barrier
	s_setprio 1
	v_mfma_f32_16x16x32_bf16 v[62:65], v[154:157], v[186:189], v[62:65]
	v_mfma_f32_16x16x32_bf16 v[58:61], v[162:165], v[186:189], v[58:61]
	v_mfma_f32_16x16x32_bf16 v[46:49], v[154:157], v[194:197], v[46:49]
	v_mfma_f32_16x16x32_bf16 v[42:45], v[162:165], v[194:197], v[42:45]
	v_mfma_f32_16x16x32_bf16 v[30:33], v[154:157], v[202:205], v[30:33]
	v_mfma_f32_16x16x32_bf16 v[26:29], v[162:165], v[202:205], v[26:29]
	v_mfma_f32_16x16x32_bf16 v[14:17], v[154:157], v[210:213], v[14:17]
	v_mfma_f32_16x16x32_bf16 v[10:13], v[162:165], v[210:213], v[10:13]
	v_mfma_f32_16x16x32_bf16 v[62:65], v[158:161], v[190:193], v[62:65]
	v_mfma_f32_16x16x32_bf16 v[58:61], v[166:169], v[190:193], v[58:61]
	v_mfma_f32_16x16x32_bf16 v[46:49], v[158:161], v[198:201], v[46:49]
	v_mfma_f32_16x16x32_bf16 v[42:45], v[166:169], v[198:201], v[42:45]
	v_mfma_f32_16x16x32_bf16 v[30:33], v[158:161], v[206:209], v[30:33]
	v_mfma_f32_16x16x32_bf16 v[26:29], v[166:169], v[206:209], v[26:29]
	v_mfma_f32_16x16x32_bf16 v[14:17], v[158:161], v[214:217], v[14:17]
	v_mfma_f32_16x16x32_bf16 v[10:13], v[166:169], v[214:217], v[10:13]
	s_setprio 0
	s_setprio 1
	v_mfma_f32_16x16x32_bf16 v[54:57], v[170:173], v[186:189], v[54:57]
	v_mfma_f32_16x16x32_bf16 v[50:53], v[178:181], v[186:189], v[50:53]
	v_mfma_f32_16x16x32_bf16 v[38:41], v[170:173], v[194:197], v[38:41]
	v_mfma_f32_16x16x32_bf16 v[34:37], v[178:181], v[194:197], v[34:37]
	v_mfma_f32_16x16x32_bf16 v[22:25], v[170:173], v[202:205], v[22:25]
	v_mfma_f32_16x16x32_bf16 v[18:21], v[178:181], v[202:205], v[18:21]
	v_mfma_f32_16x16x32_bf16 v[6:9], v[170:173], v[210:213], v[6:9]
	v_mfma_f32_16x16x32_bf16 v[2:5], v[178:181], v[210:213], v[2:5]
	v_mfma_f32_16x16x32_bf16 v[54:57], v[174:177], v[190:193], v[54:57]
	v_mfma_f32_16x16x32_bf16 v[50:53], v[182:185], v[190:193], v[50:53]
	v_mfma_f32_16x16x32_bf16 v[38:41], v[174:177], v[198:201], v[38:41]
	v_mfma_f32_16x16x32_bf16 v[34:37], v[182:185], v[198:201], v[34:37]
	v_mfma_f32_16x16x32_bf16 v[22:25], v[174:177], v[206:209], v[22:25]
	v_mfma_f32_16x16x32_bf16 v[18:21], v[182:185], v[206:209], v[18:21]
	v_mfma_f32_16x16x32_bf16 v[6:9], v[174:177], v[214:217], v[6:9]
	v_mfma_f32_16x16x32_bf16 v[2:5], v[182:185], v[214:217], v[2:5]
	s_setprio 0
	s_barrier
	s_add_u32 s25, s25, 0x100
	s_addc_u32 s64, s64, 0
	s_add_u32 s26, s26, 0x100
	s_addc_u32 s27, s27, 0
	s_cmp_ge_i32 s65, s52
	s_mov_b32 s28, s65
	s_cbranch_scc0 .LBB0_2262

; #define PG8_STAGE(bufoff, gbase, voff) do { _Pragma("unroll") for (int _i = 0; _i < 2; ++_i) \
;         __builtin_amdgcn_global_load_lds((const unsigned*)((const char*)(gbase) + (voff)[_i]), (PG8_LAS unsigned*)(lds + (bufoff) + ldsw + _i * 8192), 16, 0, 0); } while (0)
; #define PG8_LDA(dst, b, h) do { if constexpr (DT != 1) { _Pragma("unroll") for (int m = 0; m < 4; ++m) _Pragma("unroll") for (int k = 0; k < 2; ++k) dst[m][k] = *(const PG8_LAS bf16x8*)(lds + PG8_SA(b, h) + aoff + m * 2048 + k * 1024); } \
;         else { _Pragma("unroll") for (int m = 0; m < 4; ++m) dst##8[m] = ld32(lds + PG8_SA(b, h) + aoff + m * 2048); } } while (0)
; #define PG8_WAIT_V(n) asm volatile("s_waitcnt vmcnt(" #n ")" ::: "memory")
; #define PG8_WAIT_L(n) asm volatile("s_waitcnt lgkmcnt(" #n ")" ::: "memory")
; #define PG8_BAR __builtin_amdgcn_s_barrier()
; #define PG8_SCHED __builtin_amdgcn_sched_barrier(0)
;     ...
;         for (int t = 0; t < nt; t += 2) {
;             const bool last = (t == nt - 2);
;             const char* a1 = cA + (size_t)(t + 1) * kstep;
;             const char* a2 = last ? nA : cA + (size_t)(t + 2) * kstep; const char* b2 = last ? nB : cB + (size_t)(t + 2) * kstep;
;             const char* a3 = a2 + kstep; const char* b3 = b2 + kstep;
;             if (last && has_next) S.a_ready(nxt);
;             if constexpr (SP2) {
;             PG8_LDB(B0, 0, 0); PG8_LDB(B1, 0, 1); PG8_SCHED; PG8_LDA(At, 0, 0); PG8_STAGE(PG8_SA(1, 1), a1 + hstepA, voffA);
;             PG8_WAIT_V(8); PG8_WAIT_L(0); PG8_BAR; PG8_MMA(0, 0, At, B0); PG8_MMA(0, 1, At, B1); PG8_BAR; PG8_SCHED;
;             PG8_LDA(At, 0, 1); PG8_STAGE(PG8_SB(0, 0), b2, voffB); PG8_STAGE(PG8_SB(0, 1), b2 + hstepB, voffB); PG8_STAGE(PG8_SA(0, 0), a2, voffA);
;             PG8_WAIT_V(8); PG8_WAIT_L(0); PG8_BAR; PG8_MMA(1, 0, At, B0); PG8_MMA(1, 1, At, B1); PG8_BAR; PG8_SCHED;
;             PG8_LDB(B0, 1, 0); PG8_LDB(B1, 1, 1); PG8_SCHED; PG8_LDA(At, 1, 0); PG8_STAGE(PG8_SA(0, 1), a2 + hstepA, voffA);
;             PG8_WAIT_V(8); PG8_WAIT_L(0); PG8_BAR; PG8_MMA(0, 0, At, B0); PG8_MMA(0, 1, At, B1); PG8_BAR; PG8_SCHED;
;             PG8_LDA(At, 1, 1); PG8_STAGE(PG8_SB(1, 0), b3, voffB); PG8_STAGE(PG8_SB(1, 1), b3 + hstepB, voffB); PG8_STAGE(PG8_SA(1, 0), a3, voffA);
;             PG8_WAIT_V(8); PG8_WAIT_L(0); PG8_BAR; PG8_MMA(1, 0, At, B0); PG8_MMA(1, 1, At, B1); PG8_BAR; PG8_SCHED;
.LBB0_3356:
	ds_read_b128 v[130:133], v173
	ds_read_b128 v[134:137], v173 offset:1024
	ds_read_b128 v[138:141], v173 offset:2048
	ds_read_b128 v[142:145], v173 offset:3072
	ds_read_b128 v[164:167], v174
	ds_read_b128 v[168:171], v174 offset:1024
	ds_read_b128 v[178:181], v174 offset:2048
	ds_read_b128 v[182:185], v174 offset:3072
	s_add_i32 s78, s42, 2
	s_add_u32 s43, s40, 0xffff0080
	s_addc_u32 s44, s41, -1
	s_cmp_eq_u32 s74, s42
	s_cselect_b32 s42, s39, s76
	s_cselect_b32 s45, s3, s44
	s_cselect_b32 s44, s29, s43
	s_cselect_b32 s43, s31, s77
	s_add_i32 m0, s56, 0xc000
	ds_read_b128 v[186:189], v175
	ds_read_b128 v[190:193], v175 offset:1024
	ds_read_b128 v[194:197], v175 offset:2048
	ds_read_b128 v[198:201], v175 offset:3072
	ds_read_b128 v[202:205], v175 offset:4096
	ds_read_b128 v[206:209], v175 offset:5120
	ds_read_b128 v[210:213], v175 offset:6144
	ds_read_b128 v[214:217], v175 offset:7168
	global_load_lds_dwordx4 v158, s[40:41]
	s_add_i32 m0, s56, 0xe000
	s_nop 0
	global_load_lds_dwordx4 v156, s[40:41]
	s_waitcnt vmcnt(8) lgkmcnt(0)
	s_barrier
	s_setprio 1
	v_mfma_f32_16x16x32_bf16 v[126:129], v[130:133], v[186:189], v[126:129]
	v_mfma_f32_16x16x32_bf16 v[122:125], v[138:141], v[186:189], v[122:125]
	v_mfma_f32_16x16x32_bf16 v[110:113], v[130:133], v[194:197], v[110:113]
	v_mfma_f32_16x16x32_bf16 v[106:109], v[138:141], v[194:197], v[106:109]
	v_mfma_f32_16x16x32_bf16 v[94:97], v[130:133], v[202:205], v[94:97]
	v_mfma_f32_16x16x32_bf16 v[90:93], v[138:141], v[202:205], v[90:93]
	v_mfma_f32_16x16x32_bf16 v[78:81], v[130:133], v[210:213], v[78:81]
	v_mfma_f32_16x16x32_bf16 v[74:77], v[138:141], v[210:213], v[74:77]
	v_mfma_f32_16x16x32_bf16 v[126:129], v[134:137], v[190:193], v[126:129]
	v_mfma_f32_16x16x32_bf16 v[122:125], v[142:145], v[190:193], v[122:125]
	v_mfma_f32_16x16x32_bf16 v[110:113], v[134:137], v[198:201], v[110:113]
	v_mfma_f32_16x16x32_bf16 v[106:109], v[142:145], v[198:201], v[106:109]
	v_mfma_f32_16x16x32_bf16 v[94:97], v[134:137], v[206:209], v[94:97]
	v_mfma_f32_16x16x32_bf16 v[90:93], v[142:145], v[206:209], v[90:93]
	v_mfma_f32_16x16x32_bf16 v[78:81], v[134:137], v[214:217], v[78:81]
	v_mfma_f32_16x16x32_bf16 v[74:77], v[142:145], v[214:217], v[74:77]
	s_setprio 0
	s_setprio 1
	v_mfma_f32_16x16x32_bf16 v[118:121], v[164:167], v[186:189], v[118:121]
	v_mfma_f32_16x16x32_bf16 v[114:117], v[178:181], v[186:189], v[114:117]
	v_mfma_f32_16x16x32_bf16 v[102:105], v[164:167], v[194:197], v[102:105]
	v_mfma_f32_16x16x32_bf16 v[98:101], v[178:181], v[194:197], v[98:101]
	v_mfma_f32_16x16x32_bf16 v[86:89], v[164:167], v[202:205], v[86:89]
	v_mfma_f32_16x16x32_bf16 v[82:85], v[178:181], v[202:205], v[82:85]
	v_mfma_f32_16x16x32_bf16 v[70:73], v[164:167], v[210:213], v[70:73]
	v_mfma_f32_16x16x32_bf16 v[66:69], v[178:181], v[210:213], v[66:69]
	v_mfma_f32_16x16x32_bf16 v[118:121], v[168:171], v[190:193], v[118:121]
	v_mfma_f32_16x16x32_bf16 v[114:117], v[182:185], v[190:193], v[114:117]
	v_mfma_f32_16x16x32_bf16 v[102:105], v[168:171], v[198:201], v[102:105]
	v_mfma_f32_16x16x32_bf16 v[98:101], v[182:185], v[198:201], v[98:101]
	v_mfma_f32_16x16x32_bf16 v[86:89], v[168:171], v[206:209], v[86:89]
	v_mfma_f32_16x16x32_bf16 v[82:85], v[182:185], v[206:209], v[82:85]
	v_mfma_f32_16x16x32_bf16 v[70:73], v[168:171], v[214:217], v[70:73]
	v_mfma_f32_16x16x32_bf16 v[66:69], v[182:185], v[214:217], v[66:69]
	s_setprio 0
	s_barrier
	s_mov_b32 m0, s52
	s_add_u32 s98, s42, 0x80
	s_addc_u32 s99, s43, 0
	s_add_u32 s80, s42, 0x10000
	ds_read_b128 v[186:189], v175 offset:16384
	ds_read_b128 v[190:193], v175 offset:17408
	ds_read_b128 v[194:197], v175 offset:18432
	ds_read_b128 v[198:201], v175 offset:19456
	ds_read_b128 v[202:205], v175 offset:20480
	ds_read_b128 v[206:209], v175 offset:21504
	ds_read_b128 v[210:213], v175 offset:22528
	ds_read_b128 v[214:217], v175 offset:23552
	global_load_lds_dwordx4 v148, s[42:43]
	s_mov_b32 m0, s53
	s_addc_u32 s81, s43, 0
	global_load_lds_dwordx4 v152, s[42:43]
	s_mov_b32 m0, s54
	s_nop 0
	global_load_lds_dwordx4 v148, s[80:81]
	s_mov_b32 m0, s55
	s_nop 0
	global_load_lds_dwordx4 v152, s[80:81]
	s_add_u32 s100, s44, 0x80
	s_addc_u32 s101, s45, 0
	s_mov_b32 m0, s56
	s_nop 0
	global_load_lds_dwordx4 v146, s[44:45]
	s_mov_b32 m0, s57
	s_nop 0
	global_load_lds_dwordx4 v150, s[44:45]
	s_waitcnt vmcnt(8) lgkmcnt(0)
	s_barrier
	s_setprio 1
	v_mfma_f32_16x16x32_bf16 v[62:65], v[130:133], v[186:189], v[62:65]
	v_mfma_f32_16x16x32_bf16 v[58:61], v[138:141], v[186:189], v[58:61]
	v_mfma_f32_16x16x32_bf16 v[46:49], v[130:133], v[194:197], v[46:49]
	v_mfma_f32_16x16x32_bf16 v[42:45], v[138:141], v[194:197], v[42:45]
	v_mfma_f32_16x16x32_bf16 v[30:33], v[130:133], v[202:205], v[30:33]
	v_mfma_f32_16x16x32_bf16 v[26:29], v[138:141], v[202:205], v[26:29]
	v_mfma_f32_16x16x32_bf16 v[14:17], v[130:133], v[210:213], v[14:17]
	v_mfma_f32_16x16x32_bf16 v[10:13], v[138:141], v[210:213], v[10:13]
	v_mfma_f32_16x16x32_bf16 v[62:65], v[134:137], v[190:193], v[62:65]
	v_mfma_f32_16x16x32_bf16 v[58:61], v[142:145], v[190:193], v[58:61]
	v_mfma_f32_16x16x32_bf16 v[46:49], v[134:137], v[198:201], v[46:49]
	v_mfma_f32_16x16x32_bf16 v[42:45], v[142:145], v[198:201], v[42:45]
	v_mfma_f32_16x16x32_bf16 v[30:33], v[134:137], v[206:209], v[30:33]
	v_mfma_f32_16x16x32_bf16 v[26:29], v[142:145], v[206:209], v[26:29]
	v_mfma_f32_16x16x32_bf16 v[14:17], v[134:137], v[214:217], v[14:17]
	v_mfma_f32_16x16x32_bf16 v[10:13], v[142:145], v[214:217], v[10:13]
	s_setprio 0
	s_setprio 1
	v_mfma_f32_16x16x32_bf16 v[54:57], v[164:167], v[186:189], v[54:57]
	v_mfma_f32_16x16x32_bf16 v[50:53], v[178:181], v[186:189], v[50:53]
	v_mfma_f32_16x16x32_bf16 v[38:41], v[164:167], v[194:197], v[38:41]
	v_mfma_f32_16x16x32_bf16 v[34:37], v[178:181], v[194:197], v[34:37]
	v_mfma_f32_16x16x32_bf16 v[22:25], v[164:167], v[202:205], v[22:25]
	v_mfma_f32_16x16x32_bf16 v[18:21], v[178:181], v[202:205], v[18:21]
	v_mfma_f32_16x16x32_bf16 v[6:9], v[164:167], v[210:213], v[6:9]
	v_mfma_f32_16x16x32_bf16 v[2:5], v[178:181], v[210:213], v[2:5]
	v_mfma_f32_16x16x32_bf16 v[54:57], v[168:171], v[190:193], v[54:57]
	v_mfma_f32_16x16x32_bf16 v[50:53], v[182:185], v[190:193], v[50:53]
	v_mfma_f32_16x16x32_bf16 v[38:41], v[168:171], v[198:201], v[38:41]
	v_mfma_f32_16x16x32_bf16 v[34:37], v[182:185], v[198:201], v[34:37]
	v_mfma_f32_16x16x32_bf16 v[22:25], v[168:171], v[206:209], v[22:25]
	v_mfma_f32_16x16x32_bf16 v[18:21], v[182:185], v[206:209], v[18:21]
	v_mfma_f32_16x16x32_bf16 v[6:9], v[168:171], v[214:217], v[6:9]
	v_mfma_f32_16x16x32_bf16 v[2:5], v[182:185], v[214:217], v[2:5]
	s_setprio 0
	s_barrier
; #define PG8_STAGE(bufoff, gbase, voff) do { _Pragma("unroll") for (int _i = 0; _i < 2; ++_i) \
;         __builtin_amdgcn_global_load_lds((const unsigned*)((const char*)(gbase) + (voff)[_i]), (PG8_LAS unsigned*)(lds + (bufoff) + ldsw + _i * 8192), 16, 0, 0); } while (0)
; #define PG8_LDA(dst, b, h) do { if constexpr (DT != 1) { _Pragma("unroll") for (int m = 0; m < 4; ++m) _Pragma("unroll") for (int k = 0; k < 2; ++k) dst[m][k] = *(const PG8_LAS bf16x8*)(lds + PG8_SA(b, h) + aoff + m * 2048 + k * 1024); } \
;         else { _Pragma("unroll") for (int m = 0; m < 4; ++m) dst##8[m] = ld32(lds + PG8_SA(b, h) + aoff + m * 2048); } } while (0)
; #define PG8_WAIT_V(n) asm volatile("s_waitcnt vmcnt(" #n ")" ::: "memory")
; #define PG8_WAIT_L(n) asm volatile("s_waitcnt lgkmcnt(" #n ")" ::: "memory")
; #define PG8_BAR __builtin_amdgcn_s_barrier()
; #define PG8_SCHED __builtin_amdgcn_sched_barrier(0)
;     ...
;         for (int t = 0; t < nt; t += 2) {
;             const bool last = (t == nt - 2);
;             const char* a1 = cA + (size_t)(t + 1) * kstep;
;             const char* a2 = last ? nA : cA + (size_t)(t + 2) * kstep; const char* b2 = last ? nB : cB + (size_t)(t + 2) * kstep;
;             const char* a3 = a2 + kstep; const char* b3 = b2 + kstep;
;             if (last && has_next) S.a_ready(nxt);
;             if constexpr (SP2) {
;             PG8_LDB(B0, 0, 0); PG8_LDB(B1, 0, 1); PG8_SCHED; PG8_LDA(At, 0, 0); PG8_STAGE(PG8_SA(1, 1), a1 + hstepA, voffA);
;             PG8_WAIT_V(8); PG8_WAIT_L(0); PG8_BAR; PG8_MMA(0, 0, At, B0); PG8_MMA(0, 1, At, B1); PG8_BAR; PG8_SCHED;
;             PG8_LDA(At, 0, 1); PG8_STAGE(PG8_SB(0, 0), b2, voffB); PG8_STAGE(PG8_SB(0, 1), b2 + hstepB, voffB); PG8_STAGE(PG8_SA(0, 0), a2, voffA);
;             PG8_WAIT_V(8); PG8_WAIT_L(0); PG8_BAR; PG8_MMA(1, 0, At, B0); PG8_MMA(1, 1, At, B1); PG8_BAR; PG8_SCHED;
;             PG8_LDB(B0, 1, 0); PG8_LDB(B1, 1, 1); PG8_SCHED; PG8_LDA(At, 1, 0); PG8_STAGE(PG8_SA(0, 1), a2 + hstepA, voffA);
;             PG8_WAIT_V(8); PG8_WAIT_L(0); PG8_BAR; PG8_MMA(0, 0, At, B0); PG8_MMA(0, 1, At, B1); PG8_BAR; PG8_SCHED;
;             PG8_LDA(At, 1, 1); PG8_STAGE(PG8_SB(1, 0), b3, voffB); PG8_STAGE(PG8_SB(1, 1), b3 + hstepB, voffB); PG8_STAGE(PG8_SA(1, 0), a3, voffA);
;             PG8_WAIT_V(8); PG8_WAIT_L(0); PG8_BAR; PG8_MMA(1, 0, At, B0); PG8_MMA(1, 1, At, B1); PG8_BAR; PG8_SCHED;
	ds_read_b128 v[130:133], v176
	ds_read_b128 v[134:137], v176 offset:1024
	ds_read_b128 v[138:141], v176 offset:2048
	ds_read_b128 v[142:145], v176 offset:3072
	ds_read_b128 v[164:167], v177
	ds_read_b128 v[168:171], v177 offset:1024
	ds_read_b128 v[178:181], v177 offset:2048
	ds_read_b128 v[182:185], v177 offset:3072
	s_add_u32 s44, s44, 0x10000
	s_addc_u32 s45, s45, 0
	s_mov_b32 m0, s58
	ds_read_b128 v[186:189], v175 offset:32768
	ds_read_b128 v[190:193], v175 offset:33792
	ds_read_b128 v[194:197], v175 offset:34816
	ds_read_b128 v[198:201], v175 offset:35840
	ds_read_b128 v[202:205], v175 offset:36864
	ds_read_b128 v[206:209], v175 offset:37888
	ds_read_b128 v[210:213], v175 offset:38912
	ds_read_b128 v[214:217], v175 offset:39936
	global_load_lds_dwordx4 v146, s[44:45]
	s_mov_b32 m0, s59
	s_nop 0
	global_load_lds_dwordx4 v150, s[44:45]
	s_waitcnt vmcnt(8) lgkmcnt(0)
	s_barrier
	s_setprio 1
	v_mfma_f32_16x16x32_bf16 v[126:129], v[130:133], v[186:189], v[126:129]
	v_mfma_f32_16x16x32_bf16 v[122:125], v[138:141], v[186:189], v[122:125]
	v_mfma_f32_16x16x32_bf16 v[110:113], v[130:133], v[194:197], v[110:113]
	v_mfma_f32_16x16x32_bf16 v[106:109], v[138:141], v[194:197], v[106:109]
	v_mfma_f32_16x16x32_bf16 v[94:97], v[130:133], v[202:205], v[94:97]
	v_mfma_f32_16x16x32_bf16 v[90:93], v[138:141], v[202:205], v[90:93]
	v_mfma_f32_16x16x32_bf16 v[78:81], v[130:133], v[210:213], v[78:81]
	v_mfma_f32_16x16x32_bf16 v[74:77], v[138:141], v[210:213], v[74:77]
	v_mfma_f32_16x16x32_bf16 v[126:129], v[134:137], v[190:193], v[126:129]
	v_mfma_f32_16x16x32_bf16 v[122:125], v[142:145], v[190:193], v[122:125]
	v_mfma_f32_16x16x32_bf16 v[110:113], v[134:137], v[198:201], v[110:113]
	v_mfma_f32_16x16x32_bf16 v[106:109], v[142:145], v[198:201], v[106:109]
	v_mfma_f32_16x16x32_bf16 v[94:97], v[134:137], v[206:209], v[94:97]
	v_mfma_f32_16x16x32_bf16 v[90:93], v[142:145], v[206:209], v[90:93]
	v_mfma_f32_16x16x32_bf16 v[78:81], v[134:137], v[214:217], v[78:81]
	v_mfma_f32_16x16x32_bf16 v[74:77], v[142:145], v[214:217], v[74:77]
	s_setprio 0
	s_setprio 1
	v_mfma_f32_16x16x32_bf16 v[118:121], v[164:167], v[186:189], v[118:121]
	v_mfma_f32_16x16x32_bf16 v[114:117], v[178:181], v[186:189], v[114:117]
	v_mfma_f32_16x16x32_bf16 v[102:105], v[164:167], v[194:197], v[102:105]
	v_mfma_f32_16x16x32_bf16 v[98:101], v[178:181], v[194:197], v[98:101]
	v_mfma_f32_16x16x32_bf16 v[86:89], v[164:167], v[202:205], v[86:89]
	v_mfma_f32_16x16x32_bf16 v[82:85], v[178:181], v[202:205], v[82:85]
	v_mfma_f32_16x16x32_bf16 v[70:73], v[164:167], v[210:213], v[70:73]
	v_mfma_f32_16x16x32_bf16 v[66:69], v[178:181], v[210:213], v[66:69]
	v_mfma_f32_16x16x32_bf16 v[118:121], v[168:171], v[190:193], v[118:121]
	v_mfma_f32_16x16x32_bf16 v[114:117], v[182:185], v[190:193], v[114:117]
	v_mfma_f32_16x16x32_bf16 v[102:105], v[168:171], v[198:201], v[102:105]
	v_mfma_f32_16x16x32_bf16 v[98:101], v[182:185], v[198:201], v[98:101]
	v_mfma_f32_16x16x32_bf16 v[86:89], v[168:171], v[206:209], v[86:89]
	v_mfma_f32_16x16x32_bf16 v[82:85], v[182:185], v[206:209], v[82:85]
	v_mfma_f32_16x16x32_bf16 v[70:73], v[168:171], v[214:217], v[70:73]
	v_mfma_f32_16x16x32_bf16 v[66:69], v[182:185], v[214:217], v[66:69]
	s_setprio 0
	s_barrier
	s_mov_b32 m0, s66
	s_add_u32 s42, s42, 0x10080
	ds_read_b128 v[186:189], v175 offset:49152
	ds_read_b128 v[190:193], v175 offset:50176
	ds_read_b128 v[194:197], v175 offset:51200
	ds_read_b128 v[198:201], v175 offset:52224
	ds_read_b128 v[202:205], v175 offset:53248
	ds_read_b128 v[206:209], v175 offset:54272
	ds_read_b128 v[210:213], v175 offset:55296
	ds_read_b128 v[214:217], v175 offset:56320
	global_load_lds_dwordx4 v148, s[98:99]
	s_mov_b32 m0, s67
	s_addc_u32 s43, s43, 0
	global_load_lds_dwordx4 v152, s[98:99]
	s_mov_b32 m0, s70
	s_nop 0
	global_load_lds_dwordx4 v148, s[42:43]
	s_mov_b32 m0, s71
	s_nop 0
	global_load_lds_dwordx4 v152, s[42:43]
	s_mov_b32 m0, s68
	s_nop 0
	global_load_lds_dwordx4 v146, s[100:101]
	s_mov_b32 m0, s69
	s_nop 0
	global_load_lds_dwordx4 v150, s[100:101]
	s_waitcnt vmcnt(8) lgkmcnt(0)
	s_barrier
	s_setprio 1
	v_mfma_f32_16x16x32_bf16 v[62:65], v[130:133], v[186:189], v[62:65]
	v_mfma_f32_16x16x32_bf16 v[58:61], v[138:141], v[186:189], v[58:61]
	v_mfma_f32_16x16x32_bf16 v[46:49], v[130:133], v[194:197], v[46:49]
	v_mfma_f32_16x16x32_bf16 v[42:45], v[138:141], v[194:197], v[42:45]
	v_mfma_f32_16x16x32_bf16 v[30:33], v[130:133], v[202:205], v[30:33]
	v_mfma_f32_16x16x32_bf16 v[26:29], v[138:141], v[202:205], v[26:29]
	v_mfma_f32_16x16x32_bf16 v[14:17], v[130:133], v[210:213], v[14:17]
	v_mfma_f32_16x16x32_bf16 v[10:13], v[138:141], v[210:213], v[10:13]
	v_mfma_f32_16x16x32_bf16 v[62:65], v[134:137], v[190:193], v[62:65]
	v_mfma_f32_16x16x32_bf16 v[58:61], v[142:145], v[190:193], v[58:61]
	v_mfma_f32_16x16x32_bf16 v[46:49], v[134:137], v[198:201], v[46:49]
	v_mfma_f32_16x16x32_bf16 v[42:45], v[142:145], v[198:201], v[42:45]
	v_mfma_f32_16x16x32_bf16 v[30:33], v[134:137], v[206:209], v[30:33]
	v_mfma_f32_16x16x32_bf16 v[26:29], v[142:145], v[206:209], v[26:29]
	v_mfma_f32_16x16x32_bf16 v[14:17], v[134:137], v[214:217], v[14:17]
	v_mfma_f32_16x16x32_bf16 v[10:13], v[142:145], v[214:217], v[10:13]
	s_setprio 0
	s_setprio 1
	v_mfma_f32_16x16x32_bf16 v[54:57], v[164:167], v[186:189], v[54:57]
	v_mfma_f32_16x16x32_bf16 v[50:53], v[178:181], v[186:189], v[50:53]
	v_mfma_f32_16x16x32_bf16 v[38:41], v[164:167], v[194:197], v[38:41]
	v_mfma_f32_16x16x32_bf16 v[34:37], v[178:181], v[194:197], v[34:37]
	v_mfma_f32_16x16x32_bf16 v[22:25], v[164:167], v[202:205], v[22:25]
	v_mfma_f32_16x16x32_bf16 v[18:21], v[178:181], v[202:205], v[18:21]
	v_mfma_f32_16x16x32_bf16 v[6:9], v[164:167], v[210:213], v[6:9]
	v_mfma_f32_16x16x32_bf16 v[2:5], v[178:181], v[210:213], v[2:5]
	v_mfma_f32_16x16x32_bf16 v[54:57], v[168:171], v[190:193], v[54:57]
	v_mfma_f32_16x16x32_bf16 v[50:53], v[182:185], v[190:193], v[50:53]
	v_mfma_f32_16x16x32_bf16 v[38:41], v[168:171], v[198:201], v[38:41]
	v_mfma_f32_16x16x32_bf16 v[34:37], v[182:185], v[198:201], v[34:37]
	v_mfma_f32_16x16x32_bf16 v[22:25], v[168:171], v[206:209], v[22:25]
	v_mfma_f32_16x16x32_bf16 v[18:21], v[182:185], v[206:209], v[18:21]
	v_mfma_f32_16x16x32_bf16 v[6:9], v[168:171], v[214:217], v[6:9]
	v_mfma_f32_16x16x32_bf16 v[2:5], v[182:185], v[214:217], v[2:5]
	s_setprio 0
	s_barrier
	s_add_u32 s76, s76, 0x100
	s_addc_u32 s77, s77, 0
	s_add_u32 s40, s40, 0x100
	s_addc_u32 s41, s41, 0
	s_cmp_ge_i32 s78, s65
	s_mov_b32 s42, s78
	s_cbranch_scc0 .LBB0_3356
	v_readlane_b32 s76, v247, 9

; #define PG8_STAGE(bufoff, gbase, voff) do { _Pragma("unroll") for (int _i = 0; _i < 2; ++_i) \
;         __builtin_amdgcn_global_load_lds((const unsigned*)((const char*)(gbase) + (voff)[_i]), (PG8_LAS unsigned*)(lds + (bufoff) + ldsw + _i * 8192), 16, 0, 0); } while (0)
; #define PG8_LDA(dst, b, h) do { if constexpr (DT != 1) { _Pragma("unroll") for (int m = 0; m < 4; ++m) _Pragma("unroll") for (int k = 0; k < 2; ++k) dst[m][k] = *(const PG8_LAS bf16x8*)(lds + PG8_SA(b, h) + aoff + m * 2048 + k * 1024); } \
;         else { _Pragma("unroll") for (int m = 0; m < 4; ++m) dst##8[m] = ld32(lds + PG8_SA(b, h) + aoff + m * 2048); } } while (0)
; #define PG8_WAIT_V(n) asm volatile("s_waitcnt vmcnt(" #n ")" ::: "memory")
; #define PG8_WAIT_L(n) asm volatile("s_waitcnt lgkmcnt(" #n ")" ::: "memory")
; #define PG8_BAR __builtin_amdgcn_s_barrier()
; #define PG8_SCHED __builtin_amdgcn_sched_barrier(0)
;     ...
;         for (int t = 0; t < nt; t += 2) {
;             const bool last = (t == nt - 2);
;             const char* a1 = cA + (size_t)(t + 1) * kstep;
;             const char* a2 = last ? nA : cA + (size_t)(t + 2) * kstep; const char* b2 = last ? nB : cB + (size_t)(t + 2) * kstep;
;             const char* a3 = a2 + kstep; const char* b3 = b2 + kstep;
;             if (last && has_next) S.a_ready(nxt);
;             if constexpr (SP2) {
;             PG8_LDB(B0, 0, 0); PG8_LDB(B1, 0, 1); PG8_SCHED; PG8_LDA(At, 0, 0); PG8_STAGE(PG8_SA(1, 1), a1 + hstepA, voffA);
;             PG8_WAIT_V(8); PG8_WAIT_L(0); PG8_BAR; PG8_MMA(0, 0, At, B0); PG8_MMA(0, 1, At, B1); PG8_BAR; PG8_SCHED;
;             PG8_LDA(At, 0, 1); PG8_STAGE(PG8_SB(0, 0), b2, voffB); PG8_STAGE(PG8_SB(0, 1), b2 + hstepB, voffB); PG8_STAGE(PG8_SA(0, 0), a2, voffA);
;             PG8_WAIT_V(8); PG8_WAIT_L(0); PG8_BAR; PG8_MMA(1, 0, At, B0); PG8_MMA(1, 1, At, B1); PG8_BAR; PG8_SCHED;
;             PG8_LDB(B0, 1, 0); PG8_LDB(B1, 1, 1); PG8_SCHED; PG8_LDA(At, 1, 0); PG8_STAGE(PG8_SA(0, 1), a2 + hstepA, voffA);
;             PG8_WAIT_V(8); PG8_WAIT_L(0); PG8_BAR; PG8_MMA(0, 0, At, B0); PG8_MMA(0, 1, At, B1); PG8_BAR; PG8_SCHED;
;             PG8_LDA(At, 1, 1); PG8_STAGE(PG8_SB(1, 0), b3, voffB); PG8_STAGE(PG8_SB(1, 1), b3 + hstepB, voffB); PG8_STAGE(PG8_SA(1, 0), a3, voffA);
;             PG8_WAIT_V(8); PG8_WAIT_L(0); PG8_BAR; PG8_MMA(1, 0, At, B0); PG8_MMA(1, 1, At, B1); PG8_BAR; PG8_SCHED;
.LBB0_4141:
	v_add_u32_e32 v160, s35, v164
	ds_read_b128 v[122:125], v160
	ds_read_b128 v[126:129], v160 offset:1024
	ds_read_b128 v[130:133], v160 offset:2048
	ds_read_b128 v[170:173], v160 offset:3072
	v_add_u32_e32 v160, s36, v164
	ds_read_b128 v[174:177], v160
	ds_read_b128 v[178:181], v160 offset:1024
	ds_read_b128 v[182:185], v160 offset:2048
	ds_read_b128 v[186:189], v160 offset:3072
	s_add_i32 s69, s26, 2
	s_add_u32 s27, s24, 0xfffc0080
	s_addc_u32 s28, s25, -1
	s_cmp_eq_u32 s61, s26
	s_cselect_b32 s26, s66, s67
	s_cselect_b32 s29, s15, s28
	s_cselect_b32 s28, s17, s27
	s_cselect_b32 s27, s65, s68
	s_add_i32 m0, s46, 0xc000
	ds_read_b128 v[190:193], v167
	ds_read_b128 v[194:197], v167 offset:1024
	ds_read_b128 v[198:201], v167 offset:2048
	ds_read_b128 v[202:205], v167 offset:3072
	ds_read_b128 v[206:209], v167 offset:4096
	ds_read_b128 v[210:213], v167 offset:5120
	ds_read_b128 v[214:217], v167 offset:6144
	ds_read_b128 v[218:221], v167 offset:7168
	global_load_lds_dwordx4 v154, s[24:25]
	s_add_i32 m0, s46, 0xe000
	s_nop 0
	global_load_lds_dwordx4 v152, s[24:25]
	s_waitcnt vmcnt(8) lgkmcnt(0)
	s_barrier
	s_setprio 1
	v_mfma_i32_16x16x64_i8 v[134:137], v[122:125], v[190:193], v[134:137]
	v_mfma_i32_16x16x64_i8 v[114:117], v[130:133], v[190:193], v[114:117]
	v_mfma_i32_16x16x64_i8 v[106:109], v[122:125], v[198:201], v[106:109]
	v_mfma_i32_16x16x64_i8 v[98:101], v[130:133], v[198:201], v[98:101]
	v_mfma_i32_16x16x64_i8 v[90:93], v[122:125], v[206:209], v[90:93]
	v_mfma_i32_16x16x64_i8 v[82:85], v[130:133], v[206:209], v[82:85]
	v_mfma_i32_16x16x64_i8 v[74:77], v[122:125], v[214:217], v[74:77]
	v_mfma_i32_16x16x64_i8 v[66:69], v[130:133], v[214:217], v[66:69]
	v_mfma_i32_16x16x64_i8 v[134:137], v[126:129], v[194:197], v[134:137]
	v_mfma_i32_16x16x64_i8 v[114:117], v[170:173], v[194:197], v[114:117]
	v_mfma_i32_16x16x64_i8 v[106:109], v[126:129], v[202:205], v[106:109]
	v_mfma_i32_16x16x64_i8 v[98:101], v[170:173], v[202:205], v[98:101]
	v_mfma_i32_16x16x64_i8 v[90:93], v[126:129], v[210:213], v[90:93]
	v_mfma_i32_16x16x64_i8 v[82:85], v[170:173], v[210:213], v[82:85]
	v_mfma_i32_16x16x64_i8 v[74:77], v[126:129], v[218:221], v[74:77]
	v_mfma_i32_16x16x64_i8 v[66:69], v[170:173], v[218:221], v[66:69]
	s_setprio 0
	s_setprio 1
	v_mfma_i32_16x16x64_i8 v[138:141], v[174:177], v[190:193], v[138:141]
	v_mfma_i32_16x16x64_i8 v[118:121], v[182:185], v[190:193], v[118:121]
	v_mfma_i32_16x16x64_i8 v[110:113], v[174:177], v[198:201], v[110:113]
	v_mfma_i32_16x16x64_i8 v[102:105], v[182:185], v[198:201], v[102:105]
	v_mfma_i32_16x16x64_i8 v[94:97], v[174:177], v[206:209], v[94:97]
	v_mfma_i32_16x16x64_i8 v[86:89], v[182:185], v[206:209], v[86:89]
	v_mfma_i32_16x16x64_i8 v[78:81], v[174:177], v[214:217], v[78:81]
	v_mfma_i32_16x16x64_i8 v[70:73], v[182:185], v[214:217], v[70:73]
	v_mfma_i32_16x16x64_i8 v[138:141], v[178:181], v[194:197], v[138:141]
	v_mfma_i32_16x16x64_i8 v[118:121], v[186:189], v[194:197], v[118:121]
	v_mfma_i32_16x16x64_i8 v[110:113], v[178:181], v[202:205], v[110:113]
	v_mfma_i32_16x16x64_i8 v[102:105], v[186:189], v[202:205], v[102:105]
	v_mfma_i32_16x16x64_i8 v[94:97], v[178:181], v[210:213], v[94:97]
	v_mfma_i32_16x16x64_i8 v[86:89], v[186:189], v[210:213], v[86:89]
	v_mfma_i32_16x16x64_i8 v[78:81], v[178:181], v[218:221], v[78:81]
	v_mfma_i32_16x16x64_i8 v[70:73], v[186:189], v[218:221], v[70:73]
	s_setprio 0
	s_barrier
	s_mov_b32 m0, s23
	s_add_u32 s98, s26, 0x80
	s_addc_u32 s99, s27, 0
	s_add_u32 s70, s26, 0x40000
	ds_read_b128 v[190:193], v167 offset:16384
	ds_read_b128 v[194:197], v167 offset:17408
	ds_read_b128 v[198:201], v167 offset:18432
	ds_read_b128 v[202:205], v167 offset:19456
	ds_read_b128 v[206:209], v167 offset:20480
	ds_read_b128 v[210:213], v167 offset:21504
	ds_read_b128 v[214:217], v167 offset:22528
	ds_read_b128 v[218:221], v167 offset:23552
	global_load_lds_dwordx4 v144, s[26:27]
	s_mov_b32 m0, s43
	s_addc_u32 s71, s27, 0
	global_load_lds_dwordx4 v148, s[26:27]
	s_mov_b32 m0, s44
	s_nop 0
	global_load_lds_dwordx4 v144, s[70:71]
	s_mov_b32 m0, s45
	s_nop 0
	global_load_lds_dwordx4 v148, s[70:71]
	s_add_u32 s100, s28, 0x80
	s_addc_u32 s101, s29, 0
	s_mov_b32 m0, s46
	s_nop 0
	global_load_lds_dwordx4 v142, s[28:29]
	s_mov_b32 m0, s47
	s_nop 0
	global_load_lds_dwordx4 v146, s[28:29]
	s_waitcnt vmcnt(8) lgkmcnt(0)
	s_barrier
	s_setprio 1
	v_mfma_i32_16x16x64_i8 v[58:61], v[122:125], v[190:193], v[58:61]
	v_mfma_i32_16x16x64_i8 v[50:53], v[130:133], v[190:193], v[50:53]
	v_mfma_i32_16x16x64_i8 v[42:45], v[122:125], v[198:201], v[42:45]
	v_mfma_i32_16x16x64_i8 v[34:37], v[130:133], v[198:201], v[34:37]
	v_mfma_i32_16x16x64_i8 v[26:29], v[122:125], v[206:209], v[26:29]
	v_mfma_i32_16x16x64_i8 v[18:21], v[130:133], v[206:209], v[18:21]
	v_mfma_i32_16x16x64_i8 v[10:13], v[122:125], v[214:217], v[10:13]
	v_mfma_i32_16x16x64_i8 v[2:5], v[130:133], v[214:217], v[2:5]
	v_mfma_i32_16x16x64_i8 v[58:61], v[126:129], v[194:197], v[58:61]
	v_mfma_i32_16x16x64_i8 v[50:53], v[170:173], v[194:197], v[50:53]
	v_mfma_i32_16x16x64_i8 v[42:45], v[126:129], v[202:205], v[42:45]
	v_mfma_i32_16x16x64_i8 v[34:37], v[170:173], v[202:205], v[34:37]
	v_mfma_i32_16x16x64_i8 v[26:29], v[126:129], v[210:213], v[26:29]
	v_mfma_i32_16x16x64_i8 v[18:21], v[170:173], v[210:213], v[18:21]
	v_mfma_i32_16x16x64_i8 v[10:13], v[126:129], v[218:221], v[10:13]
	v_mfma_i32_16x16x64_i8 v[2:5], v[170:173], v[218:221], v[2:5]
	s_setprio 0
	s_setprio 1
	v_mfma_i32_16x16x64_i8 v[62:65], v[174:177], v[190:193], v[62:65]
	v_mfma_i32_16x16x64_i8 v[54:57], v[182:185], v[190:193], v[54:57]
	v_mfma_i32_16x16x64_i8 v[46:49], v[174:177], v[198:201], v[46:49]
	v_mfma_i32_16x16x64_i8 v[38:41], v[182:185], v[198:201], v[38:41]
	v_mfma_i32_16x16x64_i8 v[30:33], v[174:177], v[206:209], v[30:33]
	v_mfma_i32_16x16x64_i8 v[22:25], v[182:185], v[206:209], v[22:25]
	v_mfma_i32_16x16x64_i8 v[14:17], v[174:177], v[214:217], v[14:17]
	v_mfma_i32_16x16x64_i8 v[6:9], v[182:185], v[214:217], v[6:9]
	v_mfma_i32_16x16x64_i8 v[62:65], v[178:181], v[194:197], v[62:65]
	v_mfma_i32_16x16x64_i8 v[54:57], v[186:189], v[194:197], v[54:57]
	v_mfma_i32_16x16x64_i8 v[46:49], v[178:181], v[202:205], v[46:49]
	v_mfma_i32_16x16x64_i8 v[38:41], v[186:189], v[202:205], v[38:41]
	v_mfma_i32_16x16x64_i8 v[30:33], v[178:181], v[210:213], v[30:33]
	v_mfma_i32_16x16x64_i8 v[22:25], v[186:189], v[210:213], v[22:25]
	v_mfma_i32_16x16x64_i8 v[14:17], v[178:181], v[218:221], v[14:17]
	v_mfma_i32_16x16x64_i8 v[6:9], v[186:189], v[218:221], v[6:9]
	s_setprio 0
	s_barrier
; #define PG8_STAGE(bufoff, gbase, voff) do { _Pragma("unroll") for (int _i = 0; _i < 2; ++_i) \
;         __builtin_amdgcn_global_load_lds((const unsigned*)((const char*)(gbase) + (voff)[_i]), (PG8_LAS unsigned*)(lds + (bufoff) + ldsw + _i * 8192), 16, 0, 0); } while (0)
; #define PG8_LDA(dst, b, h) do { if constexpr (DT != 1) { _Pragma("unroll") for (int m = 0; m < 4; ++m) _Pragma("unroll") for (int k = 0; k < 2; ++k) dst[m][k] = *(const PG8_LAS bf16x8*)(lds + PG8_SA(b, h) + aoff + m * 2048 + k * 1024); } \
;         else { _Pragma("unroll") for (int m = 0; m < 4; ++m) dst##8[m] = ld32(lds + PG8_SA(b, h) + aoff + m * 2048); } } while (0)
; #define PG8_WAIT_V(n) asm volatile("s_waitcnt vmcnt(" #n ")" ::: "memory")
; #define PG8_WAIT_L(n) asm volatile("s_waitcnt lgkmcnt(" #n ")" ::: "memory")
; #define PG8_BAR __builtin_amdgcn_s_barrier()
; #define PG8_SCHED __builtin_amdgcn_sched_barrier(0)
;     ...
;         for (int t = 0; t < nt; t += 2) {
;             const bool last = (t == nt - 2);
;             const char* a1 = cA + (size_t)(t + 1) * kstep;
;             const char* a2 = last ? nA : cA + (size_t)(t + 2) * kstep; const char* b2 = last ? nB : cB + (size_t)(t + 2) * kstep;
;             const char* a3 = a2 + kstep; const char* b3 = b2 + kstep;
;             if (last && has_next) S.a_ready(nxt);
;             if constexpr (SP2) {
;             PG8_LDB(B0, 0, 0); PG8_LDB(B1, 0, 1); PG8_SCHED; PG8_LDA(At, 0, 0); PG8_STAGE(PG8_SA(1, 1), a1 + hstepA, voffA);
;             PG8_WAIT_V(8); PG8_WAIT_L(0); PG8_BAR; PG8_MMA(0, 0, At, B0); PG8_MMA(0, 1, At, B1); PG8_BAR; PG8_SCHED;
;             PG8_LDA(At, 0, 1); PG8_STAGE(PG8_SB(0, 0), b2, voffB); PG8_STAGE(PG8_SB(0, 1), b2 + hstepB, voffB); PG8_STAGE(PG8_SA(0, 0), a2, voffA);
;             PG8_WAIT_V(8); PG8_WAIT_L(0); PG8_BAR; PG8_MMA(1, 0, At, B0); PG8_MMA(1, 1, At, B1); PG8_BAR; PG8_SCHED;
;             PG8_LDB(B0, 1, 0); PG8_LDB(B1, 1, 1); PG8_SCHED; PG8_LDA(At, 1, 0); PG8_STAGE(PG8_SA(0, 1), a2 + hstepA, voffA);
;             PG8_WAIT_V(8); PG8_WAIT_L(0); PG8_BAR; PG8_MMA(0, 0, At, B0); PG8_MMA(0, 1, At, B1); PG8_BAR; PG8_SCHED;
;             PG8_LDA(At, 1, 1); PG8_STAGE(PG8_SB(1, 0), b3, voffB); PG8_STAGE(PG8_SB(1, 1), b3 + hstepB, voffB); PG8_STAGE(PG8_SA(1, 0), a3, voffA);
;             PG8_WAIT_V(8); PG8_WAIT_L(0); PG8_BAR; PG8_MMA(1, 0, At, B0); PG8_MMA(1, 1, At, B1); PG8_BAR; PG8_SCHED;
	v_add_u32_e32 v160, s51, v164
	ds_read_b128 v[122:125], v160
	ds_read_b128 v[126:129], v160 offset:1024
	ds_read_b128 v[130:133], v160 offset:2048
	ds_read_b128 v[170:173], v160 offset:3072
	v_add_u32_e32 v160, s52, v164
	ds_read_b128 v[174:177], v160
	ds_read_b128 v[178:181], v160 offset:1024
	ds_read_b128 v[182:185], v160 offset:2048
	ds_read_b128 v[186:189], v160 offset:3072
	s_add_u32 s28, s28, 0x40000
	s_addc_u32 s29, s29, 0
	s_mov_b32 m0, s48
	ds_read_b128 v[190:193], v167 offset:32768
	ds_read_b128 v[194:197], v167 offset:33792
	ds_read_b128 v[198:201], v167 offset:34816
	ds_read_b128 v[202:205], v167 offset:35840
	ds_read_b128 v[206:209], v167 offset:36864
	ds_read_b128 v[210:213], v167 offset:37888
	ds_read_b128 v[214:217], v167 offset:38912
	ds_read_b128 v[218:221], v167 offset:39936
	global_load_lds_dwordx4 v142, s[28:29]
	s_mov_b32 m0, s49
	s_nop 0
	global_load_lds_dwordx4 v146, s[28:29]
	s_waitcnt vmcnt(8) lgkmcnt(0)
	s_barrier
	s_setprio 1
	v_mfma_i32_16x16x64_i8 v[134:137], v[122:125], v[190:193], v[134:137]
	v_mfma_i32_16x16x64_i8 v[114:117], v[130:133], v[190:193], v[114:117]
	v_mfma_i32_16x16x64_i8 v[106:109], v[122:125], v[198:201], v[106:109]
	v_mfma_i32_16x16x64_i8 v[98:101], v[130:133], v[198:201], v[98:101]
	v_mfma_i32_16x16x64_i8 v[90:93], v[122:125], v[206:209], v[90:93]
	v_mfma_i32_16x16x64_i8 v[82:85], v[130:133], v[206:209], v[82:85]
	v_mfma_i32_16x16x64_i8 v[74:77], v[122:125], v[214:217], v[74:77]
	v_mfma_i32_16x16x64_i8 v[66:69], v[130:133], v[214:217], v[66:69]
	v_mfma_i32_16x16x64_i8 v[134:137], v[126:129], v[194:197], v[134:137]
	v_mfma_i32_16x16x64_i8 v[114:117], v[170:173], v[194:197], v[114:117]
	v_mfma_i32_16x16x64_i8 v[106:109], v[126:129], v[202:205], v[106:109]
	v_mfma_i32_16x16x64_i8 v[98:101], v[170:173], v[202:205], v[98:101]
	v_mfma_i32_16x16x64_i8 v[90:93], v[126:129], v[210:213], v[90:93]
	v_mfma_i32_16x16x64_i8 v[82:85], v[170:173], v[210:213], v[82:85]
	v_mfma_i32_16x16x64_i8 v[74:77], v[126:129], v[218:221], v[74:77]
	v_mfma_i32_16x16x64_i8 v[66:69], v[170:173], v[218:221], v[66:69]
	s_setprio 0
	s_setprio 1
	v_mfma_i32_16x16x64_i8 v[138:141], v[174:177], v[190:193], v[138:141]
	v_mfma_i32_16x16x64_i8 v[118:121], v[182:185], v[190:193], v[118:121]
	v_mfma_i32_16x16x64_i8 v[110:113], v[174:177], v[198:201], v[110:113]
	v_mfma_i32_16x16x64_i8 v[102:105], v[182:185], v[198:201], v[102:105]
	v_mfma_i32_16x16x64_i8 v[94:97], v[174:177], v[206:209], v[94:97]
	v_mfma_i32_16x16x64_i8 v[86:89], v[182:185], v[206:209], v[86:89]
	v_mfma_i32_16x16x64_i8 v[78:81], v[174:177], v[214:217], v[78:81]
	v_mfma_i32_16x16x64_i8 v[70:73], v[182:185], v[214:217], v[70:73]
	v_mfma_i32_16x16x64_i8 v[138:141], v[178:181], v[194:197], v[138:141]
	v_mfma_i32_16x16x64_i8 v[118:121], v[186:189], v[194:197], v[118:121]
	v_mfma_i32_16x16x64_i8 v[110:113], v[178:181], v[202:205], v[110:113]
	v_mfma_i32_16x16x64_i8 v[102:105], v[186:189], v[202:205], v[102:105]
	v_mfma_i32_16x16x64_i8 v[94:97], v[178:181], v[210:213], v[94:97]
	v_mfma_i32_16x16x64_i8 v[86:89], v[186:189], v[210:213], v[86:89]
	v_mfma_i32_16x16x64_i8 v[78:81], v[178:181], v[218:221], v[78:81]
	v_mfma_i32_16x16x64_i8 v[70:73], v[186:189], v[218:221], v[70:73]
	s_setprio 0
	s_barrier
	s_mov_b32 m0, s55
	s_add_u32 s26, s26, 0x40080
	ds_read_b128 v[190:193], v167 offset:49152
	ds_read_b128 v[194:197], v167 offset:50176
	ds_read_b128 v[198:201], v167 offset:51200
	ds_read_b128 v[202:205], v167 offset:52224
	ds_read_b128 v[206:209], v167 offset:53248
	ds_read_b128 v[210:213], v167 offset:54272
	ds_read_b128 v[214:217], v167 offset:55296
	ds_read_b128 v[218:221], v167 offset:56320
	global_load_lds_dwordx4 v144, s[98:99]
	s_mov_b32 m0, s56
	s_addc_u32 s27, s27, 0
	global_load_lds_dwordx4 v148, s[98:99]
	s_mov_b32 m0, s59
	s_nop 0
	global_load_lds_dwordx4 v144, s[26:27]
	s_mov_b32 m0, s60
	s_nop 0
	global_load_lds_dwordx4 v148, s[26:27]
	s_mov_b32 m0, s57
	s_nop 0
	global_load_lds_dwordx4 v142, s[100:101]
	s_mov_b32 m0, s58
	s_nop 0
	global_load_lds_dwordx4 v146, s[100:101]
	s_waitcnt vmcnt(8) lgkmcnt(0)
	s_barrier
	s_setprio 1
	v_mfma_i32_16x16x64_i8 v[58:61], v[122:125], v[190:193], v[58:61]
	v_mfma_i32_16x16x64_i8 v[50:53], v[130:133], v[190:193], v[50:53]
	v_mfma_i32_16x16x64_i8 v[42:45], v[122:125], v[198:201], v[42:45]
	v_mfma_i32_16x16x64_i8 v[34:37], v[130:133], v[198:201], v[34:37]
	v_mfma_i32_16x16x64_i8 v[26:29], v[122:125], v[206:209], v[26:29]
	v_mfma_i32_16x16x64_i8 v[18:21], v[130:133], v[206:209], v[18:21]
	v_mfma_i32_16x16x64_i8 v[10:13], v[122:125], v[214:217], v[10:13]
	v_mfma_i32_16x16x64_i8 v[2:5], v[130:133], v[214:217], v[2:5]
	v_mfma_i32_16x16x64_i8 v[58:61], v[126:129], v[194:197], v[58:61]
	v_mfma_i32_16x16x64_i8 v[50:53], v[170:173], v[194:197], v[50:53]
	v_mfma_i32_16x16x64_i8 v[42:45], v[126:129], v[202:205], v[42:45]
	v_mfma_i32_16x16x64_i8 v[34:37], v[170:173], v[202:205], v[34:37]
	v_mfma_i32_16x16x64_i8 v[26:29], v[126:129], v[210:213], v[26:29]
	v_mfma_i32_16x16x64_i8 v[18:21], v[170:173], v[210:213], v[18:21]
	v_mfma_i32_16x16x64_i8 v[10:13], v[126:129], v[218:221], v[10:13]
	v_mfma_i32_16x16x64_i8 v[2:5], v[170:173], v[218:221], v[2:5]
	s_setprio 0
	s_setprio 1
	v_mfma_i32_16x16x64_i8 v[62:65], v[174:177], v[190:193], v[62:65]
	v_mfma_i32_16x16x64_i8 v[54:57], v[182:185], v[190:193], v[54:57]
	v_mfma_i32_16x16x64_i8 v[46:49], v[174:177], v[198:201], v[46:49]
	v_mfma_i32_16x16x64_i8 v[38:41], v[182:185], v[198:201], v[38:41]
	v_mfma_i32_16x16x64_i8 v[30:33], v[174:177], v[206:209], v[30:33]
	v_mfma_i32_16x16x64_i8 v[22:25], v[182:185], v[206:209], v[22:25]
	v_mfma_i32_16x16x64_i8 v[14:17], v[174:177], v[214:217], v[14:17]
	v_mfma_i32_16x16x64_i8 v[6:9], v[182:185], v[214:217], v[6:9]
	v_mfma_i32_16x16x64_i8 v[62:65], v[178:181], v[194:197], v[62:65]
	v_mfma_i32_16x16x64_i8 v[54:57], v[186:189], v[194:197], v[54:57]
	v_mfma_i32_16x16x64_i8 v[46:49], v[178:181], v[202:205], v[46:49]
	v_mfma_i32_16x16x64_i8 v[38:41], v[186:189], v[202:205], v[38:41]
	v_mfma_i32_16x16x64_i8 v[30:33], v[178:181], v[210:213], v[30:33]
	v_mfma_i32_16x16x64_i8 v[22:25], v[186:189], v[210:213], v[22:25]
	v_mfma_i32_16x16x64_i8 v[14:17], v[178:181], v[218:221], v[14:17]
	v_mfma_i32_16x16x64_i8 v[6:9], v[186:189], v[218:221], v[6:9]
	s_setprio 0
	s_barrier
	s_add_u32 s67, s67, 0x100
	s_addc_u32 s68, s68, 0
	s_add_u32 s24, s24, 0x100
	s_addc_u32 s25, s25, 0
	s_cmp_ge_i32 s69, s54
	s_mov_b32 s26, s69
	s_cbranch_scc0 .LBB0_4141

; #define PG8_STAGE(bufoff, gbase, voff) do { _Pragma("unroll") for (int _i = 0; _i < 2; ++_i) \
;         __builtin_amdgcn_global_load_lds((const unsigned*)((const char*)(gbase) + (voff)[_i]), (PG8_LAS unsigned*)(lds + (bufoff) + ldsw + _i * 8192), 16, 0, 0); } while (0)
; #define PG8_LDA(dst, b, h) do { if constexpr (DT != 1) { _Pragma("unroll") for (int m = 0; m < 4; ++m) _Pragma("unroll") for (int k = 0; k < 2; ++k) dst[m][k] = *(const PG8_LAS bf16x8*)(lds + PG8_SA(b, h) + aoff + m * 2048 + k * 1024); } \
;         else { _Pragma("unroll") for (int m = 0; m < 4; ++m) dst##8[m] = ld32(lds + PG8_SA(b, h) + aoff + m * 2048); } } while (0)
; #define PG8_LDB(dst, b, h) do { if constexpr (DT != 1) { _Pragma("unroll") for (int n = 0; n < 2; ++n) _Pragma("unroll") for (int k = 0; k < 2; ++k) dst[n][k] = *(const PG8_LAS bf16x8*)(lds + PG8_SB(b, h) + boff + n * 2048 + k * 1024); } \
;         else { _Pragma("unroll") for (int n = 0; n < 2; ++n) dst##8[n] = ld32(lds + PG8_SB(b, h) + boff + n * 2048); } } while (0)
; #define PG8_WAIT_V(n) asm volatile("s_waitcnt vmcnt(" #n ")" ::: "memory")
; #define PG8_WAIT_L(n) asm volatile("s_waitcnt lgkmcnt(" #n ")" ::: "memory")
; #define PG8_BAR __builtin_amdgcn_s_barrier()
; #define PG8_SCHED __builtin_amdgcn_sched_barrier(0)
;     ...
;             PG8_LDB(B0, 0, 0); PG8_LDB(B1, 0, 1); PG8_SCHED; PG8_LDA(At, 0, 0); PG8_STAGE(PG8_SA(1, 1), a1 + hstepA, voffA);
;             PG8_WAIT_V(8); PG8_WAIT_L(0); PG8_BAR; PG8_MMA(0, 0, At, B0); PG8_MMA(0, 1, At, B1); PG8_BAR; PG8_SCHED;
;             PG8_LDA(At, 0, 1); PG8_STAGE(PG8_SB(0, 0), b2, voffB); PG8_STAGE(PG8_SB(0, 1), b2 + hstepB, voffB); PG8_STAGE(PG8_SA(0, 0), a2, voffA);
;             PG8_WAIT_V(8); PG8_WAIT_L(0); PG8_BAR; PG8_MMA(1, 0, At, B0); PG8_MMA(1, 1, At, B1); PG8_BAR; PG8_SCHED;
;             PG8_LDB(B0, 1, 0); PG8_LDB(B1, 1, 1); PG8_SCHED; PG8_LDA(At, 1, 0); PG8_STAGE(PG8_SA(0, 1), a2 + hstepA, voffA);
;             PG8_WAIT_V(8); PG8_WAIT_L(0); PG8_BAR; PG8_MMA(0, 0, At, B0); PG8_MMA(0, 1, At, B1); PG8_BAR; PG8_SCHED;
;             PG8_LDA(At, 1, 1); PG8_STAGE(PG8_SB(1, 0), b3, voffB); PG8_STAGE(PG8_SB(1, 1), b3 + hstepB, voffB); PG8_STAGE(PG8_SA(1, 0), a3, voffA);
;             PG8_WAIT_V(8); PG8_WAIT_L(0); PG8_BAR; PG8_MMA(1, 0, At, B0); PG8_MMA(1, 1, At, B1); PG8_BAR; PG8_SCHED;
.LBB0_4217:
	ds_read_b128 v[18:21], v187
	ds_read_b128 v[22:25], v187 offset:16
	ds_read_b128 v[26:29], v187 offset:2048
	ds_read_b128 v[30:33], v187 offset:2064
	ds_read_b128 v[2:5], v188
	ds_read_b128 v[6:9], v188 offset:16
	ds_read_b128 v[10:13], v188 offset:2048
	ds_read_b128 v[14:17], v188 offset:2064
	s_add_i32 s68, s34, 2
	s_add_u32 s30, s28, 0x100
	s_addc_u32 s31, s29, 0
	s_cmp_eq_u32 s59, s34
	s_cselect_b32 s34, s26, s66
	s_cselect_b32 s37, s3, s31
	s_cselect_b32 s36, s2, s30
	s_cselect_b32 s35, s27, s67
	v_lshl_add_u64 v[218:219], s[28:29], 0, v[172:173]
	s_add_i32 m0, s47, 0xc000
	ds_read_b128 v[178:181], v189
	ds_read_b128 v[182:185], v189 offset:16
	ds_read_b128 v[194:197], v189 offset:2048
	ds_read_b128 v[198:201], v189 offset:2064
	ds_read_b128 v[202:205], v189 offset:4096
	ds_read_b128 v[206:209], v189 offset:4112
	ds_read_b128 v[210:213], v189 offset:6144
	ds_read_b128 v[214:217], v189 offset:6160
	global_load_lds_dwordx4 v[218:219], off
	v_lshl_add_u64 v[218:219], s[28:29], 0, v[170:171]
	s_add_i32 m0, s47, 0xe000
	s_nop 0
	global_load_lds_dwordx4 v[218:219], off
	s_waitcnt vmcnt(8) lgkmcnt(0)
	s_barrier
	s_setprio 1
	v_mfma_scale_f32_16x16x128_f8f6f4 v[158:161], v[18:25], v[178:185], v[158:161], v190, v190 op_sel_hi:[0,0,0]
	v_mfma_scale_f32_16x16x128_f8f6f4 v[154:157], v[26:33], v[178:185], v[154:157], v190, v190 op_sel_hi:[0,0,0]
	v_mfma_scale_f32_16x16x128_f8f6f4 v[150:153], v[18:25], v[194:201], v[150:153], v190, v190 op_sel_hi:[0,0,0]
	v_mfma_scale_f32_16x16x128_f8f6f4 v[146:149], v[26:33], v[194:201], v[146:149], v190, v190 op_sel_hi:[0,0,0]
	v_mfma_scale_f32_16x16x128_f8f6f4 v[126:129], v[18:25], v[202:209], v[126:129], v190, v190 op_sel_hi:[0,0,0]
	v_mfma_scale_f32_16x16x128_f8f6f4 v[122:125], v[26:33], v[202:209], v[122:125], v190, v190 op_sel_hi:[0,0,0]
	v_mfma_scale_f32_16x16x128_f8f6f4 v[118:121], v[18:25], v[210:217], v[118:121], v190, v190 op_sel_hi:[0,0,0]
	v_mfma_scale_f32_16x16x128_f8f6f4 v[110:113], v[26:33], v[210:217], v[110:113], v190, v190 op_sel_hi:[0,0,0]
	s_setprio 0
	s_setprio 1
	v_mfma_scale_f32_16x16x128_f8f6f4 v[142:145], v[2:9], v[178:185], v[142:145], v190, v190 op_sel_hi:[0,0,0]
	v_mfma_scale_f32_16x16x128_f8f6f4 v[138:141], v[10:17], v[178:185], v[138:141], v190, v190 op_sel_hi:[0,0,0]
	v_mfma_scale_f32_16x16x128_f8f6f4 v[134:137], v[2:9], v[194:201], v[134:137], v190, v190 op_sel_hi:[0,0,0]
	v_mfma_scale_f32_16x16x128_f8f6f4 v[130:133], v[10:17], v[194:201], v[130:133], v190, v190 op_sel_hi:[0,0,0]
	v_mfma_scale_f32_16x16x128_f8f6f4 v[114:117], v[2:9], v[202:209], v[114:117], v190, v190 op_sel_hi:[0,0,0]
	v_mfma_scale_f32_16x16x128_f8f6f4 v[106:109], v[10:17], v[202:209], v[106:109], v190, v190 op_sel_hi:[0,0,0]
	v_mfma_scale_f32_16x16x128_f8f6f4 v[102:105], v[2:9], v[210:217], v[102:105], v190, v190 op_sel_hi:[0,0,0]
	v_mfma_scale_f32_16x16x128_f8f6f4 v[98:101], v[10:17], v[210:217], v[98:101], v190, v190 op_sel_hi:[0,0,0]
	s_setprio 0
	s_barrier
	s_mov_b32 m0, s43
	s_add_u32 s98, s34, 0x80
	s_addc_u32 s99, s35, 0
	s_add_u32 s28, s34, 0xb0000
	ds_read_b128 v[194:197], v189 offset:16384
	ds_read_b128 v[198:201], v189 offset:16400
	ds_read_b128 v[202:205], v189 offset:18432
	ds_read_b128 v[206:209], v189 offset:18448
	ds_read_b128 v[210:213], v189 offset:20480
	ds_read_b128 v[214:217], v189 offset:20496
	ds_read_b128 v[218:221], v189 offset:22528
	ds_read_b128 v[222:225], v189 offset:22544
	global_load_lds_dwordx4 v164, s[34:35]
	s_mov_b32 m0, s44
	s_addc_u32 s29, s35, 0
	global_load_lds_dwordx4 v168, s[34:35]
	s_mov_b32 m0, s45
	s_nop 0
	global_load_lds_dwordx4 v164, s[28:29]
	s_mov_b32 m0, s46
	s_nop 0
	global_load_lds_dwordx4 v168, s[28:29]
	s_add_u32 s100, s36, 0x80
	s_addc_u32 s101, s37, 0
	s_mov_b32 m0, s47
	s_nop 0
	global_load_lds_dwordx4 v162, s[36:37]
	s_mov_b32 m0, s48
	s_nop 0
	global_load_lds_dwordx4 v166, s[36:37]
	s_waitcnt vmcnt(8) lgkmcnt(0)
	s_barrier
	s_setprio 1
	v_mfma_scale_f32_16x16x128_f8f6f4 v[94:97], v[18:25], v[194:201], v[94:97], v190, v190 op_sel_hi:[0,0,0]
	v_mfma_scale_f32_16x16x128_f8f6f4 v[90:93], v[26:33], v[194:201], v[90:93], v190, v190 op_sel_hi:[0,0,0]
	v_mfma_scale_f32_16x16x128_f8f6f4 v[78:81], v[18:25], v[202:209], v[78:81], v190, v190 op_sel_hi:[0,0,0]
	v_mfma_scale_f32_16x16x128_f8f6f4 v[74:77], v[26:33], v[202:209], v[74:77], v190, v190 op_sel_hi:[0,0,0]
	v_mfma_scale_f32_16x16x128_f8f6f4 v[226:229], v[18:25], v[210:217], v[62:65], v190, v190 op_sel_hi:[0,0,0]
	v_mfma_scale_f32_16x16x128_f8f6f4 v[230:233], v[26:33], v[210:217], v[58:61], v190, v190 op_sel_hi:[0,0,0]
	v_mfma_scale_f32_16x16x128_f8f6f4 v[234:237], v[18:25], v[218:225], v[46:49], v190, v190 op_sel_hi:[0,0,0]
	v_mfma_scale_f32_16x16x128_f8f6f4 v[238:241], v[26:33], v[218:225], v[42:45], v190, v190 op_sel_hi:[0,0,0]
	s_setprio 0
	s_setprio 1
	v_mfma_scale_f32_16x16x128_f8f6f4 v[86:89], v[2:9], v[194:201], v[86:89], v190, v190 op_sel_hi:[0,0,0]
	v_mfma_scale_f32_16x16x128_f8f6f4 v[82:85], v[10:17], v[194:201], v[82:85], v190, v190 op_sel_hi:[0,0,0]
	v_mfma_scale_f32_16x16x128_f8f6f4 v[70:73], v[2:9], v[202:209], v[70:73], v190, v190 op_sel_hi:[0,0,0]
	v_mfma_scale_f32_16x16x128_f8f6f4 v[66:69], v[10:17], v[202:209], v[66:69], v190, v190 op_sel_hi:[0,0,0]
	v_mfma_scale_f32_16x16x128_f8f6f4 v[242:245], v[2:9], v[210:217], v[54:57], v190, v190 op_sel_hi:[0,0,0]
	v_mfma_scale_f32_16x16x128_f8f6f4 v[210:213], v[10:17], v[210:217], v[50:53], v190, v190 op_sel_hi:[0,0,0]
	v_mfma_scale_f32_16x16x128_f8f6f4 v[214:217], v[2:9], v[218:225], v[38:41], v190, v190 op_sel_hi:[0,0,0]
	v_mfma_scale_f32_16x16x128_f8f6f4 v[218:221], v[10:17], v[218:225], v[34:37], v190, v190 op_sel_hi:[0,0,0]
	s_setprio 0
	s_barrier
; #define PG8_STAGE(bufoff, gbase, voff) do { _Pragma("unroll") for (int _i = 0; _i < 2; ++_i) \
;         __builtin_amdgcn_global_load_lds((const unsigned*)((const char*)(gbase) + (voff)[_i]), (PG8_LAS unsigned*)(lds + (bufoff) + ldsw + _i * 8192), 16, 0, 0); } while (0)
; #define PG8_LDA(dst, b, h) do { if constexpr (DT != 1) { _Pragma("unroll") for (int m = 0; m < 4; ++m) _Pragma("unroll") for (int k = 0; k < 2; ++k) dst[m][k] = *(const PG8_LAS bf16x8*)(lds + PG8_SA(b, h) + aoff + m * 2048 + k * 1024); } \
;         else { _Pragma("unroll") for (int m = 0; m < 4; ++m) dst##8[m] = ld32(lds + PG8_SA(b, h) + aoff + m * 2048); } } while (0)
; #define PG8_LDB(dst, b, h) do { if constexpr (DT != 1) { _Pragma("unroll") for (int n = 0; n < 2; ++n) _Pragma("unroll") for (int k = 0; k < 2; ++k) dst[n][k] = *(const PG8_LAS bf16x8*)(lds + PG8_SB(b, h) + boff + n * 2048 + k * 1024); } \
;         else { _Pragma("unroll") for (int n = 0; n < 2; ++n) dst##8[n] = ld32(lds + PG8_SB(b, h) + boff + n * 2048); } } while (0)
; #define PG8_WAIT_V(n) asm volatile("s_waitcnt vmcnt(" #n ")" ::: "memory")
; #define PG8_WAIT_L(n) asm volatile("s_waitcnt lgkmcnt(" #n ")" ::: "memory")
; #define PG8_BAR __builtin_amdgcn_s_barrier()
; #define PG8_SCHED __builtin_amdgcn_sched_barrier(0)
;     ...
;             PG8_LDB(B0, 0, 0); PG8_LDB(B1, 0, 1); PG8_SCHED; PG8_LDA(At, 0, 0); PG8_STAGE(PG8_SA(1, 1), a1 + hstepA, voffA);
;             PG8_WAIT_V(8); PG8_WAIT_L(0); PG8_BAR; PG8_MMA(0, 0, At, B0); PG8_MMA(0, 1, At, B1); PG8_BAR; PG8_SCHED;
;             PG8_LDA(At, 0, 1); PG8_STAGE(PG8_SB(0, 0), b2, voffB); PG8_STAGE(PG8_SB(0, 1), b2 + hstepB, voffB); PG8_STAGE(PG8_SA(0, 0), a2, voffA);
;             PG8_WAIT_V(8); PG8_WAIT_L(0); PG8_BAR; PG8_MMA(1, 0, At, B0); PG8_MMA(1, 1, At, B1); PG8_BAR; PG8_SCHED;
;             PG8_LDB(B0, 1, 0); PG8_LDB(B1, 1, 1); PG8_SCHED; PG8_LDA(At, 1, 0); PG8_STAGE(PG8_SA(0, 1), a2 + hstepA, voffA);
;             PG8_WAIT_V(8); PG8_WAIT_L(0); PG8_BAR; PG8_MMA(0, 0, At, B0); PG8_MMA(0, 1, At, B1); PG8_BAR; PG8_SCHED;
;             PG8_LDA(At, 1, 1); PG8_STAGE(PG8_SB(1, 0), b3, voffB); PG8_STAGE(PG8_SB(1, 1), b3 + hstepB, voffB); PG8_STAGE(PG8_SA(1, 0), a3, voffA);
;             PG8_WAIT_V(8); PG8_WAIT_L(0); PG8_BAR; PG8_MMA(1, 0, At, B0); PG8_MMA(1, 1, At, B1); PG8_BAR; PG8_SCHED;
	ds_read_b128 v[2:5], v191
	ds_read_b128 v[6:9], v191 offset:16
	ds_read_b128 v[10:13], v191 offset:2048
	ds_read_b128 v[14:17], v191 offset:2064
	ds_read_b128 v[18:21], v192
	ds_read_b128 v[22:25], v192 offset:16
	ds_read_b128 v[26:29], v192 offset:2048
	ds_read_b128 v[30:33], v192 offset:2064
	s_add_u32 s28, s36, 0xb0000
	s_addc_u32 s29, s37, 0
	s_mov_b32 m0, s49
	ds_read_b128 v[34:37], v189 offset:32768
	ds_read_b128 v[38:41], v189 offset:32784
	ds_read_b128 v[42:45], v189 offset:34816
	ds_read_b128 v[46:49], v189 offset:34832
	ds_read_b128 v[50:53], v189 offset:36864
	ds_read_b128 v[54:57], v189 offset:36880
	ds_read_b128 v[58:61], v189 offset:38912
	ds_read_b128 v[62:65], v189 offset:38928
	global_load_lds_dwordx4 v162, s[28:29]
	s_mov_b32 m0, s50
	s_nop 0
	global_load_lds_dwordx4 v166, s[28:29]
	s_waitcnt vmcnt(8) lgkmcnt(0)
	s_barrier
	s_setprio 1
	v_mfma_scale_f32_16x16x128_f8f6f4 v[158:161], v[2:9], v[34:41], v[158:161], v190, v190 op_sel_hi:[0,0,0]
	v_mfma_scale_f32_16x16x128_f8f6f4 v[154:157], v[10:17], v[34:41], v[154:157], v190, v190 op_sel_hi:[0,0,0]
	v_mfma_scale_f32_16x16x128_f8f6f4 v[150:153], v[2:9], v[42:49], v[150:153], v190, v190 op_sel_hi:[0,0,0]
	v_mfma_scale_f32_16x16x128_f8f6f4 v[146:149], v[10:17], v[42:49], v[146:149], v190, v190 op_sel_hi:[0,0,0]
	v_mfma_scale_f32_16x16x128_f8f6f4 v[126:129], v[2:9], v[50:57], v[126:129], v190, v190 op_sel_hi:[0,0,0]
	v_mfma_scale_f32_16x16x128_f8f6f4 v[122:125], v[10:17], v[50:57], v[122:125], v190, v190 op_sel_hi:[0,0,0]
	v_mfma_scale_f32_16x16x128_f8f6f4 v[118:121], v[2:9], v[58:65], v[118:121], v190, v190 op_sel_hi:[0,0,0]
	v_mfma_scale_f32_16x16x128_f8f6f4 v[110:113], v[10:17], v[58:65], v[110:113], v190, v190 op_sel_hi:[0,0,0]
	s_setprio 0
	s_setprio 1
	v_mfma_scale_f32_16x16x128_f8f6f4 v[142:145], v[18:25], v[34:41], v[142:145], v190, v190 op_sel_hi:[0,0,0]
	v_mfma_scale_f32_16x16x128_f8f6f4 v[138:141], v[26:33], v[34:41], v[138:141], v190, v190 op_sel_hi:[0,0,0]
	v_mfma_scale_f32_16x16x128_f8f6f4 v[134:137], v[18:25], v[42:49], v[134:137], v190, v190 op_sel_hi:[0,0,0]
	v_mfma_scale_f32_16x16x128_f8f6f4 v[130:133], v[26:33], v[42:49], v[130:133], v190, v190 op_sel_hi:[0,0,0]
	v_mfma_scale_f32_16x16x128_f8f6f4 v[114:117], v[18:25], v[50:57], v[114:117], v190, v190 op_sel_hi:[0,0,0]
	v_mfma_scale_f32_16x16x128_f8f6f4 v[106:109], v[26:33], v[50:57], v[106:109], v190, v190 op_sel_hi:[0,0,0]
	v_mfma_scale_f32_16x16x128_f8f6f4 v[102:105], v[18:25], v[58:65], v[102:105], v190, v190 op_sel_hi:[0,0,0]
	v_mfma_scale_f32_16x16x128_f8f6f4 v[98:101], v[26:33], v[58:65], v[98:101], v190, v190 op_sel_hi:[0,0,0]
	s_setprio 0
	s_barrier
	s_mov_b32 m0, s53
	s_add_u32 s28, s34, 0xb0080
	ds_read_b128 v[34:37], v189 offset:49152
	ds_read_b128 v[38:41], v189 offset:49168
	ds_read_b128 v[50:53], v189 offset:51200
	ds_read_b128 v[54:57], v189 offset:51216
	ds_read_b128 v[194:197], v189 offset:53248
	ds_read_b128 v[198:201], v189 offset:53264
	ds_read_b128 v[202:205], v189 offset:55296
	ds_read_b128 v[206:209], v189 offset:55312
	global_load_lds_dwordx4 v164, s[98:99]
	s_mov_b32 m0, s54
	s_addc_u32 s29, s35, 0
	global_load_lds_dwordx4 v168, s[98:99]
	s_mov_b32 m0, s57
	s_nop 0
	global_load_lds_dwordx4 v164, s[28:29]
	s_mov_b32 m0, s58
	s_nop 0
	global_load_lds_dwordx4 v168, s[28:29]
	s_mov_b32 m0, s55
	s_nop 0
	global_load_lds_dwordx4 v162, s[100:101]
	s_mov_b32 m0, s56
	s_nop 0
	global_load_lds_dwordx4 v166, s[100:101]
	s_waitcnt vmcnt(8) lgkmcnt(0)
	s_barrier
	s_setprio 1
	v_mfma_scale_f32_16x16x128_f8f6f4 v[94:97], v[2:9], v[34:41], v[94:97], v190, v190 op_sel_hi:[0,0,0]
	v_mfma_scale_f32_16x16x128_f8f6f4 v[90:93], v[10:17], v[34:41], v[90:93], v190, v190 op_sel_hi:[0,0,0]
	v_mfma_scale_f32_16x16x128_f8f6f4 v[78:81], v[2:9], v[50:57], v[78:81], v190, v190 op_sel_hi:[0,0,0]
	v_mfma_scale_f32_16x16x128_f8f6f4 v[74:77], v[10:17], v[50:57], v[74:77], v190, v190 op_sel_hi:[0,0,0]
	v_mfma_scale_f32_16x16x128_f8f6f4 v[62:65], v[2:9], v[194:201], v[226:229], v190, v190 op_sel_hi:[0,0,0]
	v_mfma_scale_f32_16x16x128_f8f6f4 v[58:61], v[10:17], v[194:201], v[230:233], v190, v190 op_sel_hi:[0,0,0]
	v_mfma_scale_f32_16x16x128_f8f6f4 v[46:49], v[2:9], v[202:209], v[234:237], v190, v190 op_sel_hi:[0,0,0]
	v_mfma_scale_f32_16x16x128_f8f6f4 v[42:45], v[10:17], v[202:209], v[238:241], v190, v190 op_sel_hi:[0,0,0]
	s_setprio 0
	s_setprio 1
	v_mfma_scale_f32_16x16x128_f8f6f4 v[86:89], v[18:25], v[34:41], v[86:89], v190, v190 op_sel_hi:[0,0,0]
	v_mfma_scale_f32_16x16x128_f8f6f4 v[82:85], v[26:33], v[34:41], v[82:85], v190, v190 op_sel_hi:[0,0,0]
	v_mfma_scale_f32_16x16x128_f8f6f4 v[70:73], v[18:25], v[50:57], v[70:73], v190, v190 op_sel_hi:[0,0,0]
	v_mfma_scale_f32_16x16x128_f8f6f4 v[66:69], v[26:33], v[50:57], v[66:69], v190, v190 op_sel_hi:[0,0,0]
	v_mfma_scale_f32_16x16x128_f8f6f4 v[54:57], v[18:25], v[194:201], v[242:245], v190, v190 op_sel_hi:[0,0,0]
	v_mfma_scale_f32_16x16x128_f8f6f4 v[50:53], v[26:33], v[194:201], v[210:213], v190, v190 op_sel_hi:[0,0,0]
	v_mfma_scale_f32_16x16x128_f8f6f4 v[38:41], v[18:25], v[202:209], v[214:217], v190, v190 op_sel_hi:[0,0,0]
	v_mfma_scale_f32_16x16x128_f8f6f4 v[34:37], v[26:33], v[202:209], v[218:221], v190, v190 op_sel_hi:[0,0,0]
	s_setprio 0
	s_barrier
	s_add_u32 s66, s66, 0x100
	s_addc_u32 s67, s67, 0
	s_cmp_ge_i32 s68, s52
	s_mov_b64 s[28:29], s[30:31]
	s_mov_b32 s34, s68
	s_cbranch_scc0 .LBB0_4217

; #define PG8_STAGE(bufoff, gbase, voff) do { _Pragma("unroll") for (int _i = 0; _i < 2; ++_i) \
;         __builtin_amdgcn_global_load_lds((const unsigned*)((const char*)(gbase) + (voff)[_i]), (PG8_LAS unsigned*)(lds + (bufoff) + ldsw + _i * 8192), 16, 0, 0); } while (0)
; #define PG8_LDA(dst, b, h) do { if constexpr (DT != 1) { _Pragma("unroll") for (int m = 0; m < 4; ++m) _Pragma("unroll") for (int k = 0; k < 2; ++k) dst[m][k] = *(const PG8_LAS bf16x8*)(lds + PG8_SA(b, h) + aoff + m * 2048 + k * 1024); } \
;         else { _Pragma("unroll") for (int m = 0; m < 4; ++m) dst##8[m] = ld32(lds + PG8_SA(b, h) + aoff + m * 2048); } } while (0)
; #define PG8_WAIT_V(n) asm volatile("s_waitcnt vmcnt(" #n ")" ::: "memory")
; #define PG8_WAIT_L(n) asm volatile("s_waitcnt lgkmcnt(" #n ")" ::: "memory")
; #define PG8_BAR __builtin_amdgcn_s_barrier()
; #define PG8_SCHED __builtin_amdgcn_sched_barrier(0)
;     ...
;         for (int t = 0; t < nt; t += 2) {
;             const bool last = (t == nt - 2);
;             const char* a1 = cA + (size_t)(t + 1) * kstep;
;             const char* a2 = last ? nA : cA + (size_t)(t + 2) * kstep; const char* b2 = last ? nB : cB + (size_t)(t + 2) * kstep;
;             const char* a3 = a2 + kstep; const char* b3 = b2 + kstep;
;             if (last && has_next) S.a_ready(nxt);
;             if constexpr (SP2) {
;             PG8_LDB(B0, 0, 0); PG8_LDB(B1, 0, 1); PG8_SCHED; PG8_LDA(At, 0, 0); PG8_STAGE(PG8_SA(1, 1), a1 + hstepA, voffA);
;             PG8_WAIT_V(8); PG8_WAIT_L(0); PG8_BAR; PG8_MMA(0, 0, At, B0); PG8_MMA(0, 1, At, B1); PG8_BAR; PG8_SCHED;
;             PG8_LDA(At, 0, 1); PG8_STAGE(PG8_SB(0, 0), b2, voffB); PG8_STAGE(PG8_SB(0, 1), b2 + hstepB, voffB); PG8_STAGE(PG8_SA(0, 0), a2, voffA);
;             PG8_WAIT_V(8); PG8_WAIT_L(0); PG8_BAR; PG8_MMA(1, 0, At, B0); PG8_MMA(1, 1, At, B1); PG8_BAR; PG8_SCHED;
;             PG8_LDB(B0, 1, 0); PG8_LDB(B1, 1, 1); PG8_SCHED; PG8_LDA(At, 1, 0); PG8_STAGE(PG8_SA(0, 1), a2 + hstepA, voffA);
;             PG8_WAIT_V(8); PG8_WAIT_L(0); PG8_BAR; PG8_MMA(0, 0, At, B0); PG8_MMA(0, 1, At, B1); PG8_BAR; PG8_SCHED;
;             PG8_LDA(At, 1, 1); PG8_STAGE(PG8_SB(1, 0), b3, voffB); PG8_STAGE(PG8_SB(1, 1), b3 + hstepB, voffB); PG8_STAGE(PG8_SA(1, 0), a3, voffA);
;             PG8_WAIT_V(8); PG8_WAIT_L(0); PG8_BAR; PG8_MMA(1, 0, At, B0); PG8_MMA(1, 1, At, B1); PG8_BAR; PG8_SCHED;
.LBB0_4350:
	v_add_u32_e32 v164, s37, v170
	v_add_u32_e32 v168, s38, v170
	ds_read_b128 v[152:155], v164
	ds_read_b128 v[156:159], v164 offset:1024
	ds_read_b128 v[160:163], v164 offset:2048
	ds_read_b128 v[164:167], v164 offset:3072
	ds_read_b128 v[180:183], v168
	ds_read_b128 v[184:187], v168 offset:1024
	ds_read_b128 v[188:191], v168 offset:2048
	ds_read_b128 v[192:195], v168 offset:3072
	s_add_i32 s70, s28, 2
	s_add_u32 s29, s26, 0xfffc0080
	s_addc_u32 s30, s27, -1
	s_cmp_eq_u32 s64, s28
	s_cselect_b32 s28, s67, s68
	s_cselect_b32 s31, s17, s30
	s_cselect_b32 s30, s19, s29
	s_cselect_b32 s29, s66, s69
	s_add_i32 m0, s49, 0xc000
	ds_read_b128 v[196:199], v179
	ds_read_b128 v[200:203], v179 offset:1024
	ds_read_b128 v[204:207], v179 offset:2048
	ds_read_b128 v[208:211], v179 offset:3072
	ds_read_b128 v[212:215], v179 offset:4096
	ds_read_b128 v[216:219], v179 offset:5120
	ds_read_b128 v[220:223], v179 offset:6144
	ds_read_b128 v[224:227], v179 offset:7168
	global_load_lds_dwordx4 v146, s[26:27]
	s_add_i32 m0, s49, 0xe000
	s_nop 0
	global_load_lds_dwordx4 v144, s[26:27]
	s_waitcnt vmcnt(8) lgkmcnt(0)
	s_barrier
	s_setprio 1
	v_mfma_i32_16x16x64_i8 v[126:129], v[152:155], v[196:199], v[126:129]
	v_mfma_i32_16x16x64_i8 v[122:125], v[160:163], v[196:199], v[122:125]
	v_mfma_i32_16x16x64_i8 v[118:121], v[152:155], v[204:207], v[118:121]
	v_mfma_i32_16x16x64_i8 v[114:117], v[160:163], v[204:207], v[114:117]
	v_mfma_i32_16x16x64_i8 v[110:113], v[152:155], v[212:215], v[110:113]
	v_mfma_i32_16x16x64_i8 v[106:109], v[160:163], v[212:215], v[106:109]
	v_mfma_i32_16x16x64_i8 v[102:105], v[152:155], v[220:223], v[102:105]
	v_mfma_i32_16x16x64_i8 v[98:101], v[160:163], v[220:223], v[98:101]
	v_mfma_i32_16x16x64_i8 v[126:129], v[156:159], v[200:203], v[126:129]
	v_mfma_i32_16x16x64_i8 v[122:125], v[164:167], v[200:203], v[122:125]
	v_mfma_i32_16x16x64_i8 v[118:121], v[156:159], v[208:211], v[118:121]
	v_mfma_i32_16x16x64_i8 v[114:117], v[164:167], v[208:211], v[114:117]
	v_mfma_i32_16x16x64_i8 v[110:113], v[156:159], v[216:219], v[110:113]
	v_mfma_i32_16x16x64_i8 v[106:109], v[164:167], v[216:219], v[106:109]
	v_mfma_i32_16x16x64_i8 v[102:105], v[156:159], v[224:227], v[102:105]
	v_mfma_i32_16x16x64_i8 v[98:101], v[164:167], v[224:227], v[98:101]
	s_setprio 0
	s_setprio 1
	v_mfma_i32_16x16x64_i8 v[94:97], v[180:183], v[196:199], v[94:97]
	v_mfma_i32_16x16x64_i8 v[86:89], v[188:191], v[196:199], v[86:89]
	v_mfma_i32_16x16x64_i8 v[78:81], v[180:183], v[204:207], v[78:81]
	v_mfma_i32_16x16x64_i8 v[70:73], v[188:191], v[204:207], v[70:73]
	v_mfma_i32_16x16x64_i8 v[62:65], v[180:183], v[212:215], v[62:65]
	v_mfma_i32_16x16x64_i8 v[54:57], v[188:191], v[212:215], v[54:57]
	v_mfma_i32_16x16x64_i8 v[46:49], v[180:183], v[220:223], v[46:49]
	v_mfma_i32_16x16x64_i8 v[38:41], v[188:191], v[220:223], v[38:41]
	v_mfma_i32_16x16x64_i8 v[94:97], v[184:187], v[200:203], v[94:97]
	v_mfma_i32_16x16x64_i8 v[86:89], v[192:195], v[200:203], v[86:89]
	v_mfma_i32_16x16x64_i8 v[78:81], v[184:187], v[208:211], v[78:81]
	v_mfma_i32_16x16x64_i8 v[70:73], v[192:195], v[208:211], v[70:73]
	v_mfma_i32_16x16x64_i8 v[62:65], v[184:187], v[216:219], v[62:65]
	v_mfma_i32_16x16x64_i8 v[54:57], v[192:195], v[216:219], v[54:57]
	v_mfma_i32_16x16x64_i8 v[46:49], v[184:187], v[224:227], v[46:49]
	v_mfma_i32_16x16x64_i8 v[38:41], v[192:195], v[224:227], v[38:41]
	s_setprio 0
	s_barrier
	s_mov_b32 m0, s45
	s_add_u32 s98, s28, 0x80
	s_addc_u32 s99, s29, 0
	s_add_u32 s72, s28, 0x40000
	ds_read_b128 v[196:199], v179 offset:16384
	ds_read_b128 v[200:203], v179 offset:17408
	ds_read_b128 v[204:207], v179 offset:18432
	ds_read_b128 v[208:211], v179 offset:19456
	ds_read_b128 v[212:215], v179 offset:20480
	ds_read_b128 v[216:219], v179 offset:21504
	ds_read_b128 v[220:223], v179 offset:22528
	ds_read_b128 v[224:227], v179 offset:23552
	global_load_lds_dwordx4 v132, s[28:29]
	s_mov_b32 m0, s46
	s_addc_u32 s73, s29, 0
	global_load_lds_dwordx4 v136, s[28:29]
	s_mov_b32 m0, s47
	s_nop 0
	global_load_lds_dwordx4 v132, s[72:73]
	s_mov_b32 m0, s48
	s_nop 0
	global_load_lds_dwordx4 v136, s[72:73]
	s_add_u32 s100, s30, 0x80
	s_addc_u32 s101, s31, 0
	s_mov_b32 m0, s49
	s_nop 0
	global_load_lds_dwordx4 v130, s[30:31]
	s_mov_b32 m0, s50
	s_nop 0
	global_load_lds_dwordx4 v134, s[30:31]
	s_waitcnt vmcnt(8) lgkmcnt(0)
	s_barrier
	s_setprio 1
	v_mfma_i32_16x16x64_i8 v[90:93], v[152:155], v[196:199], v[90:93]
	v_mfma_i32_16x16x64_i8 v[82:85], v[160:163], v[196:199], v[82:85]
	v_mfma_i32_16x16x64_i8 v[74:77], v[152:155], v[204:207], v[74:77]
	v_mfma_i32_16x16x64_i8 v[66:69], v[160:163], v[204:207], v[66:69]
	v_mfma_i32_16x16x64_i8 v[58:61], v[152:155], v[212:215], v[58:61]
	v_mfma_i32_16x16x64_i8 v[50:53], v[160:163], v[212:215], v[50:53]
	v_mfma_i32_16x16x64_i8 v[42:45], v[152:155], v[220:223], v[42:45]
	v_mfma_i32_16x16x64_i8 v[34:37], v[160:163], v[220:223], v[34:37]
	v_mfma_i32_16x16x64_i8 v[90:93], v[156:159], v[200:203], v[90:93]
	v_mfma_i32_16x16x64_i8 v[82:85], v[164:167], v[200:203], v[82:85]
	v_mfma_i32_16x16x64_i8 v[74:77], v[156:159], v[208:211], v[74:77]
	v_mfma_i32_16x16x64_i8 v[66:69], v[164:167], v[208:211], v[66:69]
	v_mfma_i32_16x16x64_i8 v[58:61], v[156:159], v[216:219], v[58:61]
	v_mfma_i32_16x16x64_i8 v[50:53], v[164:167], v[216:219], v[50:53]
	v_mfma_i32_16x16x64_i8 v[42:45], v[156:159], v[224:227], v[42:45]
	v_mfma_i32_16x16x64_i8 v[34:37], v[164:167], v[224:227], v[34:37]
	s_setprio 0
	s_setprio 1
	v_mfma_i32_16x16x64_i8 v[30:33], v[180:183], v[196:199], v[30:33]
	v_mfma_i32_16x16x64_i8 v[26:29], v[188:191], v[196:199], v[26:29]
	v_mfma_i32_16x16x64_i8 v[22:25], v[180:183], v[204:207], v[22:25]
	v_mfma_i32_16x16x64_i8 v[18:21], v[188:191], v[204:207], v[18:21]
	v_mfma_i32_16x16x64_i8 v[14:17], v[180:183], v[212:215], v[14:17]
	v_mfma_i32_16x16x64_i8 v[10:13], v[188:191], v[212:215], v[10:13]
	v_mfma_i32_16x16x64_i8 v[6:9], v[180:183], v[220:223], v[6:9]
	v_mfma_i32_16x16x64_i8 v[2:5], v[188:191], v[220:223], v[2:5]
	v_mfma_i32_16x16x64_i8 v[30:33], v[184:187], v[200:203], v[30:33]
	v_mfma_i32_16x16x64_i8 v[26:29], v[192:195], v[200:203], v[26:29]
	v_mfma_i32_16x16x64_i8 v[22:25], v[184:187], v[208:211], v[22:25]
	v_mfma_i32_16x16x64_i8 v[18:21], v[192:195], v[208:211], v[18:21]
	v_mfma_i32_16x16x64_i8 v[14:17], v[184:187], v[216:219], v[14:17]
	v_mfma_i32_16x16x64_i8 v[10:13], v[192:195], v[216:219], v[10:13]
	v_mfma_i32_16x16x64_i8 v[6:9], v[184:187], v[224:227], v[6:9]
	v_mfma_i32_16x16x64_i8 v[2:5], v[192:195], v[224:227], v[2:5]
	s_setprio 0
	s_barrier
; #define PG8_STAGE(bufoff, gbase, voff) do { _Pragma("unroll") for (int _i = 0; _i < 2; ++_i) \
;         __builtin_amdgcn_global_load_lds((const unsigned*)((const char*)(gbase) + (voff)[_i]), (PG8_LAS unsigned*)(lds + (bufoff) + ldsw + _i * 8192), 16, 0, 0); } while (0)
; #define PG8_LDA(dst, b, h) do { if constexpr (DT != 1) { _Pragma("unroll") for (int m = 0; m < 4; ++m) _Pragma("unroll") for (int k = 0; k < 2; ++k) dst[m][k] = *(const PG8_LAS bf16x8*)(lds + PG8_SA(b, h) + aoff + m * 2048 + k * 1024); } \
;         else { _Pragma("unroll") for (int m = 0; m < 4; ++m) dst##8[m] = ld32(lds + PG8_SA(b, h) + aoff + m * 2048); } } while (0)
; #define PG8_WAIT_V(n) asm volatile("s_waitcnt vmcnt(" #n ")" ::: "memory")
; #define PG8_WAIT_L(n) asm volatile("s_waitcnt lgkmcnt(" #n ")" ::: "memory")
; #define PG8_BAR __builtin_amdgcn_s_barrier()
; #define PG8_SCHED __builtin_amdgcn_sched_barrier(0)
;     ...
;         for (int t = 0; t < nt; t += 2) {
;             const bool last = (t == nt - 2);
;             const char* a1 = cA + (size_t)(t + 1) * kstep;
;             const char* a2 = last ? nA : cA + (size_t)(t + 2) * kstep; const char* b2 = last ? nB : cB + (size_t)(t + 2) * kstep;
;             const char* a3 = a2 + kstep; const char* b3 = b2 + kstep;
;             if (last && has_next) S.a_ready(nxt);
;             if constexpr (SP2) {
;             PG8_LDB(B0, 0, 0); PG8_LDB(B1, 0, 1); PG8_SCHED; PG8_LDA(At, 0, 0); PG8_STAGE(PG8_SA(1, 1), a1 + hstepA, voffA);
;             PG8_WAIT_V(8); PG8_WAIT_L(0); PG8_BAR; PG8_MMA(0, 0, At, B0); PG8_MMA(0, 1, At, B1); PG8_BAR; PG8_SCHED;
;             PG8_LDA(At, 0, 1); PG8_STAGE(PG8_SB(0, 0), b2, voffB); PG8_STAGE(PG8_SB(0, 1), b2 + hstepB, voffB); PG8_STAGE(PG8_SA(0, 0), a2, voffA);
;             PG8_WAIT_V(8); PG8_WAIT_L(0); PG8_BAR; PG8_MMA(1, 0, At, B0); PG8_MMA(1, 1, At, B1); PG8_BAR; PG8_SCHED;
;             PG8_LDB(B0, 1, 0); PG8_LDB(B1, 1, 1); PG8_SCHED; PG8_LDA(At, 1, 0); PG8_STAGE(PG8_SA(0, 1), a2 + hstepA, voffA);
;             PG8_WAIT_V(8); PG8_WAIT_L(0); PG8_BAR; PG8_MMA(0, 0, At, B0); PG8_MMA(0, 1, At, B1); PG8_BAR; PG8_SCHED;
;             PG8_LDA(At, 1, 1); PG8_STAGE(PG8_SB(1, 0), b3, voffB); PG8_STAGE(PG8_SB(1, 1), b3 + hstepB, voffB); PG8_STAGE(PG8_SA(1, 0), a3, voffA);
;             PG8_WAIT_V(8); PG8_WAIT_L(0); PG8_BAR; PG8_MMA(1, 0, At, B0); PG8_MMA(1, 1, At, B1); PG8_BAR; PG8_SCHED;
	v_add_u32_e32 v164, s54, v170
	v_add_u32_e32 v192, s55, v170
	ds_read_b128 v[152:155], v164
	ds_read_b128 v[156:159], v164 offset:1024
	ds_read_b128 v[160:163], v164 offset:2048
	ds_read_b128 v[164:167], v164 offset:3072
	ds_read_b128 v[180:183], v192
	ds_read_b128 v[184:187], v192 offset:1024
	ds_read_b128 v[188:191], v192 offset:2048
	ds_read_b128 v[192:195], v192 offset:3072
	s_add_u32 s30, s30, 0x40000
	s_addc_u32 s31, s31, 0
	s_mov_b32 m0, s51
	ds_read_b128 v[196:199], v179 offset:32768
	ds_read_b128 v[200:203], v179 offset:33792
	ds_read_b128 v[204:207], v179 offset:34816
	ds_read_b128 v[208:211], v179 offset:35840
	ds_read_b128 v[212:215], v179 offset:36864
	ds_read_b128 v[216:219], v179 offset:37888
	ds_read_b128 v[220:223], v179 offset:38912
	ds_read_b128 v[224:227], v179 offset:39936
	global_load_lds_dwordx4 v130, s[30:31]
	s_mov_b32 m0, s52
	s_nop 0
	global_load_lds_dwordx4 v134, s[30:31]
	s_waitcnt vmcnt(8) lgkmcnt(0)
	s_barrier
	s_setprio 1
	v_mfma_i32_16x16x64_i8 v[126:129], v[152:155], v[196:199], v[126:129]
	v_mfma_i32_16x16x64_i8 v[122:125], v[160:163], v[196:199], v[122:125]
	v_mfma_i32_16x16x64_i8 v[118:121], v[152:155], v[204:207], v[118:121]
	v_mfma_i32_16x16x64_i8 v[114:117], v[160:163], v[204:207], v[114:117]
	v_mfma_i32_16x16x64_i8 v[110:113], v[152:155], v[212:215], v[110:113]
	v_mfma_i32_16x16x64_i8 v[106:109], v[160:163], v[212:215], v[106:109]
	v_mfma_i32_16x16x64_i8 v[102:105], v[152:155], v[220:223], v[102:105]
	v_mfma_i32_16x16x64_i8 v[98:101], v[160:163], v[220:223], v[98:101]
	v_mfma_i32_16x16x64_i8 v[126:129], v[156:159], v[200:203], v[126:129]
	v_mfma_i32_16x16x64_i8 v[122:125], v[164:167], v[200:203], v[122:125]
	v_mfma_i32_16x16x64_i8 v[118:121], v[156:159], v[208:211], v[118:121]
	v_mfma_i32_16x16x64_i8 v[114:117], v[164:167], v[208:211], v[114:117]
	v_mfma_i32_16x16x64_i8 v[110:113], v[156:159], v[216:219], v[110:113]
	v_mfma_i32_16x16x64_i8 v[106:109], v[164:167], v[216:219], v[106:109]
	v_mfma_i32_16x16x64_i8 v[102:105], v[156:159], v[224:227], v[102:105]
	v_mfma_i32_16x16x64_i8 v[98:101], v[164:167], v[224:227], v[98:101]
	s_setprio 0
	s_setprio 1
	v_mfma_i32_16x16x64_i8 v[94:97], v[180:183], v[196:199], v[94:97]
	v_mfma_i32_16x16x64_i8 v[86:89], v[188:191], v[196:199], v[86:89]
	v_mfma_i32_16x16x64_i8 v[78:81], v[180:183], v[204:207], v[78:81]
	v_mfma_i32_16x16x64_i8 v[70:73], v[188:191], v[204:207], v[70:73]
	v_mfma_i32_16x16x64_i8 v[62:65], v[180:183], v[212:215], v[62:65]
	v_mfma_i32_16x16x64_i8 v[54:57], v[188:191], v[212:215], v[54:57]
	v_mfma_i32_16x16x64_i8 v[46:49], v[180:183], v[220:223], v[46:49]
	v_mfma_i32_16x16x64_i8 v[38:41], v[188:191], v[220:223], v[38:41]
	v_mfma_i32_16x16x64_i8 v[94:97], v[184:187], v[200:203], v[94:97]
	v_mfma_i32_16x16x64_i8 v[86:89], v[192:195], v[200:203], v[86:89]
	v_mfma_i32_16x16x64_i8 v[78:81], v[184:187], v[208:211], v[78:81]
	v_mfma_i32_16x16x64_i8 v[70:73], v[192:195], v[208:211], v[70:73]
	v_mfma_i32_16x16x64_i8 v[62:65], v[184:187], v[216:219], v[62:65]
	v_mfma_i32_16x16x64_i8 v[54:57], v[192:195], v[216:219], v[54:57]
	v_mfma_i32_16x16x64_i8 v[46:49], v[184:187], v[224:227], v[46:49]
	v_mfma_i32_16x16x64_i8 v[38:41], v[192:195], v[224:227], v[38:41]
	s_setprio 0
	s_barrier
	s_mov_b32 m0, s58
	s_add_u32 s28, s28, 0x40080
	ds_read_b128 v[196:199], v179 offset:49152
	ds_read_b128 v[200:203], v179 offset:50176
	ds_read_b128 v[204:207], v179 offset:51200
	ds_read_b128 v[208:211], v179 offset:52224
	ds_read_b128 v[212:215], v179 offset:53248
	ds_read_b128 v[216:219], v179 offset:54272
	ds_read_b128 v[220:223], v179 offset:55296
	ds_read_b128 v[224:227], v179 offset:56320
	global_load_lds_dwordx4 v132, s[98:99]
	s_mov_b32 m0, s59
	s_addc_u32 s29, s29, 0
	global_load_lds_dwordx4 v136, s[98:99]
	s_mov_b32 m0, s62
	s_nop 0
	global_load_lds_dwordx4 v132, s[28:29]
	s_mov_b32 m0, s63
	s_nop 0
	global_load_lds_dwordx4 v136, s[28:29]
	s_mov_b32 m0, s60
	s_nop 0
	global_load_lds_dwordx4 v130, s[100:101]
	s_mov_b32 m0, s61
	s_nop 0
	global_load_lds_dwordx4 v134, s[100:101]
	s_waitcnt vmcnt(8) lgkmcnt(0)
	s_barrier
; #define PG8_STAGE(bufoff, gbase, voff) do { _Pragma("unroll") for (int _i = 0; _i < 2; ++_i) \
;         __builtin_amdgcn_global_load_lds((const unsigned*)((const char*)(gbase) + (voff)[_i]), (PG8_LAS unsigned*)(lds + (bufoff) + ldsw + _i * 8192), 16, 0, 0); } while (0)
; #define PG8_LDA(dst, b, h) do { if constexpr (DT != 1) { _Pragma("unroll") for (int m = 0; m < 4; ++m) _Pragma("unroll") for (int k = 0; k < 2; ++k) dst[m][k] = *(const PG8_LAS bf16x8*)(lds + PG8_SA(b, h) + aoff + m * 2048 + k * 1024); } \
;         else { _Pragma("unroll") for (int m = 0; m < 4; ++m) dst##8[m] = ld32(lds + PG8_SA(b, h) + aoff + m * 2048); } } while (0)
; #define PG8_WAIT_V(n) asm volatile("s_waitcnt vmcnt(" #n ")" ::: "memory")
; #define PG8_WAIT_L(n) asm volatile("s_waitcnt lgkmcnt(" #n ")" ::: "memory")
; #define PG8_BAR __builtin_amdgcn_s_barrier()
; #define PG8_SCHED __builtin_amdgcn_sched_barrier(0)
; __device__ __forceinline__ f32x4 i32bits_to_f32(f32x4 v) { return (f32x4){(float)__float_as_int(v.x), (float)__float_as_int(v.y), (float)__float_as_int(v.z), (float)__float_as_int(v.w)}; }
;     ...
;             PG8_WAIT_V(8); PG8_WAIT_L(0); PG8_BAR; PG8_MMA(0, 0, At, B0); PG8_MMA(0, 1, At, B1); PG8_BAR; PG8_SCHED;
;             PG8_LDA(At, 1, 1); PG8_STAGE(PG8_SB(1, 0), b3, voffB); PG8_STAGE(PG8_SB(1, 1), b3 + hstepB, voffB); PG8_STAGE(PG8_SA(1, 0), a3, voffA);
;             PG8_WAIT_V(8); PG8_WAIT_L(0); PG8_BAR; PG8_MMA(1, 0, At, B0); PG8_MMA(1, 1, At, B1); PG8_BAR; PG8_SCHED;
	s_setprio 1
	v_mfma_i32_16x16x64_i8 v[90:93], v[152:155], v[196:199], v[90:93]
	v_mfma_i32_16x16x64_i8 v[82:85], v[160:163], v[196:199], v[82:85]
	v_mfma_i32_16x16x64_i8 v[74:77], v[152:155], v[204:207], v[74:77]
	v_mfma_i32_16x16x64_i8 v[66:69], v[160:163], v[204:207], v[66:69]
	v_mfma_i32_16x16x64_i8 v[58:61], v[152:155], v[212:215], v[58:61]
	v_mfma_i32_16x16x64_i8 v[50:53], v[160:163], v[212:215], v[50:53]
	v_mfma_i32_16x16x64_i8 v[42:45], v[152:155], v[220:223], v[42:45]
	v_mfma_i32_16x16x64_i8 v[34:37], v[160:163], v[220:223], v[34:37]
	v_mfma_i32_16x16x64_i8 v[90:93], v[156:159], v[200:203], v[90:93]
	v_mfma_i32_16x16x64_i8 v[82:85], v[164:167], v[200:203], v[82:85]
	v_mfma_i32_16x16x64_i8 v[74:77], v[156:159], v[208:211], v[74:77]
	v_mfma_i32_16x16x64_i8 v[66:69], v[164:167], v[208:211], v[66:69]
	v_mfma_i32_16x16x64_i8 v[58:61], v[156:159], v[216:219], v[58:61]
	v_mfma_i32_16x16x64_i8 v[50:53], v[164:167], v[216:219], v[50:53]
	v_mfma_i32_16x16x64_i8 v[42:45], v[156:159], v[224:227], v[42:45]
	v_mfma_i32_16x16x64_i8 v[34:37], v[164:167], v[224:227], v[34:37]
	s_setprio 0
	s_setprio 1
	v_mfma_i32_16x16x64_i8 v[30:33], v[180:183], v[196:199], v[30:33]
	v_mfma_i32_16x16x64_i8 v[26:29], v[188:191], v[196:199], v[26:29]
	v_mfma_i32_16x16x64_i8 v[22:25], v[180:183], v[204:207], v[22:25]
	v_mfma_i32_16x16x64_i8 v[18:21], v[188:191], v[204:207], v[18:21]
	v_mfma_i32_16x16x64_i8 v[14:17], v[180:183], v[212:215], v[14:17]
	v_mfma_i32_16x16x64_i8 v[10:13], v[188:191], v[212:215], v[10:13]
	v_mfma_i32_16x16x64_i8 v[6:9], v[180:183], v[220:223], v[6:9]
	v_mfma_i32_16x16x64_i8 v[2:5], v[188:191], v[220:223], v[2:5]
	v_mfma_i32_16x16x64_i8 v[30:33], v[184:187], v[200:203], v[30:33]
	v_mfma_i32_16x16x64_i8 v[26:29], v[192:195], v[200:203], v[26:29]
	v_mfma_i32_16x16x64_i8 v[22:25], v[184:187], v[208:211], v[22:25]
	v_mfma_i32_16x16x64_i8 v[18:21], v[192:195], v[208:211], v[18:21]
	v_mfma_i32_16x16x64_i8 v[14:17], v[184:187], v[216:219], v[14:17]
	v_mfma_i32_16x16x64_i8 v[10:13], v[192:195], v[216:219], v[10:13]
	v_mfma_i32_16x16x64_i8 v[6:9], v[184:187], v[224:227], v[6:9]
	v_mfma_i32_16x16x64_i8 v[2:5], v[192:195], v[224:227], v[2:5]
	s_setprio 0
	s_barrier
	s_add_u32 s68, s68, 0x100
	s_addc_u32 s69, s69, 0
	s_add_u32 s26, s26, 0x100
	s_addc_u32 s27, s27, 0
	s_cmp_ge_i32 s70, s57
	s_mov_b32 s28, s70
	s_cbranch_scc0 .LBB0_4350
	v_cvt_f32_i32_e32 v166, v126
	v_cvt_f32_i32_e32 v167, v127
	v_cvt_f32_i32_e32 v160, v128
	v_cvt_f32_i32_e32 v161, v129
	v_cvt_f32_i32_e32 v162, v122
	v_cvt_f32_i32_e32 v163, v123
	v_cvt_f32_i32_e32 v164, v124
	v_cvt_f32_i32_e32 v165, v125
	v_cvt_f32_i32_e32 v152, v118
	v_cvt_f32_i32_e32 v153, v119
	v_cvt_f32_i32_e32 v154, v120
	v_cvt_f32_i32_e32 v155, v121
	v_cvt_f32_i32_e32 v156, v114
	v_cvt_f32_i32_e32 v157, v115
	v_cvt_f32_i32_e32 v158, v116
	v_cvt_f32_i32_e32 v159, v117
	v_cvt_f32_i32_e32 v110, v110
	v_cvt_f32_i32_e32 v111, v111
	v_cvt_f32_i32_e32 v112, v112
	v_cvt_f32_i32_e32 v113, v113
	v_cvt_f32_i32_e32 v106, v106
	v_cvt_f32_i32_e32 v107, v107
	v_cvt_f32_i32_e32 v108, v108
	v_cvt_f32_i32_e32 v109, v109
	v_cvt_f32_i32_e32 v102, v102
	v_cvt_f32_i32_e32 v103, v103
	v_cvt_f32_i32_e32 v104, v104
	v_cvt_f32_i32_e32 v105, v105
	v_cvt_f32_i32_e32 v98, v98
	v_cvt_f32_i32_e32 v99, v99
	v_cvt_f32_i32_e32 v100, v100
	v_cvt_f32_i32_e32 v101, v101
	v_cvt_f32_i32_e32 v90, v90
	v_cvt_f32_i32_e32 v91, v91
	v_cvt_f32_i32_e32 v92, v92
	v_cvt_f32_i32_e32 v93, v93
	v_cvt_f32_i32_e32 v82, v82
	v_cvt_f32_i32_e32 v83, v83
	v_cvt_f32_i32_e32 v84, v84
	v_cvt_f32_i32_e32 v85, v85
	v_cvt_f32_i32_e32 v74, v74
	v_cvt_f32_i32_e32 v75, v75
	v_cvt_f32_i32_e32 v76, v76
	v_cvt_f32_i32_e32 v77, v77
	v_cvt_f32_i32_e32 v66, v66
	v_cvt_f32_i32_e32 v67, v67
	v_cvt_f32_i32_e32 v68, v68
	v_cvt_f32_i32_e32 v69, v69
	v_cvt_f32_i32_e32 v58, v58
	v_cvt_f32_i32_e32 v59, v59
	v_cvt_f32_i32_e32 v60, v60
	v_cvt_f32_i32_e32 v61, v61
	v_cvt_f32_i32_e32 v50, v50
	v_cvt_f32_i32_e32 v51, v51
	v_cvt_f32_i32_e32 v52, v52
	v_cvt_f32_i32_e32 v53, v53
	v_cvt_f32_i32_e32 v42, v42
	v_cvt_f32_i32_e32 v43, v43
	v_cvt_f32_i32_e32 v44, v44
	v_cvt_f32_i32_e32 v45, v45
	v_cvt_f32_i32_e32 v34, v34
	v_cvt_f32_i32_e32 v35, v35
	v_cvt_f32_i32_e32 v36, v36
	v_cvt_f32_i32_e32 v37, v37
	v_cvt_f32_i32_e32 v114, v94
	v_cvt_f32_i32_e32 v115, v95
	v_cvt_f32_i32_e32 v116, v96
	v_cvt_f32_i32_e32 v117, v97
	v_cvt_f32_i32_e32 v118, v86
	v_cvt_f32_i32_e32 v119, v87
	v_cvt_f32_i32_e32 v120, v88
	v_cvt_f32_i32_e32 v121, v89
	v_cvt_f32_i32_e32 v122, v78
	v_cvt_f32_i32_e32 v123, v79
	v_cvt_f32_i32_e32 v124, v80
	v_cvt_f32_i32_e32 v125, v81
	v_cvt_f32_i32_e32 v126, v70
	v_cvt_f32_i32_e32 v127, v71
	v_cvt_f32_i32_e32 v128, v72
	v_cvt_f32_i32_e32 v129, v73
	v_cvt_f32_i32_e32 v88, v62
	v_cvt_f32_i32_e32 v89, v63
	v_cvt_f32_i32_e32 v96, v64
	v_cvt_f32_i32_e32 v97, v65
	v_cvt_f32_i32_e32 v86, v54
	v_cvt_f32_i32_e32 v87, v55
	v_cvt_f32_i32_e32 v94, v56
	v_cvt_f32_i32_e32 v95, v57
	v_cvt_f32_i32_e32 v72, v46
	v_cvt_f32_i32_e32 v73, v47
	v_cvt_f32_i32_e32 v80, v48
	v_cvt_f32_i32_e32 v81, v49
	v_cvt_f32_i32_e32 v70, v38
	v_cvt_f32_i32_e32 v71, v39
	v_cvt_f32_i32_e32 v78, v40
	v_cvt_f32_i32_e32 v79, v41
	v_cvt_f32_i32_e32 v56, v30
	v_cvt_f32_i32_e32 v57, v31
	v_cvt_f32_i32_e32 v64, v32
	v_cvt_f32_i32_e32 v65, v33
	v_cvt_f32_i32_e32 v54, v26
	v_cvt_f32_i32_e32 v55, v27
	v_cvt_f32_i32_e32 v62, v28
	v_cvt_f32_i32_e32 v63, v29
	v_cvt_f32_i32_e32 v40, v22
	v_cvt_f32_i32_e32 v41, v23
	v_cvt_f32_i32_e32 v48, v24
	v_cvt_f32_i32_e32 v49, v25
	v_cvt_f32_i32_e32 v38, v18
	v_cvt_f32_i32_e32 v39, v19
	v_cvt_f32_i32_e32 v46, v20
	v_cvt_f32_i32_e32 v47, v21
	v_cvt_f32_i32_e32 v28, v14
	v_cvt_f32_i32_e32 v29, v15
	v_cvt_f32_i32_e32 v32, v16
	v_cvt_f32_i32_e32 v33, v17
	v_cvt_f32_i32_e32 v26, v10
	v_cvt_f32_i32_e32 v27, v11
	v_cvt_f32_i32_e32 v30, v12
	v_cvt_f32_i32_e32 v31, v13
	v_cvt_f32_i32_e32 v20, v6
	v_cvt_f32_i32_e32 v21, v7
	v_cvt_f32_i32_e32 v24, v8
	v_cvt_f32_i32_e32 v25, v9
	v_cvt_f32_i32_e32 v18, v2
	v_cvt_f32_i32_e32 v19, v3
	v_cvt_f32_i32_e32 v22, v4
	v_cvt_f32_i32_e32 v23, v5

; #define PG8_STAGE(bufoff, gbase, voff) do { _Pragma("unroll") for (int _i = 0; _i < 2; ++_i) \
;         __builtin_amdgcn_global_load_lds((const unsigned*)((const char*)(gbase) + (voff)[_i]), (PG8_LAS unsigned*)(lds + (bufoff) + ldsw + _i * 8192), 16, 0, 0); } while (0)
; #define PG8_LDA(dst, b, h) do { if constexpr (DT != 1) { _Pragma("unroll") for (int m = 0; m < 4; ++m) _Pragma("unroll") for (int k = 0; k < 2; ++k) dst[m][k] = *(const PG8_LAS bf16x8*)(lds + PG8_SA(b, h) + aoff + m * 2048 + k * 1024); } \
;         else { _Pragma("unroll") for (int m = 0; m < 4; ++m) dst##8[m] = ld32(lds + PG8_SA(b, h) + aoff + m * 2048); } } while (0)
; #define PG8_WAIT_V(n) asm volatile("s_waitcnt vmcnt(" #n ")" ::: "memory")
; #define PG8_WAIT_L(n) asm volatile("s_waitcnt lgkmcnt(" #n ")" ::: "memory")
; #define PG8_BAR __builtin_amdgcn_s_barrier()
; #define PG8_SCHED __builtin_amdgcn_sched_barrier(0)
;     ...
;         for (int t = 0; t < nt; t += 2) {
;             const bool last = (t == nt - 2);
;             const char* a1 = cA + (size_t)(t + 1) * kstep;
;             const char* a2 = last ? nA : cA + (size_t)(t + 2) * kstep; const char* b2 = last ? nB : cB + (size_t)(t + 2) * kstep;
;             const char* a3 = a2 + kstep; const char* b3 = b2 + kstep;
;             if (last && has_next) S.a_ready(nxt);
;             if constexpr (SP2) {
;             PG8_LDB(B0, 0, 0); PG8_LDB(B1, 0, 1); PG8_SCHED; PG8_LDA(At, 0, 0); PG8_STAGE(PG8_SA(1, 1), a1 + hstepA, voffA);
;             PG8_WAIT_V(8); PG8_WAIT_L(0); PG8_BAR; PG8_MMA(0, 0, At, B0); PG8_MMA(0, 1, At, B1); PG8_BAR; PG8_SCHED;
;             PG8_LDA(At, 0, 1); PG8_STAGE(PG8_SB(0, 0), b2, voffB); PG8_STAGE(PG8_SB(0, 1), b2 + hstepB, voffB); PG8_STAGE(PG8_SA(0, 0), a2, voffA);
;             PG8_WAIT_V(8); PG8_WAIT_L(0); PG8_BAR; PG8_MMA(1, 0, At, B0); PG8_MMA(1, 1, At, B1); PG8_BAR; PG8_SCHED;
;             PG8_LDB(B0, 1, 0); PG8_LDB(B1, 1, 1); PG8_SCHED; PG8_LDA(At, 1, 0); PG8_STAGE(PG8_SA(0, 1), a2 + hstepA, voffA);
;             PG8_WAIT_V(8); PG8_WAIT_L(0); PG8_BAR; PG8_MMA(0, 0, At, B0); PG8_MMA(0, 1, At, B1); PG8_BAR; PG8_SCHED;
;             PG8_LDA(At, 1, 1); PG8_STAGE(PG8_SB(1, 0), b3, voffB); PG8_STAGE(PG8_SB(1, 1), b3 + hstepB, voffB); PG8_STAGE(PG8_SA(1, 0), a3, voffA);
;             PG8_WAIT_V(8); PG8_WAIT_L(0); PG8_BAR; PG8_MMA(1, 0, At, B0); PG8_MMA(1, 1, At, B1); PG8_BAR; PG8_SCHED;
.LBB0_4646:
	ds_read_b128 v[146:149], v157
	ds_read_b128 v[150:153], v157 offset:1024
	ds_read_b128 v[162:165], v157 offset:2048
	ds_read_b128 v[166:169], v157 offset:3072
	ds_read_b128 v[170:173], v158
	ds_read_b128 v[174:177], v158 offset:1024
	ds_read_b128 v[178:181], v158 offset:2048
	ds_read_b128 v[182:185], v158 offset:3072
	s_add_i32 s71, s38, 2
	s_add_u32 s39, s36, 0xfff80080
	s_addc_u32 s40, s37, -1
	s_cmp_eq_u32 s63, s38
	s_cselect_b32 s38, s68, s69
	s_cselect_b32 s41, s25, s40
	s_cselect_b32 s40, s27, s39
	s_cselect_b32 s39, s67, s70
	s_add_i32 m0, s51, 0xc000
	ds_read_b128 v[186:189], v159
	ds_read_b128 v[190:193], v159 offset:1024
	ds_read_b128 v[194:197], v159 offset:2048
	ds_read_b128 v[198:201], v159 offset:3072
	ds_read_b128 v[202:205], v159 offset:4096
	ds_read_b128 v[206:209], v159 offset:5120
	ds_read_b128 v[210:213], v159 offset:6144
	ds_read_b128 v[214:217], v159 offset:7168
	global_load_lds_dwordx4 v140, s[36:37]
	s_add_i32 m0, s51, 0xe000
	s_nop 0
	global_load_lds_dwordx4 v138, s[36:37]
	s_waitcnt vmcnt(8) lgkmcnt(0)
	s_barrier
	s_setprio 1
	v_mfma_f32_16x16x32_bf16 v[122:125], v[146:149], v[186:189], v[122:125]
	v_mfma_f32_16x16x32_bf16 v[126:129], v[162:165], v[186:189], v[126:129]
	v_mfma_f32_16x16x32_bf16 v[110:113], v[146:149], v[194:197], v[110:113]
	v_mfma_f32_16x16x32_bf16 v[106:109], v[162:165], v[194:197], v[106:109]
	v_mfma_f32_16x16x32_bf16 v[94:97], v[146:149], v[202:205], v[94:97]
	v_mfma_f32_16x16x32_bf16 v[90:93], v[162:165], v[202:205], v[90:93]
	v_mfma_f32_16x16x32_bf16 v[78:81], v[146:149], v[210:213], v[78:81]
	v_mfma_f32_16x16x32_bf16 v[74:77], v[162:165], v[210:213], v[74:77]
	v_mfma_f32_16x16x32_bf16 v[122:125], v[150:153], v[190:193], v[122:125]
	v_mfma_f32_16x16x32_bf16 v[126:129], v[166:169], v[190:193], v[126:129]
	v_mfma_f32_16x16x32_bf16 v[110:113], v[150:153], v[198:201], v[110:113]
	v_mfma_f32_16x16x32_bf16 v[106:109], v[166:169], v[198:201], v[106:109]
	v_mfma_f32_16x16x32_bf16 v[94:97], v[150:153], v[206:209], v[94:97]
	v_mfma_f32_16x16x32_bf16 v[90:93], v[166:169], v[206:209], v[90:93]
	v_mfma_f32_16x16x32_bf16 v[78:81], v[150:153], v[214:217], v[78:81]
	v_mfma_f32_16x16x32_bf16 v[74:77], v[166:169], v[214:217], v[74:77]
	s_setprio 0
	s_setprio 1
	v_mfma_f32_16x16x32_bf16 v[118:121], v[170:173], v[186:189], v[118:121]
	v_mfma_f32_16x16x32_bf16 v[114:117], v[178:181], v[186:189], v[114:117]
	v_mfma_f32_16x16x32_bf16 v[102:105], v[170:173], v[194:197], v[102:105]
	v_mfma_f32_16x16x32_bf16 v[98:101], v[178:181], v[194:197], v[98:101]
	v_mfma_f32_16x16x32_bf16 v[86:89], v[170:173], v[202:205], v[86:89]
	v_mfma_f32_16x16x32_bf16 v[82:85], v[178:181], v[202:205], v[82:85]
	v_mfma_f32_16x16x32_bf16 v[70:73], v[170:173], v[210:213], v[70:73]
	v_mfma_f32_16x16x32_bf16 v[66:69], v[178:181], v[210:213], v[66:69]
	v_mfma_f32_16x16x32_bf16 v[118:121], v[174:177], v[190:193], v[118:121]
	v_mfma_f32_16x16x32_bf16 v[114:117], v[182:185], v[190:193], v[114:117]
	v_mfma_f32_16x16x32_bf16 v[102:105], v[174:177], v[198:201], v[102:105]
	v_mfma_f32_16x16x32_bf16 v[98:101], v[182:185], v[198:201], v[98:101]
	v_mfma_f32_16x16x32_bf16 v[86:89], v[174:177], v[206:209], v[86:89]
	v_mfma_f32_16x16x32_bf16 v[82:85], v[182:185], v[206:209], v[82:85]
	v_mfma_f32_16x16x32_bf16 v[70:73], v[174:177], v[214:217], v[70:73]
	v_mfma_f32_16x16x32_bf16 v[66:69], v[182:185], v[214:217], v[66:69]
	s_setprio 0
	s_barrier
	s_mov_b32 m0, s35
	s_add_u32 s98, s38, 0x80
	s_addc_u32 s99, s39, 0
	s_add_u32 s72, s38, 0x80000
	ds_read_b128 v[186:189], v159 offset:16384
	ds_read_b128 v[190:193], v159 offset:17408
	ds_read_b128 v[194:197], v159 offset:18432
	ds_read_b128 v[198:201], v159 offset:19456
	ds_read_b128 v[202:205], v159 offset:20480
	ds_read_b128 v[206:209], v159 offset:21504
	ds_read_b128 v[210:213], v159 offset:22528
	ds_read_b128 v[214:217], v159 offset:23552
	global_load_lds_dwordx4 v132, s[38:39]
	s_mov_b32 m0, s48
	s_addc_u32 s73, s39, 0
	global_load_lds_dwordx4 v136, s[38:39]
	s_mov_b32 m0, s49
	s_nop 0
	global_load_lds_dwordx4 v132, s[72:73]
	s_mov_b32 m0, s50
	s_nop 0
	global_load_lds_dwordx4 v136, s[72:73]
	s_add_u32 s100, s40, 0x80
	s_addc_u32 s101, s41, 0
	s_mov_b32 m0, s51
	s_nop 0
	global_load_lds_dwordx4 v130, s[40:41]
	s_mov_b32 m0, s52
	s_nop 0
	global_load_lds_dwordx4 v134, s[40:41]
	s_waitcnt vmcnt(8) lgkmcnt(0)
	s_barrier
	s_setprio 1
	v_mfma_f32_16x16x32_bf16 v[62:65], v[146:149], v[186:189], v[62:65]
	v_mfma_f32_16x16x32_bf16 v[58:61], v[162:165], v[186:189], v[58:61]
	v_mfma_f32_16x16x32_bf16 v[46:49], v[146:149], v[194:197], v[46:49]
	v_mfma_f32_16x16x32_bf16 v[42:45], v[162:165], v[194:197], v[42:45]
	v_mfma_f32_16x16x32_bf16 v[30:33], v[146:149], v[202:205], v[30:33]
	v_mfma_f32_16x16x32_bf16 v[26:29], v[162:165], v[202:205], v[26:29]
	v_mfma_f32_16x16x32_bf16 v[14:17], v[146:149], v[210:213], v[14:17]
	v_mfma_f32_16x16x32_bf16 v[10:13], v[162:165], v[210:213], v[10:13]
	v_mfma_f32_16x16x32_bf16 v[62:65], v[150:153], v[190:193], v[62:65]
	v_mfma_f32_16x16x32_bf16 v[58:61], v[166:169], v[190:193], v[58:61]
	v_mfma_f32_16x16x32_bf16 v[46:49], v[150:153], v[198:201], v[46:49]
	v_mfma_f32_16x16x32_bf16 v[42:45], v[166:169], v[198:201], v[42:45]
	v_mfma_f32_16x16x32_bf16 v[30:33], v[150:153], v[206:209], v[30:33]
	v_mfma_f32_16x16x32_bf16 v[26:29], v[166:169], v[206:209], v[26:29]
	v_mfma_f32_16x16x32_bf16 v[14:17], v[150:153], v[214:217], v[14:17]
	v_mfma_f32_16x16x32_bf16 v[10:13], v[166:169], v[214:217], v[10:13]
	s_setprio 0
	s_setprio 1
	v_mfma_f32_16x16x32_bf16 v[54:57], v[170:173], v[186:189], v[54:57]
	v_mfma_f32_16x16x32_bf16 v[50:53], v[178:181], v[186:189], v[50:53]
	v_mfma_f32_16x16x32_bf16 v[38:41], v[170:173], v[194:197], v[38:41]
	v_mfma_f32_16x16x32_bf16 v[34:37], v[178:181], v[194:197], v[34:37]
	v_mfma_f32_16x16x32_bf16 v[22:25], v[170:173], v[202:205], v[22:25]
	v_mfma_f32_16x16x32_bf16 v[18:21], v[178:181], v[202:205], v[18:21]
	v_mfma_f32_16x16x32_bf16 v[6:9], v[170:173], v[210:213], v[6:9]
	v_mfma_f32_16x16x32_bf16 v[2:5], v[178:181], v[210:213], v[2:5]
	v_mfma_f32_16x16x32_bf16 v[54:57], v[174:177], v[190:193], v[54:57]
	v_mfma_f32_16x16x32_bf16 v[50:53], v[182:185], v[190:193], v[50:53]
	v_mfma_f32_16x16x32_bf16 v[38:41], v[174:177], v[198:201], v[38:41]
	v_mfma_f32_16x16x32_bf16 v[34:37], v[182:185], v[198:201], v[34:37]
	v_mfma_f32_16x16x32_bf16 v[22:25], v[174:177], v[206:209], v[22:25]
	v_mfma_f32_16x16x32_bf16 v[18:21], v[182:185], v[206:209], v[18:21]
	v_mfma_f32_16x16x32_bf16 v[6:9], v[174:177], v[214:217], v[6:9]
	v_mfma_f32_16x16x32_bf16 v[2:5], v[182:185], v[214:217], v[2:5]
	s_setprio 0
	s_barrier
; #define PG8_STAGE(bufoff, gbase, voff) do { _Pragma("unroll") for (int _i = 0; _i < 2; ++_i) \
;         __builtin_amdgcn_global_load_lds((const unsigned*)((const char*)(gbase) + (voff)[_i]), (PG8_LAS unsigned*)(lds + (bufoff) + ldsw + _i * 8192), 16, 0, 0); } while (0)
; #define PG8_LDA(dst, b, h) do { if constexpr (DT != 1) { _Pragma("unroll") for (int m = 0; m < 4; ++m) _Pragma("unroll") for (int k = 0; k < 2; ++k) dst[m][k] = *(const PG8_LAS bf16x8*)(lds + PG8_SA(b, h) + aoff + m * 2048 + k * 1024); } \
;         else { _Pragma("unroll") for (int m = 0; m < 4; ++m) dst##8[m] = ld32(lds + PG8_SA(b, h) + aoff + m * 2048); } } while (0)
; #define PG8_WAIT_V(n) asm volatile("s_waitcnt vmcnt(" #n ")" ::: "memory")
; #define PG8_WAIT_L(n) asm volatile("s_waitcnt lgkmcnt(" #n ")" ::: "memory")
; #define PG8_BAR __builtin_amdgcn_s_barrier()
; #define PG8_SCHED __builtin_amdgcn_sched_barrier(0)
;     ...
;         for (int t = 0; t < nt; t += 2) {
;             const bool last = (t == nt - 2);
;             const char* a1 = cA + (size_t)(t + 1) * kstep;
;             const char* a2 = last ? nA : cA + (size_t)(t + 2) * kstep; const char* b2 = last ? nB : cB + (size_t)(t + 2) * kstep;
;             const char* a3 = a2 + kstep; const char* b3 = b2 + kstep;
;             if (last && has_next) S.a_ready(nxt);
;             if constexpr (SP2) {
;             PG8_LDB(B0, 0, 0); PG8_LDB(B1, 0, 1); PG8_SCHED; PG8_LDA(At, 0, 0); PG8_STAGE(PG8_SA(1, 1), a1 + hstepA, voffA);
;             PG8_WAIT_V(8); PG8_WAIT_L(0); PG8_BAR; PG8_MMA(0, 0, At, B0); PG8_MMA(0, 1, At, B1); PG8_BAR; PG8_SCHED;
;             PG8_LDA(At, 0, 1); PG8_STAGE(PG8_SB(0, 0), b2, voffB); PG8_STAGE(PG8_SB(0, 1), b2 + hstepB, voffB); PG8_STAGE(PG8_SA(0, 0), a2, voffA);
;             PG8_WAIT_V(8); PG8_WAIT_L(0); PG8_BAR; PG8_MMA(1, 0, At, B0); PG8_MMA(1, 1, At, B1); PG8_BAR; PG8_SCHED;
;             PG8_LDB(B0, 1, 0); PG8_LDB(B1, 1, 1); PG8_SCHED; PG8_LDA(At, 1, 0); PG8_STAGE(PG8_SA(0, 1), a2 + hstepA, voffA);
;             PG8_WAIT_V(8); PG8_WAIT_L(0); PG8_BAR; PG8_MMA(0, 0, At, B0); PG8_MMA(0, 1, At, B1); PG8_BAR; PG8_SCHED;
;             PG8_LDA(At, 1, 1); PG8_STAGE(PG8_SB(1, 0), b3, voffB); PG8_STAGE(PG8_SB(1, 1), b3 + hstepB, voffB); PG8_STAGE(PG8_SA(1, 0), a3, voffA);
;             PG8_WAIT_V(8); PG8_WAIT_L(0); PG8_BAR; PG8_MMA(1, 0, At, B0); PG8_MMA(1, 1, At, B1); PG8_BAR; PG8_SCHED;
	ds_read_b128 v[146:149], v160
	ds_read_b128 v[150:153], v160 offset:1024
	ds_read_b128 v[162:165], v160 offset:2048
	ds_read_b128 v[166:169], v160 offset:3072
	ds_read_b128 v[170:173], v161
	ds_read_b128 v[174:177], v161 offset:1024
	ds_read_b128 v[178:181], v161 offset:2048
	ds_read_b128 v[182:185], v161 offset:3072
	s_add_u32 s40, s40, 0x80000
	s_addc_u32 s41, s41, 0
	s_mov_b32 m0, s53
	ds_read_b128 v[186:189], v159 offset:32768
	ds_read_b128 v[190:193], v159 offset:33792
	ds_read_b128 v[194:197], v159 offset:34816
	ds_read_b128 v[198:201], v159 offset:35840
	ds_read_b128 v[202:205], v159 offset:36864
	ds_read_b128 v[206:209], v159 offset:37888
	ds_read_b128 v[210:213], v159 offset:38912
	ds_read_b128 v[214:217], v159 offset:39936
	global_load_lds_dwordx4 v130, s[40:41]
	s_mov_b32 m0, s54
	s_nop 0
	global_load_lds_dwordx4 v134, s[40:41]
	s_waitcnt vmcnt(8) lgkmcnt(0)
	s_barrier
	s_setprio 1
	v_mfma_f32_16x16x32_bf16 v[122:125], v[146:149], v[186:189], v[122:125]
	v_mfma_f32_16x16x32_bf16 v[126:129], v[162:165], v[186:189], v[126:129]
	v_mfma_f32_16x16x32_bf16 v[110:113], v[146:149], v[194:197], v[110:113]
	v_mfma_f32_16x16x32_bf16 v[106:109], v[162:165], v[194:197], v[106:109]
	v_mfma_f32_16x16x32_bf16 v[94:97], v[146:149], v[202:205], v[94:97]
	v_mfma_f32_16x16x32_bf16 v[90:93], v[162:165], v[202:205], v[90:93]
	v_mfma_f32_16x16x32_bf16 v[78:81], v[146:149], v[210:213], v[78:81]
	v_mfma_f32_16x16x32_bf16 v[74:77], v[162:165], v[210:213], v[74:77]
	v_mfma_f32_16x16x32_bf16 v[122:125], v[150:153], v[190:193], v[122:125]
	v_mfma_f32_16x16x32_bf16 v[126:129], v[166:169], v[190:193], v[126:129]
	v_mfma_f32_16x16x32_bf16 v[110:113], v[150:153], v[198:201], v[110:113]
	v_mfma_f32_16x16x32_bf16 v[106:109], v[166:169], v[198:201], v[106:109]
	v_mfma_f32_16x16x32_bf16 v[94:97], v[150:153], v[206:209], v[94:97]
	v_mfma_f32_16x16x32_bf16 v[90:93], v[166:169], v[206:209], v[90:93]
	v_mfma_f32_16x16x32_bf16 v[78:81], v[150:153], v[214:217], v[78:81]
	v_mfma_f32_16x16x32_bf16 v[74:77], v[166:169], v[214:217], v[74:77]
	s_setprio 0
	s_setprio 1
	v_mfma_f32_16x16x32_bf16 v[118:121], v[170:173], v[186:189], v[118:121]
	v_mfma_f32_16x16x32_bf16 v[114:117], v[178:181], v[186:189], v[114:117]
	v_mfma_f32_16x16x32_bf16 v[102:105], v[170:173], v[194:197], v[102:105]
	v_mfma_f32_16x16x32_bf16 v[98:101], v[178:181], v[194:197], v[98:101]
	v_mfma_f32_16x16x32_bf16 v[86:89], v[170:173], v[202:205], v[86:89]
	v_mfma_f32_16x16x32_bf16 v[82:85], v[178:181], v[202:205], v[82:85]
	v_mfma_f32_16x16x32_bf16 v[70:73], v[170:173], v[210:213], v[70:73]
	v_mfma_f32_16x16x32_bf16 v[66:69], v[178:181], v[210:213], v[66:69]
	v_mfma_f32_16x16x32_bf16 v[118:121], v[174:177], v[190:193], v[118:121]
	v_mfma_f32_16x16x32_bf16 v[114:117], v[182:185], v[190:193], v[114:117]
	v_mfma_f32_16x16x32_bf16 v[102:105], v[174:177], v[198:201], v[102:105]
	v_mfma_f32_16x16x32_bf16 v[98:101], v[182:185], v[198:201], v[98:101]
	v_mfma_f32_16x16x32_bf16 v[86:89], v[174:177], v[206:209], v[86:89]
	v_mfma_f32_16x16x32_bf16 v[82:85], v[182:185], v[206:209], v[82:85]
	v_mfma_f32_16x16x32_bf16 v[70:73], v[174:177], v[214:217], v[70:73]
	v_mfma_f32_16x16x32_bf16 v[66:69], v[182:185], v[214:217], v[66:69]
	s_setprio 0
	s_barrier
	s_mov_b32 m0, s57
	s_add_u32 s38, s38, 0x80080
	ds_read_b128 v[186:189], v159 offset:49152
	ds_read_b128 v[190:193], v159 offset:50176
	ds_read_b128 v[194:197], v159 offset:51200
	ds_read_b128 v[198:201], v159 offset:52224
	ds_read_b128 v[202:205], v159 offset:53248
	ds_read_b128 v[206:209], v159 offset:54272
	ds_read_b128 v[210:213], v159 offset:55296
	ds_read_b128 v[214:217], v159 offset:56320
	global_load_lds_dwordx4 v132, s[98:99]
	s_mov_b32 m0, s58
	s_addc_u32 s39, s39, 0
	global_load_lds_dwordx4 v136, s[98:99]
	s_mov_b32 m0, s61
	s_nop 0
	global_load_lds_dwordx4 v132, s[38:39]
	s_mov_b32 m0, s62
	s_nop 0
	global_load_lds_dwordx4 v136, s[38:39]
	s_mov_b32 m0, s59
	s_nop 0
	global_load_lds_dwordx4 v130, s[100:101]
	s_mov_b32 m0, s60
	s_nop 0
	global_load_lds_dwordx4 v134, s[100:101]
	s_waitcnt vmcnt(8) lgkmcnt(0)
	s_barrier
	s_setprio 1
	v_mfma_f32_16x16x32_bf16 v[62:65], v[146:149], v[186:189], v[62:65]
	v_mfma_f32_16x16x32_bf16 v[58:61], v[162:165], v[186:189], v[58:61]
	v_mfma_f32_16x16x32_bf16 v[46:49], v[146:149], v[194:197], v[46:49]
	v_mfma_f32_16x16x32_bf16 v[42:45], v[162:165], v[194:197], v[42:45]
	v_mfma_f32_16x16x32_bf16 v[30:33], v[146:149], v[202:205], v[30:33]
	v_mfma_f32_16x16x32_bf16 v[26:29], v[162:165], v[202:205], v[26:29]
	v_mfma_f32_16x16x32_bf16 v[14:17], v[146:149], v[210:213], v[14:17]
	v_mfma_f32_16x16x32_bf16 v[10:13], v[162:165], v[210:213], v[10:13]
	v_mfma_f32_16x16x32_bf16 v[62:65], v[150:153], v[190:193], v[62:65]
	v_mfma_f32_16x16x32_bf16 v[58:61], v[166:169], v[190:193], v[58:61]
	v_mfma_f32_16x16x32_bf16 v[46:49], v[150:153], v[198:201], v[46:49]
	v_mfma_f32_16x16x32_bf16 v[42:45], v[166:169], v[198:201], v[42:45]
	v_mfma_f32_16x16x32_bf16 v[30:33], v[150:153], v[206:209], v[30:33]
	v_mfma_f32_16x16x32_bf16 v[26:29], v[166:169], v[206:209], v[26:29]
	v_mfma_f32_16x16x32_bf16 v[14:17], v[150:153], v[214:217], v[14:17]
	v_mfma_f32_16x16x32_bf16 v[10:13], v[166:169], v[214:217], v[10:13]
	s_setprio 0
	s_setprio 1
	v_mfma_f32_16x16x32_bf16 v[54:57], v[170:173], v[186:189], v[54:57]
	v_mfma_f32_16x16x32_bf16 v[50:53], v[178:181], v[186:189], v[50:53]
	v_mfma_f32_16x16x32_bf16 v[38:41], v[170:173], v[194:197], v[38:41]
	v_mfma_f32_16x16x32_bf16 v[34:37], v[178:181], v[194:197], v[34:37]
	v_mfma_f32_16x16x32_bf16 v[22:25], v[170:173], v[202:205], v[22:25]
	v_mfma_f32_16x16x32_bf16 v[18:21], v[178:181], v[202:205], v[18:21]
	v_mfma_f32_16x16x32_bf16 v[6:9], v[170:173], v[210:213], v[6:9]
	v_mfma_f32_16x16x32_bf16 v[2:5], v[178:181], v[210:213], v[2:5]
	v_mfma_f32_16x16x32_bf16 v[54:57], v[174:177], v[190:193], v[54:57]
	v_mfma_f32_16x16x32_bf16 v[50:53], v[182:185], v[190:193], v[50:53]
	v_mfma_f32_16x16x32_bf16 v[38:41], v[174:177], v[198:201], v[38:41]
	v_mfma_f32_16x16x32_bf16 v[34:37], v[182:185], v[198:201], v[34:37]
	v_mfma_f32_16x16x32_bf16 v[22:25], v[174:177], v[206:209], v[22:25]
	v_mfma_f32_16x16x32_bf16 v[18:21], v[182:185], v[206:209], v[18:21]
	v_mfma_f32_16x16x32_bf16 v[6:9], v[174:177], v[214:217], v[6:9]
	v_mfma_f32_16x16x32_bf16 v[2:5], v[182:185], v[214:217], v[2:5]
	s_setprio 0
	s_barrier
	s_add_u32 s69, s69, 0x100
	s_addc_u32 s70, s70, 0
	s_add_u32 s36, s36, 0x100
	s_addc_u32 s37, s37, 0
	s_cmp_ge_i32 s71, s56
	s_mov_b32 s38, s71
	s_cbranch_scc0 .LBB0_4646

; #define PG8_STAGE(bufoff, gbase, voff) do { _Pragma("unroll") for (int _i = 0; _i < 2; ++_i) \
;         __builtin_amdgcn_global_load_lds((const unsigned*)((const char*)(gbase) + (voff)[_i]), (PG8_LAS unsigned*)(lds + (bufoff) + ldsw + _i * 8192), 16, 0, 0); } while (0)
; #define PG8_LDA(dst, b, h) do { if constexpr (DT != 1) { _Pragma("unroll") for (int m = 0; m < 4; ++m) _Pragma("unroll") for (int k = 0; k < 2; ++k) dst[m][k] = *(const PG8_LAS bf16x8*)(lds + PG8_SA(b, h) + aoff + m * 2048 + k * 1024); } \
;         else { _Pragma("unroll") for (int m = 0; m < 4; ++m) dst##8[m] = ld32(lds + PG8_SA(b, h) + aoff + m * 2048); } } while (0)
; #define PG8_LDB(dst, b, h) do { if constexpr (DT != 1) { _Pragma("unroll") for (int n = 0; n < 2; ++n) _Pragma("unroll") for (int k = 0; k < 2; ++k) dst[n][k] = *(const PG8_LAS bf16x8*)(lds + PG8_SB(b, h) + boff + n * 2048 + k * 1024); } \
;         else { _Pragma("unroll") for (int n = 0; n < 2; ++n) dst##8[n] = ld32(lds + PG8_SB(b, h) + boff + n * 2048); } } while (0)
; #define PG8_WAIT_V(n) asm volatile("s_waitcnt vmcnt(" #n ")" ::: "memory")
; #define PG8_WAIT_L(n) asm volatile("s_waitcnt lgkmcnt(" #n ")" ::: "memory")
; #define PG8_BAR __builtin_amdgcn_s_barrier()
; #define PG8_SCHED __builtin_amdgcn_sched_barrier(0)
;     ...
;             PG8_LDB(B0, 0, 0); PG8_LDB(B1, 0, 1); PG8_SCHED; PG8_LDA(At, 0, 0); PG8_STAGE(PG8_SA(1, 1), a1 + hstepA, voffA);
;             PG8_WAIT_V(8); PG8_WAIT_L(0); PG8_BAR; PG8_MMA(0, 0, At, B0); PG8_MMA(0, 1, At, B1); PG8_BAR; PG8_SCHED;
;             PG8_LDA(At, 0, 1); PG8_STAGE(PG8_SB(0, 0), b2, voffB); PG8_STAGE(PG8_SB(0, 1), b2 + hstepB, voffB); PG8_STAGE(PG8_SA(0, 0), a2, voffA);
;             PG8_WAIT_V(8); PG8_WAIT_L(0); PG8_BAR; PG8_MMA(1, 0, At, B0); PG8_MMA(1, 1, At, B1); PG8_BAR; PG8_SCHED;
;             PG8_LDB(B0, 1, 0); PG8_LDB(B1, 1, 1); PG8_SCHED; PG8_LDA(At, 1, 0); PG8_STAGE(PG8_SA(0, 1), a2 + hstepA, voffA);
;             PG8_WAIT_V(8); PG8_WAIT_L(0); PG8_BAR; PG8_MMA(0, 0, At, B0); PG8_MMA(0, 1, At, B1); PG8_BAR; PG8_SCHED;
;             PG8_LDA(At, 1, 1); PG8_STAGE(PG8_SB(1, 0), b3, voffB); PG8_STAGE(PG8_SB(1, 1), b3 + hstepB, voffB); PG8_STAGE(PG8_SA(1, 0), a3, voffA);
;             PG8_WAIT_V(8); PG8_WAIT_L(0); PG8_BAR; PG8_MMA(1, 0, At, B0); PG8_MMA(1, 1, At, B1); PG8_BAR; PG8_SCHED;
.LBB0_4855:
	ds_read_b128 v[16:19], v186
	ds_read_b128 v[20:23], v186 offset:16
	ds_read_b128 v[24:27], v186 offset:2048
	ds_read_b128 v[28:31], v186 offset:2064
	ds_read_b128 v[0:3], v187
	ds_read_b128 v[4:7], v187 offset:16
	ds_read_b128 v[8:11], v187 offset:2048
	ds_read_b128 v[12:15], v187 offset:2064
	s_add_i32 s61, s26, 2
	s_add_u32 s24, s22, 0x100
	s_addc_u32 s25, s23, 0
	s_cmp_eq_u32 s52, s26
	s_cselect_b32 s26, s20, s59
	s_cselect_b32 s29, s3, s25
	s_cselect_b32 s28, s2, s24
	s_cselect_b32 s27, s21, s60
	v_lshl_add_u64 v[216:217], s[22:23], 0, v[170:171]
	s_add_i32 m0, s40, 0xc000
	ds_read_b128 v[176:179], v188
	ds_read_b128 v[180:183], v188 offset:16
	ds_read_b128 v[192:195], v188 offset:2048
	ds_read_b128 v[196:199], v188 offset:2064
	ds_read_b128 v[200:203], v188 offset:4096
	ds_read_b128 v[204:207], v188 offset:4112
	ds_read_b128 v[208:211], v188 offset:6144
	ds_read_b128 v[212:215], v188 offset:6160
	global_load_lds_dwordx4 v[216:217], off
	v_lshl_add_u64 v[216:217], s[22:23], 0, v[168:169]
	s_add_i32 m0, s40, 0xe000
	s_nop 0
	global_load_lds_dwordx4 v[216:217], off
	s_waitcnt vmcnt(8) lgkmcnt(0)
	s_barrier
	s_setprio 1
	v_mfma_scale_f32_16x16x128_f8f6f4 v[156:159], v[16:23], v[176:183], v[156:159], v189, v189 op_sel_hi:[0,0,0]
	v_mfma_scale_f32_16x16x128_f8f6f4 v[152:155], v[24:31], v[176:183], v[152:155], v189, v189 op_sel_hi:[0,0,0]
	v_mfma_scale_f32_16x16x128_f8f6f4 v[148:151], v[16:23], v[192:199], v[148:151], v189, v189 op_sel_hi:[0,0,0]
	v_mfma_scale_f32_16x16x128_f8f6f4 v[144:147], v[24:31], v[192:199], v[144:147], v189, v189 op_sel_hi:[0,0,0]
	v_mfma_scale_f32_16x16x128_f8f6f4 v[128:131], v[16:23], v[200:207], v[128:131], v189, v189 op_sel_hi:[0,0,0]
	v_mfma_scale_f32_16x16x128_f8f6f4 v[120:123], v[24:31], v[200:207], v[120:123], v189, v189 op_sel_hi:[0,0,0]
	v_mfma_scale_f32_16x16x128_f8f6f4 v[108:111], v[16:23], v[208:215], v[108:111], v189, v189 op_sel_hi:[0,0,0]
	v_mfma_scale_f32_16x16x128_f8f6f4 v[104:107], v[24:31], v[208:215], v[104:107], v189, v189 op_sel_hi:[0,0,0]
	s_setprio 0
	s_setprio 1
	v_mfma_scale_f32_16x16x128_f8f6f4 v[140:143], v[0:7], v[176:183], v[140:143], v189, v189 op_sel_hi:[0,0,0]
	v_mfma_scale_f32_16x16x128_f8f6f4 v[136:139], v[8:15], v[176:183], v[136:139], v189, v189 op_sel_hi:[0,0,0]
	v_mfma_scale_f32_16x16x128_f8f6f4 v[132:135], v[0:7], v[192:199], v[132:135], v189, v189 op_sel_hi:[0,0,0]
	v_mfma_scale_f32_16x16x128_f8f6f4 v[124:127], v[8:15], v[192:199], v[124:127], v189, v189 op_sel_hi:[0,0,0]
	v_mfma_scale_f32_16x16x128_f8f6f4 v[116:119], v[0:7], v[200:207], v[116:119], v189, v189 op_sel_hi:[0,0,0]
	v_mfma_scale_f32_16x16x128_f8f6f4 v[112:115], v[8:15], v[200:207], v[112:115], v189, v189 op_sel_hi:[0,0,0]
	v_mfma_scale_f32_16x16x128_f8f6f4 v[100:103], v[0:7], v[208:215], v[100:103], v189, v189 op_sel_hi:[0,0,0]
	v_mfma_scale_f32_16x16x128_f8f6f4 v[96:99], v[8:15], v[208:215], v[96:99], v189, v189 op_sel_hi:[0,0,0]
	s_setprio 0
	s_barrier
	s_mov_b32 m0, s36
	s_add_u32 s98, s26, 0x80
	s_addc_u32 s99, s27, 0
	s_add_u32 s22, s26, 0xb0000
	ds_read_b128 v[192:195], v188 offset:16384
	ds_read_b128 v[196:199], v188 offset:16400
	ds_read_b128 v[200:203], v188 offset:18432
	ds_read_b128 v[204:207], v188 offset:18448
	ds_read_b128 v[208:211], v188 offset:20480
	ds_read_b128 v[212:215], v188 offset:20496
	ds_read_b128 v[216:219], v188 offset:22528
	ds_read_b128 v[220:223], v188 offset:22544
	global_load_lds_dwordx4 v162, s[26:27]
	s_mov_b32 m0, s37
	s_addc_u32 s23, s27, 0
	global_load_lds_dwordx4 v166, s[26:27]
	s_mov_b32 m0, s38
	s_nop 0
	global_load_lds_dwordx4 v162, s[22:23]
	s_mov_b32 m0, s39
	s_nop 0
	global_load_lds_dwordx4 v166, s[22:23]
	s_add_u32 s100, s28, 0x80
	s_addc_u32 s101, s29, 0
	s_mov_b32 m0, s40
	s_nop 0
	global_load_lds_dwordx4 v160, s[28:29]
	s_mov_b32 m0, s41
	s_nop 0
	global_load_lds_dwordx4 v164, s[28:29]
	s_waitcnt vmcnt(8) lgkmcnt(0)
	s_barrier
	s_setprio 1
	v_mfma_scale_f32_16x16x128_f8f6f4 v[92:95], v[16:23], v[192:199], v[92:95], v189, v189 op_sel_hi:[0,0,0]
	v_mfma_scale_f32_16x16x128_f8f6f4 v[88:91], v[24:31], v[192:199], v[88:91], v189, v189 op_sel_hi:[0,0,0]
	v_mfma_scale_f32_16x16x128_f8f6f4 v[76:79], v[16:23], v[200:207], v[76:79], v189, v189 op_sel_hi:[0,0,0]
	v_mfma_scale_f32_16x16x128_f8f6f4 v[72:75], v[24:31], v[200:207], v[72:75], v189, v189 op_sel_hi:[0,0,0]
	v_mfma_scale_f32_16x16x128_f8f6f4 v[224:227], v[16:23], v[208:215], v[60:63], v189, v189 op_sel_hi:[0,0,0]
	v_mfma_scale_f32_16x16x128_f8f6f4 v[228:231], v[24:31], v[208:215], v[56:59], v189, v189 op_sel_hi:[0,0,0]
	v_mfma_scale_f32_16x16x128_f8f6f4 v[232:235], v[16:23], v[216:223], v[44:47], v189, v189 op_sel_hi:[0,0,0]
	v_mfma_scale_f32_16x16x128_f8f6f4 v[236:239], v[24:31], v[216:223], v[40:43], v189, v189 op_sel_hi:[0,0,0]
	s_setprio 0
	s_setprio 1
	v_mfma_scale_f32_16x16x128_f8f6f4 v[84:87], v[0:7], v[192:199], v[84:87], v189, v189 op_sel_hi:[0,0,0]
	v_mfma_scale_f32_16x16x128_f8f6f4 v[80:83], v[8:15], v[192:199], v[80:83], v189, v189 op_sel_hi:[0,0,0]
	v_mfma_scale_f32_16x16x128_f8f6f4 v[68:71], v[0:7], v[200:207], v[68:71], v189, v189 op_sel_hi:[0,0,0]
	v_mfma_scale_f32_16x16x128_f8f6f4 v[64:67], v[8:15], v[200:207], v[64:67], v189, v189 op_sel_hi:[0,0,0]
	v_mfma_scale_f32_16x16x128_f8f6f4 v[240:243], v[0:7], v[208:215], v[52:55], v189, v189 op_sel_hi:[0,0,0]
	v_mfma_scale_f32_16x16x128_f8f6f4 v[208:211], v[8:15], v[208:215], v[48:51], v189, v189 op_sel_hi:[0,0,0]
	v_mfma_scale_f32_16x16x128_f8f6f4 v[212:215], v[0:7], v[216:223], v[36:39], v189, v189 op_sel_hi:[0,0,0]
	v_mfma_scale_f32_16x16x128_f8f6f4 v[216:219], v[8:15], v[216:223], v[32:35], v189, v189 op_sel_hi:[0,0,0]
	s_setprio 0
	s_barrier
; #define PG8_STAGE(bufoff, gbase, voff) do { _Pragma("unroll") for (int _i = 0; _i < 2; ++_i) \
;         __builtin_amdgcn_global_load_lds((const unsigned*)((const char*)(gbase) + (voff)[_i]), (PG8_LAS unsigned*)(lds + (bufoff) + ldsw + _i * 8192), 16, 0, 0); } while (0)
; #define PG8_LDA(dst, b, h) do { if constexpr (DT != 1) { _Pragma("unroll") for (int m = 0; m < 4; ++m) _Pragma("unroll") for (int k = 0; k < 2; ++k) dst[m][k] = *(const PG8_LAS bf16x8*)(lds + PG8_SA(b, h) + aoff + m * 2048 + k * 1024); } \
;         else { _Pragma("unroll") for (int m = 0; m < 4; ++m) dst##8[m] = ld32(lds + PG8_SA(b, h) + aoff + m * 2048); } } while (0)
; #define PG8_LDB(dst, b, h) do { if constexpr (DT != 1) { _Pragma("unroll") for (int n = 0; n < 2; ++n) _Pragma("unroll") for (int k = 0; k < 2; ++k) dst[n][k] = *(const PG8_LAS bf16x8*)(lds + PG8_SB(b, h) + boff + n * 2048 + k * 1024); } \
;         else { _Pragma("unroll") for (int n = 0; n < 2; ++n) dst##8[n] = ld32(lds + PG8_SB(b, h) + boff + n * 2048); } } while (0)
; #define PG8_WAIT_V(n) asm volatile("s_waitcnt vmcnt(" #n ")" ::: "memory")
; #define PG8_WAIT_L(n) asm volatile("s_waitcnt lgkmcnt(" #n ")" ::: "memory")
; #define PG8_BAR __builtin_amdgcn_s_barrier()
; #define PG8_SCHED __builtin_amdgcn_sched_barrier(0)
;     ...
;             PG8_LDB(B0, 0, 0); PG8_LDB(B1, 0, 1); PG8_SCHED; PG8_LDA(At, 0, 0); PG8_STAGE(PG8_SA(1, 1), a1 + hstepA, voffA);
;             PG8_WAIT_V(8); PG8_WAIT_L(0); PG8_BAR; PG8_MMA(0, 0, At, B0); PG8_MMA(0, 1, At, B1); PG8_BAR; PG8_SCHED;
;             PG8_LDA(At, 0, 1); PG8_STAGE(PG8_SB(0, 0), b2, voffB); PG8_STAGE(PG8_SB(0, 1), b2 + hstepB, voffB); PG8_STAGE(PG8_SA(0, 0), a2, voffA);
;             PG8_WAIT_V(8); PG8_WAIT_L(0); PG8_BAR; PG8_MMA(1, 0, At, B0); PG8_MMA(1, 1, At, B1); PG8_BAR; PG8_SCHED;
;             PG8_LDB(B0, 1, 0); PG8_LDB(B1, 1, 1); PG8_SCHED; PG8_LDA(At, 1, 0); PG8_STAGE(PG8_SA(0, 1), a2 + hstepA, voffA);
;             PG8_WAIT_V(8); PG8_WAIT_L(0); PG8_BAR; PG8_MMA(0, 0, At, B0); PG8_MMA(0, 1, At, B1); PG8_BAR; PG8_SCHED;
;             PG8_LDA(At, 1, 1); PG8_STAGE(PG8_SB(1, 0), b3, voffB); PG8_STAGE(PG8_SB(1, 1), b3 + hstepB, voffB); PG8_STAGE(PG8_SA(1, 0), a3, voffA);
;             PG8_WAIT_V(8); PG8_WAIT_L(0); PG8_BAR; PG8_MMA(1, 0, At, B0); PG8_MMA(1, 1, At, B1); PG8_BAR; PG8_SCHED;
	ds_read_b128 v[0:3], v190
	ds_read_b128 v[4:7], v190 offset:16
	ds_read_b128 v[8:11], v190 offset:2048
	ds_read_b128 v[12:15], v190 offset:2064
	ds_read_b128 v[16:19], v191
	ds_read_b128 v[20:23], v191 offset:16
	ds_read_b128 v[24:27], v191 offset:2048
	ds_read_b128 v[28:31], v191 offset:2064
	s_add_u32 s22, s28, 0xb0000
	s_addc_u32 s23, s29, 0
	s_mov_b32 m0, s42
	ds_read_b128 v[32:35], v188 offset:32768
	ds_read_b128 v[36:39], v188 offset:32784
	ds_read_b128 v[40:43], v188 offset:34816
	ds_read_b128 v[44:47], v188 offset:34832
	ds_read_b128 v[48:51], v188 offset:36864
	ds_read_b128 v[52:55], v188 offset:36880
	ds_read_b128 v[56:59], v188 offset:38912
	ds_read_b128 v[60:63], v188 offset:38928
	global_load_lds_dwordx4 v160, s[22:23]
	s_mov_b32 m0, s43
	s_nop 0
	global_load_lds_dwordx4 v164, s[22:23]
	s_waitcnt vmcnt(8) lgkmcnt(0)
	s_barrier
	s_setprio 1
	v_mfma_scale_f32_16x16x128_f8f6f4 v[156:159], v[0:7], v[32:39], v[156:159], v189, v189 op_sel_hi:[0,0,0]
	v_mfma_scale_f32_16x16x128_f8f6f4 v[152:155], v[8:15], v[32:39], v[152:155], v189, v189 op_sel_hi:[0,0,0]
	v_mfma_scale_f32_16x16x128_f8f6f4 v[148:151], v[0:7], v[40:47], v[148:151], v189, v189 op_sel_hi:[0,0,0]
	v_mfma_scale_f32_16x16x128_f8f6f4 v[144:147], v[8:15], v[40:47], v[144:147], v189, v189 op_sel_hi:[0,0,0]
	v_mfma_scale_f32_16x16x128_f8f6f4 v[128:131], v[0:7], v[48:55], v[128:131], v189, v189 op_sel_hi:[0,0,0]
	v_mfma_scale_f32_16x16x128_f8f6f4 v[120:123], v[8:15], v[48:55], v[120:123], v189, v189 op_sel_hi:[0,0,0]
	v_mfma_scale_f32_16x16x128_f8f6f4 v[108:111], v[0:7], v[56:63], v[108:111], v189, v189 op_sel_hi:[0,0,0]
	v_mfma_scale_f32_16x16x128_f8f6f4 v[104:107], v[8:15], v[56:63], v[104:107], v189, v189 op_sel_hi:[0,0,0]
	s_setprio 0
	s_setprio 1
	v_mfma_scale_f32_16x16x128_f8f6f4 v[140:143], v[16:23], v[32:39], v[140:143], v189, v189 op_sel_hi:[0,0,0]
	v_mfma_scale_f32_16x16x128_f8f6f4 v[136:139], v[24:31], v[32:39], v[136:139], v189, v189 op_sel_hi:[0,0,0]
	v_mfma_scale_f32_16x16x128_f8f6f4 v[132:135], v[16:23], v[40:47], v[132:135], v189, v189 op_sel_hi:[0,0,0]
	v_mfma_scale_f32_16x16x128_f8f6f4 v[124:127], v[24:31], v[40:47], v[124:127], v189, v189 op_sel_hi:[0,0,0]
	v_mfma_scale_f32_16x16x128_f8f6f4 v[116:119], v[16:23], v[48:55], v[116:119], v189, v189 op_sel_hi:[0,0,0]
	v_mfma_scale_f32_16x16x128_f8f6f4 v[112:115], v[24:31], v[48:55], v[112:115], v189, v189 op_sel_hi:[0,0,0]
	v_mfma_scale_f32_16x16x128_f8f6f4 v[100:103], v[16:23], v[56:63], v[100:103], v189, v189 op_sel_hi:[0,0,0]
	v_mfma_scale_f32_16x16x128_f8f6f4 v[96:99], v[24:31], v[56:63], v[96:99], v189, v189 op_sel_hi:[0,0,0]
	s_setprio 0
	s_barrier
	s_mov_b32 m0, s46
	s_add_u32 s22, s26, 0xb0080
	ds_read_b128 v[32:35], v188 offset:49152
	ds_read_b128 v[36:39], v188 offset:49168
	ds_read_b128 v[48:51], v188 offset:51200
	ds_read_b128 v[52:55], v188 offset:51216
	ds_read_b128 v[192:195], v188 offset:53248
	ds_read_b128 v[196:199], v188 offset:53264
	ds_read_b128 v[200:203], v188 offset:55296
	ds_read_b128 v[204:207], v188 offset:55312
	global_load_lds_dwordx4 v162, s[98:99]
	s_mov_b32 m0, s47
	s_addc_u32 s23, s27, 0
	global_load_lds_dwordx4 v166, s[98:99]
	s_mov_b32 m0, s50
	s_nop 0
	global_load_lds_dwordx4 v162, s[22:23]
	s_mov_b32 m0, s51
	s_nop 0
	global_load_lds_dwordx4 v166, s[22:23]
	s_mov_b32 m0, s48
	s_nop 0
	global_load_lds_dwordx4 v160, s[100:101]
	s_mov_b32 m0, s49
	s_nop 0
	global_load_lds_dwordx4 v164, s[100:101]
	s_waitcnt vmcnt(8) lgkmcnt(0)
	s_barrier
	s_setprio 1
	v_mfma_scale_f32_16x16x128_f8f6f4 v[92:95], v[0:7], v[32:39], v[92:95], v189, v189 op_sel_hi:[0,0,0]
	v_mfma_scale_f32_16x16x128_f8f6f4 v[88:91], v[8:15], v[32:39], v[88:91], v189, v189 op_sel_hi:[0,0,0]
	v_mfma_scale_f32_16x16x128_f8f6f4 v[76:79], v[0:7], v[48:55], v[76:79], v189, v189 op_sel_hi:[0,0,0]
	v_mfma_scale_f32_16x16x128_f8f6f4 v[72:75], v[8:15], v[48:55], v[72:75], v189, v189 op_sel_hi:[0,0,0]
	v_mfma_scale_f32_16x16x128_f8f6f4 v[60:63], v[0:7], v[192:199], v[224:227], v189, v189 op_sel_hi:[0,0,0]
	v_mfma_scale_f32_16x16x128_f8f6f4 v[56:59], v[8:15], v[192:199], v[228:231], v189, v189 op_sel_hi:[0,0,0]
	v_mfma_scale_f32_16x16x128_f8f6f4 v[44:47], v[0:7], v[200:207], v[232:235], v189, v189 op_sel_hi:[0,0,0]
	v_mfma_scale_f32_16x16x128_f8f6f4 v[40:43], v[8:15], v[200:207], v[236:239], v189, v189 op_sel_hi:[0,0,0]
	s_setprio 0
	s_setprio 1
	v_mfma_scale_f32_16x16x128_f8f6f4 v[84:87], v[16:23], v[32:39], v[84:87], v189, v189 op_sel_hi:[0,0,0]
	v_mfma_scale_f32_16x16x128_f8f6f4 v[80:83], v[24:31], v[32:39], v[80:83], v189, v189 op_sel_hi:[0,0,0]
	v_mfma_scale_f32_16x16x128_f8f6f4 v[68:71], v[16:23], v[48:55], v[68:71], v189, v189 op_sel_hi:[0,0,0]
	v_mfma_scale_f32_16x16x128_f8f6f4 v[64:67], v[24:31], v[48:55], v[64:67], v189, v189 op_sel_hi:[0,0,0]
	v_mfma_scale_f32_16x16x128_f8f6f4 v[52:55], v[16:23], v[192:199], v[240:243], v189, v189 op_sel_hi:[0,0,0]
	v_mfma_scale_f32_16x16x128_f8f6f4 v[48:51], v[24:31], v[192:199], v[208:211], v189, v189 op_sel_hi:[0,0,0]
	v_mfma_scale_f32_16x16x128_f8f6f4 v[36:39], v[16:23], v[200:207], v[212:215], v189, v189 op_sel_hi:[0,0,0]
	v_mfma_scale_f32_16x16x128_f8f6f4 v[32:35], v[24:31], v[200:207], v[216:219], v189, v189 op_sel_hi:[0,0,0]
	s_setprio 0
	s_barrier
	s_add_u32 s59, s59, 0x100
	s_addc_u32 s60, s60, 0
	s_cmp_ge_i32 s61, s45
	s_mov_b64 s[22:23], s[24:25]
	s_mov_b32 s26, s61
	s_cbranch_scc0 .LBB0_4855
